# v23 + LDS-DMA issue rebalanced 4/4/4/4 (As[b][0] stage moved from SP2 to next SP1, vmcnt 8/6) in 6 GEMM loops
# speedup vs baseline: 1.0042x; 1.0029x over previous
; #define PG8_WAIT_V(n) asm volatile("s_waitcnt vmcnt(" #n ")" ::: "memory")
;     __host__ __device__ bool next(int i, Unit& u) const {
;         const long L = (long)i * G + c; if (L >= nwg) return false;
;         int wgid = (int)L; { const int q = nwg / NXCD, r = nwg % NXCD, xcd = wgid % NXCD, off = wgid / NXCD; wgid = (xcd < r ? xcd * (q + 1) : r * (q + 1) + (xcd - r) * q) + off; }
;         const int nig = WGM * nN, gid = wgid / nig, fm = gid * WGM, gsz = (nM - fm) < WGM ? (nM - fm) : WGM;
;         u.pm = fm + ((wgid % nig) % gsz); u.pn = (wgid % nig) / gsz; return true;
; template <class Epi, class Sched, bool ALIGN_EPI = false, bool SP2 = false>
; __device__ __forceinline__ void gemm_phase(PG8_LAS unsigned char* lds, const Gemm g, const Sched& S, const Epi& E) {
;     ...
;     for (int i = 0; i < 2; ++i) { int R, C; stage_rc(tid * 16 + i * 8192, R, C); const int Rb = Epi::PERM ? ((R & ~31) + perm32(R & 31)) : R;
;         voffA[i] = (unsigned)(R * g.lda + C) * 2u; voffB[i] = (unsigned)(Rb * g.ldb + C) * 2u; }
;     const size_t kstep = (size_t)(BK * 2);
;     const size_t hstepA = (size_t)HALF * g.lda * 2, hstepB = (size_t)HALF * g.ldb * 2;
;     const size_t tstepA = 2 * hstepA, tstepB = 2 * hstepB;
;     const unsigned ldsw = (unsigned)wid * 1024u;
;     const int aoff = lds_byte(wr * 64 + fr, fq * 8), boff = lds_byte(wc * 32 + fr, fq * 8);
;     ...
;     Unit cur, nxt; int ui = 0;
;     if (!S.next(0, cur)) return;
;     f32x4 acc[2][2][4][2];
; #pragma unroll
;     for (int a = 0; a < 2; ++a)
; #pragma unroll
;         for (int b = 0; b < 2; ++b)
; #pragma unroll
;             for (int m = 0; m < 4; ++m)
; #pragma unroll
;                 for (int n = 0; n < 2; ++n) acc[a][b][m][n] = (f32x4){0.f, 0.f, 0.f, 0.f};
;     bf16x8 At[4][2], B0[2][2], B1[2][2];
;     const char* cA = (const char*)g.A + (size_t)cur.pm * tstepA; const char* cB = (const char*)g.Bt + (size_t)cur.pn * tstepB;
;     S.a_ready(cur);
;     if constexpr (SP2) {
;         PG8_STAGE(PG8_SB(0, 0), cB, voffB); PG8_STAGE(PG8_SB(0, 1), cB + hstepB, voffB); PG8_STAGE(PG8_SA(0, 0), cA, voffA); PG8_STAGE(PG8_SA(0, 1), cA + hstepA, voffA);
;         if (wr == 1) PG8_BAR;
;         PG8_WAIT_V(2); PG8_BAR;
;         PG8_STAGE(PG8_SB(1, 0), cB + kstep, voffB); PG8_STAGE(PG8_SA(1, 0), cA + kstep, voffA); PG8_STAGE(PG8_SB(1, 1), cB + hstepB + kstep, voffB);
;         PG8_WAIT_V(6); PG8_BAR;
;     } else {
.LBB0_143:
	v_readlane_b32 s4, v253, 55
	s_lshr_b32 s1, s4, 2
	s_lshl_b32 s38, s1, 4
	s_lshl_b32 s36, s1, 9
	s_andn2_b64 vcc, exec, s[2:3]
	s_and_b32 s37, s4, 1
	v_readlane_b32 s5, v253, 56
	v_writelane_b32 v252, s1, 0
	s_cbranch_vccnz .LBB0_645
	v_readlane_b32 s0, v253, 32
	v_readlane_b32 s1, v253, 33
	s_mov_b64 s[4:5], s[0:1]
	v_readlane_b32 s0, v253, 38
	v_mov_b32_e32 v146, v0
	v_readlane_b32 s1, v253, 39
	s_add_u32 s28, s4, 0x800000
	v_readlane_b32 s3, v253, 35
	s_load_dword s1, s[0:1], 0x0
	s_mov_b32 s30, s88
	s_addc_u32 s29, s5, 0
	s_waitcnt vmcnt(0)
	v_mov_b32_e32 v12, v0
	v_readfirstlane_b32 s0, v146
	s_waitcnt lgkmcnt(0)
	s_cmpk_gt_i32 s30, 0x57f
	v_readfirstlane_b32 s3, v12
	v_readlane_b32 s2, v253, 34
	s_cbranch_scc1 .LBB0_160
	v_lshlrev_b32_e32 v2, 4, v12
	v_add_u32_e32 v4, 0x2000, v2
	v_ashrrev_i32_e32 v5, 31, v4
	v_lshrrev_b32_e32 v5, 22, v5
	v_add_u32_e32 v5, v4, v5
	v_ashrrev_i32_e32 v13, 10, v5
	v_mul_i32_i24_e32 v5, 0x400, v13
	v_sub_u32_e32 v4, v4, v5
	v_lshrrev_b32_e32 v5, 4, v4
	v_readlane_b32 s6, v253, 55
	v_bitop3_b32 v4, v5, v4, 32 bitop3:0x6c
	v_readlane_b32 s7, v253, 56
	s_mul_i32 s68, s6, 0x580000
	s_add_u32 s31, s4, 0xb000000
	v_ashrrev_i32_e32 v5, 31, v4
	s_addc_u32 s33, s5, 0
	s_lshl_b64 s[6:7], s[68:69], 1
	v_lshrrev_b32_e32 v5, 26, v5
	s_add_u32 s34, s28, s6
	v_add_u32_e32 v5, v4, v5
	v_lshlrev_b32_e32 v6, 3, v13
	s_addc_u32 s35, s29, s7
	v_ashrrev_i32_e32 v14, 6, v5
	v_and_b32_e32 v6, -16, v6
	s_ashr_i32 s40, s30, 31
	v_add_u32_e32 v6, v14, v6
	s_lshr_b32 s2, s40, 29
	v_and_b32_e32 v7, 3, v14
	v_lshrrev_b32_e32 v8, 2, v6
	v_lshlrev_b32_e32 v9, 1, v6
	v_and_b32_e32 v5, 0xc0, v5
	s_add_i32 s2, s30, s2
	s_ashr_i32 s11, s3, 6
	v_and_or_b32 v7, v6, s75, v7
	v_and_b32_e32 v8, 4, v8
	v_and_b32_e32 v9, 24, v9
	v_sub_u32_e32 v4, v4, v5
	s_ashr_i32 s6, s2, 3
	s_and_b32 s2, s2, -8
	s_ashr_i32 s10, s3, 8
	s_lshl_b32 s39, s11, 10
	v_or3_b32 v7, v7, v8, v9
	v_lshlrev_b32_e32 v8, 5, v13
	v_ashrrev_i16_sdwa v4, v1, sext(v4) dst_sel:DWORD dst_unused:UNUSED_PAD src0_sel:DWORD src1_sel:BYTE_0
	s_sub_i32 s2, s30, s2
	v_and_b32_e32 v8, 32, v8
	v_bfe_i32 v15, v4, 0, 16
	s_cmp_lt_i32 s2, 0
	v_add_lshl_u32 v4, v8, v15, 1
	s_cselect_b32 s7, s78, 0xb0
	v_lshl_add_u32 v132, v7, 11, v4
	v_lshl_add_u32 v134, v6, 11, v4
	v_bfe_i32 v4, v12, 27, 1
	s_mul_i32 s2, s2, s7
	v_lshrrev_b32_e32 v4, 22, v4
	s_add_i32 s2, s2, s6
	v_add_u32_e32 v4, v2, v4
	s_mul_hi_i32 s6, s2, 0x2e8ba2e9
	v_and_b32_e32 v4, 0xfffffc00, v4
	s_lshr_b32 s7, s6, 31
	s_ashr_i32 s6, s6, 5
	v_sub_u32_e32 v2, v2, v4
	s_add_i32 s6, s6, s7
	v_lshrrev_b32_e32 v4, 4, v2
	v_ashrrev_i32_e32 v5, 31, v12
	s_lshl_b32 s7, s6, 3
	s_mulk_i32 s6, 0xb0
	v_bitop3_b32 v2, v4, v2, 32 bitop3:0x6c
	v_lshrrev_b32_e32 v5, 26, v5
	s_sub_i32 s6, s2, s6
	v_ashrrev_i32_e32 v4, 31, v2
	v_add_u32_e32 v5, v12, v5
	s_bfe_u32 s2, s6, 0x3001c
	v_lshrrev_b32_e32 v4, 26, v4
	v_ashrrev_i32_e32 v17, 6, v5
	s_add_i32 s8, s6, s2
	v_add_u32_e32 v4, v2, v4
	v_lshlrev_b32_e32 v5, 3, v17
	s_sext_i32_i16 s2, s8
	s_and_b32 s8, s8, 0xfff8
	v_ashrrev_i32_e32 v16, 6, v4
	v_and_b32_e32 v5, -16, v5
	s_sub_i32 s6, s6, s8
	v_add_u32_e32 v5, v16, v5
	s_sext_i32_i16 s6, s6
	v_and_b32_e32 v6, 3, v16
	v_lshrrev_b32_e32 v7, 2, v5
	v_lshlrev_b32_e32 v8, 1, v5
	v_and_b32_e32 v4, 0xc0, v4
	s_lshr_b32 s2, s2, 3
	s_add_i32 s20, s7, s6
	v_and_or_b32 v6, v5, s75, v6
	v_and_b32_e32 v7, 4, v7
	v_and_b32_e32 v8, 24, v8
	v_sub_u32_e32 v2, v2, v4
	s_ashr_i32 s21, s20, 31
	s_bfe_i64 s[8:9], s[2:3], 0x100000
	v_or3_b32 v6, v6, v7, v8
	v_lshlrev_b32_e32 v7, 5, v17
	v_ashrrev_i16_sdwa v2, v1, sext(v2) dst_sel:DWORD dst_unused:UNUSED_PAD src0_sel:DWORD src1_sel:BYTE_0
	s_lshl_b64 s[6:7], s[20:21], 19
	s_lshl_b64 s[8:9], s[8:9], 19
	v_and_b32_e32 v7, 32, v7
	v_bfe_i32 v18, v2, 0, 16
	s_add_u32 s22, s34, s8
	v_add_lshl_u32 v2, v7, v18, 1
	s_addc_u32 s23, s35, s9
	s_add_i32 s41, s39, 0
	v_lshl_add_u32 v136, v6, 11, v2
	s_add_i32 m0, s41, 0x10000
	v_lshl_add_u32 v138, v5, 11, v2
	global_load_lds_dwordx4 v136, s[22:23]
	s_add_i32 m0, s41, 0x12000
	s_add_u32 s8, s22, 0x40000
	global_load_lds_dwordx4 v132, s[22:23]
	s_addc_u32 s9, s23, 0
	s_add_i32 m0, s41, 0x14000
	v_mov_b32_e32 v137, v3
	global_load_lds_dwordx4 v136, s[8:9]
	s_add_i32 m0, s41, 0x16000
	s_add_u32 s24, s31, s6
	s_addc_u32 s25, s33, s7
	s_add_i32 s42, s41, 0x2000
	global_load_lds_dwordx4 v132, s[8:9]
	s_mov_b32 m0, s41
	s_add_u32 s6, s24, 0x40000
	global_load_lds_dwordx4 v138, s[24:25]
	s_mov_b32 m0, s42
	s_addc_u32 s7, s25, 0
	s_add_i32 s43, s41, 0x4000
	global_load_lds_dwordx4 v134, s[24:25]
	s_mov_b32 m0, s43
	s_add_i32 s44, s41, 0x6000
	global_load_lds_dwordx4 v138, s[6:7]
	s_mov_b32 m0, s44
	v_mov_b32_e32 v133, v3
	global_load_lds_dwordx4 v134, s[6:7]
	v_mov_b32_e32 v139, v3
	v_mov_b32_e32 v135, v3
	s_cmp_eq_u32 s10, 1
	v_lshl_add_u64 v[10:11], s[22:23], 0, v[136:137]
	v_lshl_add_u64 v[8:9], s[22:23], 0, v[132:133]
	v_lshl_add_u64 v[4:5], s[24:25], 0, v[138:139]
	s_cselect_b64 s[6:7], -1, 0
	s_cmp_lg_u32 s10, 1
	v_lshl_add_u64 v[6:7], s[24:25], 0, v[134:135]
	v_lshl_add_u64 v[240:241], s[24:25], 0, v[138:139]
	v_lshl_add_u64 v[242:243], s[24:25], 0, v[134:135]
	s_cbranch_scc1 .LBB0_147
	s_barrier

; #define PG8_STAGE(bufoff, gbase, voff) do { _Pragma("unroll") for (int _i = 0; _i < 2; ++_i) \
;         __builtin_amdgcn_global_load_lds((const unsigned*)((const char*)(gbase) + (voff)[_i]), (PG8_LAS unsigned*)(lds + (bufoff) + ldsw + _i * 8192), 16, 0, 0); } while (0)
; #define PG8_LDA(dst, b, h) do { _Pragma("unroll") for (int m = 0; m < 4; ++m) _Pragma("unroll") for (int k = 0; k < 2; ++k) dst[m][k] = *(const PG8_LAS bf16x8*)(lds + PG8_SA(b, h) + aoff + m * 2048 + k * 1024); } while (0)
; #define PG8_LDB(dst, b, h) do { _Pragma("unroll") for (int n = 0; n < 2; ++n) _Pragma("unroll") for (int k = 0; k < 2; ++k) dst[n][k] = *(const PG8_LAS bf16x8*)(lds + PG8_SB(b, h) + boff + n * 2048 + k * 1024); } while (0)
; #define PG8_MMA(ai, bj, At, Bt) do { __builtin_amdgcn_s_setprio(1); _Pragma("unroll") for (int m = 0; m < 4; ++m) _Pragma("unroll") for (int n = 0; n < 2; ++n) _Pragma("unroll") for (int k = 0; k < 2; ++k) \
;         acc[ai][bj][m][n] = __builtin_amdgcn_mfma_f32_16x16x32_bf16(Bt[n][k], At[m][k], acc[ai][bj][m][n], 0, 0, 0); __builtin_amdgcn_s_setprio(0); } while (0)
; #define PG8_WAIT_V(n) asm volatile("s_waitcnt vmcnt(" #n ")" ::: "memory")
; #define PG8_WAIT_L(n) asm volatile("s_waitcnt lgkmcnt(" #n ")" ::: "memory")
; template <class Epi, class Sched, bool ALIGN_EPI = false, bool SP2 = false>
; __device__ __forceinline__ void gemm_phase(PG8_LAS unsigned char* lds, const Gemm g, const Sched& S, const Epi& E) {
;     ...
;             const bool last = (t == nt - 2);
;             const char* a1 = cA + (size_t)(t + 1) * kstep;
;             const char* a2 = last ? nA : cA + (size_t)(t + 2) * kstep; const char* b2 = last ? nB : cB + (size_t)(t + 2) * kstep;
;             const char* a3 = a2 + kstep; const char* b3 = b2 + kstep;
;             if (last && has_next) S.a_ready(nxt);
;             if constexpr (SP2) {
;             PG8_LDB(B0, 0, 0); PG8_LDB(B1, 0, 1); PG8_SCHED; PG8_LDA(At, 0, 0); PG8_STAGE(PG8_SA(1, 1), a1 + hstepA, voffA);
;             PG8_WAIT_V(8); PG8_WAIT_L(0); PG8_BAR; PG8_MMA(0, 0, At, B0); PG8_MMA(0, 1, At, B1); PG8_BAR; PG8_SCHED;
;             PG8_LDA(At, 0, 1); PG8_STAGE(PG8_SB(0, 0), b2, voffB); PG8_STAGE(PG8_SB(0, 1), b2 + hstepB, voffB); PG8_STAGE(PG8_SA(0, 0), a2, voffA);
;             PG8_WAIT_V(8); PG8_WAIT_L(0); PG8_BAR; PG8_MMA(1, 0, At, B0); PG8_MMA(1, 1, At, B1); PG8_BAR; PG8_SCHED;
.LBB0_152:
	s_ashr_i32 s15, s14, 31
	s_lshl_b64 s[16:17], s[14:15], 19
	s_add_u32 s16, s31, s16
	s_addc_u32 s17, s33, s17
	s_and_b64 s[18:19], s[2:3], exec
	s_cselect_b32 s15, s17, s25
	s_cselect_b32 s49, s16, s24
	s_ashr_i32 s13, s12, 31
	s_lshl_b64 s[18:19], s[12:13], 19
	s_add_u32 s18, s34, s18
	s_addc_u32 s19, s35, s19
	s_and_b64 s[26:27], s[2:3], exec
	s_cselect_b32 s13, s19, s23
	s_cselect_b32 s50, s18, s22
	s_add_u32 s51, s22, 0x100
	s_addc_u32 s52, s23, 0
	s_add_u32 s22, s24, 0x40080
	s_addc_u32 s23, s25, 0
	s_mov_b32 s53, -2
	s_add_u32 s24, s22, 0xfffc0080
	s_addc_u32 s25, s23, -1
	s_add_i32 s54, 0, 0x10000
	s_cmp_eq_u32 s53, 12
	s_cselect_b32 s27, s15, s25
	s_cselect_b32 s26, s49, s24
	v_add_u32_e32 v144, s54, v147
	s_cselect_b32 s25, s13, s52
	s_cselect_b32 s24, s50, s51
	s_add_i32 s56, 0, 0x14000
	ds_read_b128 v[150:153], v144
	ds_read_b128 v[154:157], v144 offset:1024
	ds_read_b128 v[158:161], v144 offset:2048
	ds_read_b128 v[162:165], v144 offset:3072
	v_add_u32_e32 v144, s56, v147
	ds_read_b128 v[166:169], v144
	ds_read_b128 v[170:173], v144 offset:1024
	ds_read_b128 v[174:177], v144 offset:2048
	ds_read_b128 v[178:181], v144 offset:3072
	v_lshl_add_u64 v[144:145], s[22:23], 0, v[142:143]
	s_add_i32 m0, s41, 0xc000
	ds_read_b128 v[182:185], v149
	ds_read_b128 v[186:189], v149 offset:1024
	ds_read_b128 v[190:193], v149 offset:2048
	ds_read_b128 v[194:197], v149 offset:3072
	ds_read_b128 v[210:213], v149 offset:4096
	ds_read_b128 v[226:229], v149 offset:5120
	ds_read_b128 v[230:233], v149 offset:6144
	ds_read_b128 v[234:237], v149 offset:7168
	v_lshl_add_u64 v[244:245], v[240:241], 0, s[64:65]
	s_mov_b32 m0, s45
	s_nop 0
	global_load_lds_dwordx4 v[244:245], off
	v_lshl_add_u64 v[244:245], v[242:243], 0, s[64:65]
	s_mov_b32 m0, s46
	s_nop 0
	global_load_lds_dwordx4 v[244:245], off
	s_add_i32 m0, s41, 0xc000
	s_nop 0
	global_load_lds_dwordx4 v[144:145], off
	v_lshl_add_u64 v[144:145], s[22:23], 0, v[140:141]
	s_add_i32 m0, s41, 0xe000
	s_nop 0
	global_load_lds_dwordx4 v[144:145], off
	s_waitcnt vmcnt(8)
	s_waitcnt lgkmcnt(0)
	s_barrier
	s_setprio 1
	s_waitcnt lgkmcnt(0)
	v_mfma_f32_16x16x32_bf16 v[128:131], v[150:153], v[182:185], 0
	v_mfma_f32_16x16x32_bf16 v[120:123], v[158:161], v[182:185], 0
	v_mfma_f32_16x16x32_bf16 v[112:115], v[150:153], v[190:193], 0
	v_mfma_f32_16x16x32_bf16 v[104:107], v[158:161], v[190:193], 0
	v_mfma_f32_16x16x32_bf16 v[96:99], v[150:153], v[210:213], 0
	v_mfma_f32_16x16x32_bf16 v[88:91], v[158:161], v[210:213], 0
	v_mfma_f32_16x16x32_bf16 v[80:83], v[150:153], v[230:233], 0
	v_mfma_f32_16x16x32_bf16 v[72:75], v[158:161], v[230:233], 0
	v_mfma_f32_16x16x32_bf16 v[128:131], v[154:157], v[186:189], v[128:131]
	v_mfma_f32_16x16x32_bf16 v[120:123], v[162:165], v[186:189], v[120:123]
	v_mfma_f32_16x16x32_bf16 v[112:115], v[154:157], v[194:197], v[112:115]
	v_mfma_f32_16x16x32_bf16 v[104:107], v[162:165], v[194:197], v[104:107]
	v_mfma_f32_16x16x32_bf16 v[96:99], v[154:157], v[226:229], v[96:99]
	v_mfma_f32_16x16x32_bf16 v[88:91], v[162:165], v[226:229], v[88:91]
	v_mfma_f32_16x16x32_bf16 v[80:83], v[154:157], v[234:237], v[80:83]
	v_mfma_f32_16x16x32_bf16 v[72:75], v[162:165], v[234:237], v[72:75]
	s_setprio 0
	s_setprio 1
	v_mfma_f32_16x16x32_bf16 v[124:127], v[166:169], v[182:185], 0
	v_mfma_f32_16x16x32_bf16 v[116:119], v[174:177], v[182:185], 0
	v_mfma_f32_16x16x32_bf16 v[108:111], v[166:169], v[190:193], 0
	v_mfma_f32_16x16x32_bf16 v[100:103], v[174:177], v[190:193], 0
	v_mfma_f32_16x16x32_bf16 v[92:95], v[166:169], v[210:213], 0
	v_mfma_f32_16x16x32_bf16 v[84:87], v[174:177], v[210:213], 0
	v_mfma_f32_16x16x32_bf16 v[76:79], v[166:169], v[230:233], 0
	v_mfma_f32_16x16x32_bf16 v[68:71], v[174:177], v[230:233], 0
	v_mfma_f32_16x16x32_bf16 v[124:127], v[170:173], v[186:189], v[124:127]
	v_mfma_f32_16x16x32_bf16 v[116:119], v[178:181], v[186:189], v[116:119]
	v_mfma_f32_16x16x32_bf16 v[108:111], v[170:173], v[194:197], v[108:111]
	v_mfma_f32_16x16x32_bf16 v[100:103], v[178:181], v[194:197], v[100:103]
	v_mfma_f32_16x16x32_bf16 v[92:95], v[170:173], v[226:229], v[92:95]
	v_mfma_f32_16x16x32_bf16 v[84:87], v[178:181], v[226:229], v[84:87]
	v_mfma_f32_16x16x32_bf16 v[76:79], v[170:173], v[234:237], v[76:79]
	v_mfma_f32_16x16x32_bf16 v[68:71], v[178:181], v[234:237], v[68:71]
	s_setprio 0
	s_barrier
	s_add_i32 s54, s54, s39
	v_lshl_add_u64 v[144:145], s[24:25], 0, v[136:137]
	s_mov_b32 m0, s54
	ds_read_b128 v[182:185], v149 offset:16384
	ds_read_b128 v[186:189], v149 offset:17408
	ds_read_b128 v[190:193], v149 offset:18432
	ds_read_b128 v[194:197], v149 offset:19456
	ds_read_b128 v[210:213], v149 offset:20480
	ds_read_b128 v[226:229], v149 offset:21504
	ds_read_b128 v[230:233], v149 offset:22528
	ds_read_b128 v[234:237], v149 offset:23552
	global_load_lds_dwordx4 v[144:145], off
	s_add_i32 m0, s54, 0x2000
	s_add_u32 s54, s24, 0x40000
	v_lshl_add_u64 v[238:239], s[24:25], 0, v[132:133]
	s_addc_u32 s55, s25, 0
	s_add_i32 s56, s56, s39
	global_load_lds_dwordx4 v[238:239], off
	v_lshl_add_u64 v[240:241], s[54:55], 0, v[136:137]
	s_mov_b32 m0, s56
	v_lshl_add_u64 v[242:243], s[26:27], 0, v[134:135]
	global_load_lds_dwordx4 v[240:241], off
	v_lshl_add_u64 v[240:241], s[54:55], 0, v[132:133]
	s_add_i32 m0, s56, 0x2000
	s_nop 0
	global_load_lds_dwordx4 v[240:241], off
	v_lshl_add_u64 v[240:241], s[26:27], 0, v[138:139]
	s_waitcnt vmcnt(6)
	s_waitcnt lgkmcnt(0)
	s_barrier
; #define PG8_STAGE(bufoff, gbase, voff) do { _Pragma("unroll") for (int _i = 0; _i < 2; ++_i) \
;         __builtin_amdgcn_global_load_lds((const unsigned*)((const char*)(gbase) + (voff)[_i]), (PG8_LAS unsigned*)(lds + (bufoff) + ldsw + _i * 8192), 16, 0, 0); } while (0)
; #define PG8_LDA(dst, b, h) do { _Pragma("unroll") for (int m = 0; m < 4; ++m) _Pragma("unroll") for (int k = 0; k < 2; ++k) dst[m][k] = *(const PG8_LAS bf16x8*)(lds + PG8_SA(b, h) + aoff + m * 2048 + k * 1024); } while (0)
; #define PG8_LDB(dst, b, h) do { _Pragma("unroll") for (int n = 0; n < 2; ++n) _Pragma("unroll") for (int k = 0; k < 2; ++k) dst[n][k] = *(const PG8_LAS bf16x8*)(lds + PG8_SB(b, h) + boff + n * 2048 + k * 1024); } while (0)
; #define PG8_MMA(ai, bj, At, Bt) do { __builtin_amdgcn_s_setprio(1); _Pragma("unroll") for (int m = 0; m < 4; ++m) _Pragma("unroll") for (int n = 0; n < 2; ++n) _Pragma("unroll") for (int k = 0; k < 2; ++k) \
;         acc[ai][bj][m][n] = __builtin_amdgcn_mfma_f32_16x16x32_bf16(Bt[n][k], At[m][k], acc[ai][bj][m][n], 0, 0, 0); __builtin_amdgcn_s_setprio(0); } while (0)
; #define PG8_WAIT_V(n) asm volatile("s_waitcnt vmcnt(" #n ")" ::: "memory")
; #define PG8_WAIT_L(n) asm volatile("s_waitcnt lgkmcnt(" #n ")" ::: "memory")
; #define PG8_BAR __builtin_amdgcn_s_barrier()
; #define PG8_SCHED __builtin_amdgcn_sched_barrier(0)
; template <class Epi, class Sched, bool ALIGN_EPI = false, bool SP2 = false>
; __device__ __forceinline__ void gemm_phase(PG8_LAS unsigned char* lds, const Gemm g, const Sched& S, const Epi& E) {
;     ...
;             PG8_WAIT_V(8); PG8_WAIT_L(0); PG8_BAR; PG8_MMA(1, 0, At, B0); PG8_MMA(1, 1, At, B1); PG8_BAR; PG8_SCHED;
;             PG8_LDB(B0, 1, 0); PG8_LDB(B1, 1, 1); PG8_SCHED; PG8_LDA(At, 1, 0); PG8_STAGE(PG8_SA(0, 1), a2 + hstepA, voffA);
;             PG8_WAIT_V(8); PG8_WAIT_L(0); PG8_BAR; PG8_MMA(0, 0, At, B0); PG8_MMA(0, 1, At, B1); PG8_BAR; PG8_SCHED;
	s_setprio 1
	s_waitcnt lgkmcnt(0)
	v_mfma_f32_16x16x32_bf16 v[64:67], v[150:153], v[182:185], 0
	v_mfma_f32_16x16x32_bf16 v[56:59], v[158:161], v[182:185], 0
	v_mfma_f32_16x16x32_bf16 v[48:51], v[150:153], v[190:193], 0
	v_mfma_f32_16x16x32_bf16 v[40:43], v[158:161], v[190:193], 0
	v_mfma_f32_16x16x32_bf16 v[32:35], v[150:153], v[210:213], 0
	v_mfma_f32_16x16x32_bf16 v[24:27], v[158:161], v[210:213], 0
	v_mfma_f32_16x16x32_bf16 v[16:19], v[150:153], v[230:233], 0
	v_mfma_f32_16x16x32_bf16 v[8:11], v[158:161], v[230:233], 0
	v_mfma_f32_16x16x32_bf16 v[64:67], v[154:157], v[186:189], v[64:67]
	v_mfma_f32_16x16x32_bf16 v[56:59], v[162:165], v[186:189], v[56:59]
	v_mfma_f32_16x16x32_bf16 v[48:51], v[154:157], v[194:197], v[48:51]
	v_mfma_f32_16x16x32_bf16 v[40:43], v[162:165], v[194:197], v[40:43]
	v_mfma_f32_16x16x32_bf16 v[32:35], v[154:157], v[226:229], v[32:35]
	v_mfma_f32_16x16x32_bf16 v[24:27], v[162:165], v[226:229], v[24:27]
	v_mfma_f32_16x16x32_bf16 v[16:19], v[154:157], v[234:237], v[16:19]
	v_mfma_f32_16x16x32_bf16 v[8:11], v[162:165], v[234:237], v[8:11]
	s_setprio 0
	s_setprio 1
	v_mfma_f32_16x16x32_bf16 v[60:63], v[166:169], v[182:185], 0
	v_mfma_f32_16x16x32_bf16 v[52:55], v[174:177], v[182:185], 0
	v_mfma_f32_16x16x32_bf16 v[44:47], v[166:169], v[190:193], 0
	v_mfma_f32_16x16x32_bf16 v[36:39], v[174:177], v[190:193], 0
	v_mfma_f32_16x16x32_bf16 v[28:31], v[166:169], v[210:213], 0
	v_mfma_f32_16x16x32_bf16 v[20:23], v[174:177], v[210:213], 0
	v_mfma_f32_16x16x32_bf16 v[12:15], v[166:169], v[230:233], 0
	v_mfma_f32_16x16x32_bf16 v[4:7], v[174:177], v[230:233], 0
	v_mfma_f32_16x16x32_bf16 v[60:63], v[170:173], v[186:189], v[60:63]
	v_mfma_f32_16x16x32_bf16 v[52:55], v[178:181], v[186:189], v[52:55]
	v_mfma_f32_16x16x32_bf16 v[44:47], v[170:173], v[194:197], v[44:47]
	v_mfma_f32_16x16x32_bf16 v[36:39], v[178:181], v[194:197], v[36:39]
	v_mfma_f32_16x16x32_bf16 v[28:31], v[170:173], v[226:229], v[28:31]
	v_mfma_f32_16x16x32_bf16 v[20:23], v[178:181], v[226:229], v[20:23]
	v_mfma_f32_16x16x32_bf16 v[12:15], v[170:173], v[234:237], v[12:15]
	v_mfma_f32_16x16x32_bf16 v[4:7], v[178:181], v[234:237], v[4:7]
	s_setprio 0
	s_barrier
	s_add_i32 s54, 0, 0x18000
	s_add_i32 s55, 0, 0x1c000
	v_add_u32_e32 v162, s54, v147
	v_add_u32_e32 v178, s55, v147
	ds_read_b128 v[150:153], v162
	ds_read_b128 v[154:157], v162 offset:1024
	ds_read_b128 v[158:161], v162 offset:2048
	ds_read_b128 v[162:165], v162 offset:3072
	ds_read_b128 v[166:169], v178
	ds_read_b128 v[170:173], v178 offset:1024
	ds_read_b128 v[174:177], v178 offset:2048
	ds_read_b128 v[178:181], v178 offset:3072
	s_add_u32 s26, s26, 0x40000
	s_addc_u32 s27, s27, 0
	s_mov_b32 m0, s43
	v_lshl_add_u64 v[244:245], s[26:27], 0, v[138:139]
	ds_read_b128 v[182:185], v149 offset:32768
	ds_read_b128 v[186:189], v149 offset:33792
	ds_read_b128 v[190:193], v149 offset:34816
	ds_read_b128 v[194:197], v149 offset:35840
	ds_read_b128 v[210:213], v149 offset:36864
	ds_read_b128 v[226:229], v149 offset:37888
	ds_read_b128 v[230:233], v149 offset:38912
	ds_read_b128 v[234:237], v149 offset:39936
	s_mov_b32 m0, s41
	s_nop 0
	global_load_lds_dwordx4 v[240:241], off
	s_mov_b32 m0, s42
	s_nop 0
	global_load_lds_dwordx4 v[242:243], off
	s_mov_b32 m0, s43
	s_nop 0
	global_load_lds_dwordx4 v[244:245], off
	v_lshl_add_u64 v[244:245], s[26:27], 0, v[134:135]
	s_mov_b32 m0, s44
	s_nop 0
	global_load_lds_dwordx4 v[244:245], off
	s_waitcnt vmcnt(8)
	s_waitcnt lgkmcnt(0)
	s_barrier
	s_setprio 1
	s_waitcnt lgkmcnt(0)
	v_mfma_f32_16x16x32_bf16 v[128:131], v[150:153], v[182:185], v[128:131]
	v_mfma_f32_16x16x32_bf16 v[120:123], v[158:161], v[182:185], v[120:123]
	v_mfma_f32_16x16x32_bf16 v[112:115], v[150:153], v[190:193], v[112:115]
	v_mfma_f32_16x16x32_bf16 v[104:107], v[158:161], v[190:193], v[104:107]
	v_mfma_f32_16x16x32_bf16 v[96:99], v[150:153], v[210:213], v[96:99]
	v_mfma_f32_16x16x32_bf16 v[88:91], v[158:161], v[210:213], v[88:91]
	v_mfma_f32_16x16x32_bf16 v[80:83], v[150:153], v[230:233], v[80:83]
	v_mfma_f32_16x16x32_bf16 v[72:75], v[158:161], v[230:233], v[72:75]
	v_mfma_f32_16x16x32_bf16 v[128:131], v[154:157], v[186:189], v[128:131]
	v_mfma_f32_16x16x32_bf16 v[120:123], v[162:165], v[186:189], v[120:123]
	v_mfma_f32_16x16x32_bf16 v[112:115], v[154:157], v[194:197], v[112:115]
	v_mfma_f32_16x16x32_bf16 v[104:107], v[162:165], v[194:197], v[104:107]
	v_mfma_f32_16x16x32_bf16 v[96:99], v[154:157], v[226:229], v[96:99]
	v_mfma_f32_16x16x32_bf16 v[88:91], v[162:165], v[226:229], v[88:91]
	v_mfma_f32_16x16x32_bf16 v[80:83], v[154:157], v[234:237], v[80:83]
	v_mfma_f32_16x16x32_bf16 v[72:75], v[162:165], v[234:237], v[72:75]
	s_setprio 0
	s_setprio 1
	v_mfma_f32_16x16x32_bf16 v[124:127], v[166:169], v[182:185], v[124:127]
	v_mfma_f32_16x16x32_bf16 v[116:119], v[174:177], v[182:185], v[116:119]
	v_mfma_f32_16x16x32_bf16 v[108:111], v[166:169], v[190:193], v[108:111]
	v_mfma_f32_16x16x32_bf16 v[100:103], v[174:177], v[190:193], v[100:103]
	v_mfma_f32_16x16x32_bf16 v[92:95], v[166:169], v[210:213], v[92:95]
	v_mfma_f32_16x16x32_bf16 v[84:87], v[174:177], v[210:213], v[84:87]
	v_mfma_f32_16x16x32_bf16 v[76:79], v[166:169], v[230:233], v[76:79]
	v_mfma_f32_16x16x32_bf16 v[68:71], v[174:177], v[230:233], v[68:71]
	v_mfma_f32_16x16x32_bf16 v[124:127], v[170:173], v[186:189], v[124:127]
	v_mfma_f32_16x16x32_bf16 v[116:119], v[178:181], v[186:189], v[116:119]
	v_mfma_f32_16x16x32_bf16 v[108:111], v[170:173], v[194:197], v[108:111]
	v_mfma_f32_16x16x32_bf16 v[100:103], v[178:181], v[194:197], v[100:103]
	v_mfma_f32_16x16x32_bf16 v[92:95], v[170:173], v[226:229], v[92:95]
	v_mfma_f32_16x16x32_bf16 v[84:87], v[178:181], v[226:229], v[84:87]
	v_mfma_f32_16x16x32_bf16 v[76:79], v[170:173], v[234:237], v[76:79]
	v_mfma_f32_16x16x32_bf16 v[68:71], v[178:181], v[234:237], v[68:71]
	s_setprio 0
	s_barrier
; #define PG8_STAGE(bufoff, gbase, voff) do { _Pragma("unroll") for (int _i = 0; _i < 2; ++_i) \
;         __builtin_amdgcn_global_load_lds((const unsigned*)((const char*)(gbase) + (voff)[_i]), (PG8_LAS unsigned*)(lds + (bufoff) + ldsw + _i * 8192), 16, 0, 0); } while (0)
; #define PG8_LDA(dst, b, h) do { _Pragma("unroll") for (int m = 0; m < 4; ++m) _Pragma("unroll") for (int k = 0; k < 2; ++k) dst[m][k] = *(const PG8_LAS bf16x8*)(lds + PG8_SA(b, h) + aoff + m * 2048 + k * 1024); } while (0)
; #define PG8_LDB(dst, b, h) do { _Pragma("unroll") for (int n = 0; n < 2; ++n) _Pragma("unroll") for (int k = 0; k < 2; ++k) dst[n][k] = *(const PG8_LAS bf16x8*)(lds + PG8_SB(b, h) + boff + n * 2048 + k * 1024); } while (0)
; #define PG8_MMA(ai, bj, At, Bt) do { __builtin_amdgcn_s_setprio(1); _Pragma("unroll") for (int m = 0; m < 4; ++m) _Pragma("unroll") for (int n = 0; n < 2; ++n) _Pragma("unroll") for (int k = 0; k < 2; ++k) \
;         acc[ai][bj][m][n] = __builtin_amdgcn_mfma_f32_16x16x32_bf16(Bt[n][k], At[m][k], acc[ai][bj][m][n], 0, 0, 0); __builtin_amdgcn_s_setprio(0); } while (0)
; #define PG8_WAIT_V(n) asm volatile("s_waitcnt vmcnt(" #n ")" ::: "memory")
; #define PG8_WAIT_L(n) asm volatile("s_waitcnt lgkmcnt(" #n ")" ::: "memory")
; #define PG8_BAR __builtin_amdgcn_s_barrier()
; #define PG8_SCHED __builtin_amdgcn_sched_barrier(0)
; template <class Epi, class Sched, bool ALIGN_EPI = false, bool SP2 = false>
; __device__ __forceinline__ void gemm_phase(PG8_LAS unsigned char* lds, const Gemm g, const Sched& S, const Epi& E) {
;     ...
;             PG8_LDB(B0, 0, 0); PG8_LDB(B1, 0, 1); PG8_SCHED; PG8_LDA(At, 0, 0); PG8_STAGE(PG8_SA(1, 1), a1 + hstepA, voffA);
;             PG8_WAIT_V(8); PG8_WAIT_L(0); PG8_BAR; PG8_MMA(0, 0, At, B0); PG8_MMA(0, 1, At, B1); PG8_BAR; PG8_SCHED;
;     ...
;             PG8_LDB(B0, 1, 0); PG8_LDB(B1, 1, 1); PG8_SCHED; PG8_LDA(At, 1, 0); PG8_STAGE(PG8_SA(0, 1), a2 + hstepA, voffA);
;             PG8_WAIT_V(8); PG8_WAIT_L(0); PG8_BAR; PG8_MMA(0, 0, At, B0); PG8_MMA(0, 1, At, B1); PG8_BAR; PG8_SCHED;
;             PG8_LDA(At, 1, 1); PG8_STAGE(PG8_SB(1, 0), b3, voffB); PG8_STAGE(PG8_SB(1, 1), b3 + hstepB, voffB); PG8_STAGE(PG8_SA(1, 0), a3, voffA);
;             PG8_WAIT_V(8); PG8_WAIT_L(0); PG8_BAR; PG8_MMA(1, 0, At, B0); PG8_MMA(1, 1, At, B1); PG8_BAR; PG8_SCHED;
	s_add_i32 s26, s54, s39
	v_lshl_add_u64 v[144:145], v[144:145], 0, s[64:65]
	s_mov_b32 m0, s26
	ds_read_b128 v[182:185], v149 offset:49152
	ds_read_b128 v[186:189], v149 offset:50176
	ds_read_b128 v[190:193], v149 offset:51200
	ds_read_b128 v[194:197], v149 offset:52224
	ds_read_b128 v[210:213], v149 offset:53248
	ds_read_b128 v[226:229], v149 offset:54272
	ds_read_b128 v[230:233], v149 offset:55296
	ds_read_b128 v[234:237], v149 offset:56320
	global_load_lds_dwordx4 v[144:145], off
	s_add_i32 m0, s26, 0x2000
	s_add_u32 s24, s24, 0x40080
	v_lshl_add_u64 v[144:145], v[238:239], 0, s[64:65]
	s_addc_u32 s25, s25, 0
	s_add_i32 s26, s55, s39
	global_load_lds_dwordx4 v[144:145], off
	v_lshl_add_u64 v[144:145], s[24:25], 0, v[136:137]
	s_mov_b32 m0, s26
	s_nop 0
	global_load_lds_dwordx4 v[144:145], off
	v_lshl_add_u64 v[144:145], s[24:25], 0, v[132:133]
	s_add_i32 m0, s26, 0x2000
	s_nop 0
	global_load_lds_dwordx4 v[144:145], off
	s_waitcnt vmcnt(6)
	s_waitcnt lgkmcnt(0)
	s_barrier
	s_setprio 1
	s_waitcnt lgkmcnt(0)
	v_mfma_f32_16x16x32_bf16 v[64:67], v[150:153], v[182:185], v[64:67]
	v_mfma_f32_16x16x32_bf16 v[56:59], v[158:161], v[182:185], v[56:59]
	v_mfma_f32_16x16x32_bf16 v[48:51], v[150:153], v[190:193], v[48:51]
	v_mfma_f32_16x16x32_bf16 v[40:43], v[158:161], v[190:193], v[40:43]
	v_mfma_f32_16x16x32_bf16 v[32:35], v[150:153], v[210:213], v[32:35]
	v_mfma_f32_16x16x32_bf16 v[24:27], v[158:161], v[210:213], v[24:27]
	v_mfma_f32_16x16x32_bf16 v[16:19], v[150:153], v[230:233], v[16:19]
	v_mfma_f32_16x16x32_bf16 v[8:11], v[158:161], v[230:233], v[8:11]
	v_mfma_f32_16x16x32_bf16 v[64:67], v[154:157], v[186:189], v[64:67]
	v_mfma_f32_16x16x32_bf16 v[56:59], v[162:165], v[186:189], v[56:59]
	v_mfma_f32_16x16x32_bf16 v[48:51], v[154:157], v[194:197], v[48:51]
	v_mfma_f32_16x16x32_bf16 v[40:43], v[162:165], v[194:197], v[40:43]
	v_mfma_f32_16x16x32_bf16 v[32:35], v[154:157], v[226:229], v[32:35]
	v_mfma_f32_16x16x32_bf16 v[24:27], v[162:165], v[226:229], v[24:27]
	v_mfma_f32_16x16x32_bf16 v[16:19], v[154:157], v[234:237], v[16:19]
	v_mfma_f32_16x16x32_bf16 v[8:11], v[162:165], v[234:237], v[8:11]
	s_setprio 0
	s_setprio 1
	v_mfma_f32_16x16x32_bf16 v[60:63], v[166:169], v[182:185], v[60:63]
	v_mfma_f32_16x16x32_bf16 v[52:55], v[174:177], v[182:185], v[52:55]
	v_mfma_f32_16x16x32_bf16 v[44:47], v[166:169], v[190:193], v[44:47]
	v_mfma_f32_16x16x32_bf16 v[36:39], v[174:177], v[190:193], v[36:39]
	v_mfma_f32_16x16x32_bf16 v[28:31], v[166:169], v[210:213], v[28:31]
	v_mfma_f32_16x16x32_bf16 v[20:23], v[174:177], v[210:213], v[20:23]
	v_mfma_f32_16x16x32_bf16 v[12:15], v[166:169], v[230:233], v[12:15]
	v_mfma_f32_16x16x32_bf16 v[4:7], v[174:177], v[230:233], v[4:7]
	v_mfma_f32_16x16x32_bf16 v[60:63], v[170:173], v[186:189], v[60:63]
	v_mfma_f32_16x16x32_bf16 v[52:55], v[178:181], v[186:189], v[52:55]
	v_mfma_f32_16x16x32_bf16 v[44:47], v[170:173], v[194:197], v[44:47]
	v_mfma_f32_16x16x32_bf16 v[36:39], v[178:181], v[194:197], v[36:39]
	v_mfma_f32_16x16x32_bf16 v[28:31], v[170:173], v[226:229], v[28:31]
	v_mfma_f32_16x16x32_bf16 v[20:23], v[178:181], v[226:229], v[20:23]
	v_mfma_f32_16x16x32_bf16 v[12:15], v[170:173], v[234:237], v[12:15]
	v_mfma_f32_16x16x32_bf16 v[4:7], v[178:181], v[234:237], v[4:7]
	s_setprio 0
	s_barrier
	s_add_i32 s53, s53, 2
	s_add_u32 s51, s51, 0x100
	s_addc_u32 s52, s52, 0
	s_add_u32 s22, s22, 0x100
	s_addc_u32 s23, s23, 0
	s_cmp_gt_u32 s53, 13
	s_cbranch_scc1 .Lpeel_exit_0
.LBB0_153:
	s_add_u32 s24, s22, 0xfffc0080
	s_addc_u32 s25, s23, -1
	s_add_i32 s54, 0, 0x10000
	s_cmp_eq_u32 s53, 12
	s_cselect_b32 s27, s15, s25
	s_cselect_b32 s26, s49, s24
	v_add_u32_e32 v144, s54, v147
	s_cselect_b32 s25, s13, s52
	s_cselect_b32 s24, s50, s51
	s_add_i32 s56, 0, 0x14000
	ds_read_b128 v[150:153], v144
	ds_read_b128 v[154:157], v144 offset:1024
	ds_read_b128 v[158:161], v144 offset:2048
	ds_read_b128 v[162:165], v144 offset:3072
	v_add_u32_e32 v144, s56, v147
	ds_read_b128 v[166:169], v144
	ds_read_b128 v[170:173], v144 offset:1024
	ds_read_b128 v[174:177], v144 offset:2048
	ds_read_b128 v[178:181], v144 offset:3072
	v_lshl_add_u64 v[144:145], s[22:23], 0, v[142:143]
	s_add_i32 m0, s41, 0xc000
	ds_read_b128 v[182:185], v149
	ds_read_b128 v[186:189], v149 offset:1024
	ds_read_b128 v[190:193], v149 offset:2048
	ds_read_b128 v[194:197], v149 offset:3072
	ds_read_b128 v[210:213], v149 offset:4096
	ds_read_b128 v[226:229], v149 offset:5120
	ds_read_b128 v[230:233], v149 offset:6144
	ds_read_b128 v[234:237], v149 offset:7168
	v_lshl_add_u64 v[244:245], v[240:241], 0, s[64:65]
	s_mov_b32 m0, s45
	s_nop 0
	global_load_lds_dwordx4 v[244:245], off
	v_lshl_add_u64 v[244:245], v[242:243], 0, s[64:65]
	s_mov_b32 m0, s46
	s_nop 0
	global_load_lds_dwordx4 v[244:245], off
	s_add_i32 m0, s41, 0xc000
	s_nop 0
	global_load_lds_dwordx4 v[144:145], off
	v_lshl_add_u64 v[144:145], s[22:23], 0, v[140:141]
	s_add_i32 m0, s41, 0xe000
	s_nop 0
	global_load_lds_dwordx4 v[144:145], off
	s_waitcnt vmcnt(8)
	s_waitcnt lgkmcnt(0)
	s_barrier
; #define PG8_STAGE(bufoff, gbase, voff) do { _Pragma("unroll") for (int _i = 0; _i < 2; ++_i) \
;         __builtin_amdgcn_global_load_lds((const unsigned*)((const char*)(gbase) + (voff)[_i]), (PG8_LAS unsigned*)(lds + (bufoff) + ldsw + _i * 8192), 16, 0, 0); } while (0)
; #define PG8_LDA(dst, b, h) do { _Pragma("unroll") for (int m = 0; m < 4; ++m) _Pragma("unroll") for (int k = 0; k < 2; ++k) dst[m][k] = *(const PG8_LAS bf16x8*)(lds + PG8_SA(b, h) + aoff + m * 2048 + k * 1024); } while (0)
; #define PG8_MMA(ai, bj, At, Bt) do { __builtin_amdgcn_s_setprio(1); _Pragma("unroll") for (int m = 0; m < 4; ++m) _Pragma("unroll") for (int n = 0; n < 2; ++n) _Pragma("unroll") for (int k = 0; k < 2; ++k) \
;         acc[ai][bj][m][n] = __builtin_amdgcn_mfma_f32_16x16x32_bf16(Bt[n][k], At[m][k], acc[ai][bj][m][n], 0, 0, 0); __builtin_amdgcn_s_setprio(0); } while (0)
; #define PG8_WAIT_V(n) asm volatile("s_waitcnt vmcnt(" #n ")" ::: "memory")
; #define PG8_WAIT_L(n) asm volatile("s_waitcnt lgkmcnt(" #n ")" ::: "memory")
; #define PG8_BAR __builtin_amdgcn_s_barrier()
; #define PG8_SCHED __builtin_amdgcn_sched_barrier(0)
; template <class Epi, class Sched, bool ALIGN_EPI = false, bool SP2 = false>
; __device__ __forceinline__ void gemm_phase(PG8_LAS unsigned char* lds, const Gemm g, const Sched& S, const Epi& E) {
;     ...
;             PG8_WAIT_V(8); PG8_WAIT_L(0); PG8_BAR; PG8_MMA(0, 0, At, B0); PG8_MMA(0, 1, At, B1); PG8_BAR; PG8_SCHED;
;             PG8_LDA(At, 0, 1); PG8_STAGE(PG8_SB(0, 0), b2, voffB); PG8_STAGE(PG8_SB(0, 1), b2 + hstepB, voffB); PG8_STAGE(PG8_SA(0, 0), a2, voffA);
;             PG8_WAIT_V(8); PG8_WAIT_L(0); PG8_BAR; PG8_MMA(1, 0, At, B0); PG8_MMA(1, 1, At, B1); PG8_BAR; PG8_SCHED;
	s_setprio 1
	s_waitcnt lgkmcnt(0)
	v_mfma_f32_16x16x32_bf16 v[128:131], v[150:153], v[182:185], v[128:131]
	v_mfma_f32_16x16x32_bf16 v[120:123], v[158:161], v[182:185], v[120:123]
	v_mfma_f32_16x16x32_bf16 v[112:115], v[150:153], v[190:193], v[112:115]
	v_mfma_f32_16x16x32_bf16 v[104:107], v[158:161], v[190:193], v[104:107]
	v_mfma_f32_16x16x32_bf16 v[96:99], v[150:153], v[210:213], v[96:99]
	v_mfma_f32_16x16x32_bf16 v[88:91], v[158:161], v[210:213], v[88:91]
	v_mfma_f32_16x16x32_bf16 v[80:83], v[150:153], v[230:233], v[80:83]
	v_mfma_f32_16x16x32_bf16 v[72:75], v[158:161], v[230:233], v[72:75]
	v_mfma_f32_16x16x32_bf16 v[128:131], v[154:157], v[186:189], v[128:131]
	v_mfma_f32_16x16x32_bf16 v[120:123], v[162:165], v[186:189], v[120:123]
	v_mfma_f32_16x16x32_bf16 v[112:115], v[154:157], v[194:197], v[112:115]
	v_mfma_f32_16x16x32_bf16 v[104:107], v[162:165], v[194:197], v[104:107]
	v_mfma_f32_16x16x32_bf16 v[96:99], v[154:157], v[226:229], v[96:99]
	v_mfma_f32_16x16x32_bf16 v[88:91], v[162:165], v[226:229], v[88:91]
	v_mfma_f32_16x16x32_bf16 v[80:83], v[154:157], v[234:237], v[80:83]
	v_mfma_f32_16x16x32_bf16 v[72:75], v[162:165], v[234:237], v[72:75]
	s_setprio 0
	s_setprio 1
	v_mfma_f32_16x16x32_bf16 v[124:127], v[166:169], v[182:185], v[124:127]
	v_mfma_f32_16x16x32_bf16 v[116:119], v[174:177], v[182:185], v[116:119]
	v_mfma_f32_16x16x32_bf16 v[108:111], v[166:169], v[190:193], v[108:111]
	v_mfma_f32_16x16x32_bf16 v[100:103], v[174:177], v[190:193], v[100:103]
	v_mfma_f32_16x16x32_bf16 v[92:95], v[166:169], v[210:213], v[92:95]
	v_mfma_f32_16x16x32_bf16 v[84:87], v[174:177], v[210:213], v[84:87]
	v_mfma_f32_16x16x32_bf16 v[76:79], v[166:169], v[230:233], v[76:79]
	v_mfma_f32_16x16x32_bf16 v[68:71], v[174:177], v[230:233], v[68:71]
	v_mfma_f32_16x16x32_bf16 v[124:127], v[170:173], v[186:189], v[124:127]
	v_mfma_f32_16x16x32_bf16 v[116:119], v[178:181], v[186:189], v[116:119]
	v_mfma_f32_16x16x32_bf16 v[108:111], v[170:173], v[194:197], v[108:111]
	v_mfma_f32_16x16x32_bf16 v[100:103], v[178:181], v[194:197], v[100:103]
	v_mfma_f32_16x16x32_bf16 v[92:95], v[170:173], v[226:229], v[92:95]
	v_mfma_f32_16x16x32_bf16 v[84:87], v[178:181], v[226:229], v[84:87]
	v_mfma_f32_16x16x32_bf16 v[76:79], v[170:173], v[234:237], v[76:79]
	v_mfma_f32_16x16x32_bf16 v[68:71], v[178:181], v[234:237], v[68:71]
	s_setprio 0
	s_barrier
	s_add_i32 s54, s54, s39
	v_lshl_add_u64 v[144:145], s[24:25], 0, v[136:137]
	s_mov_b32 m0, s54
	ds_read_b128 v[182:185], v149 offset:16384
	ds_read_b128 v[186:189], v149 offset:17408
	ds_read_b128 v[190:193], v149 offset:18432
	ds_read_b128 v[194:197], v149 offset:19456
	ds_read_b128 v[210:213], v149 offset:20480
	ds_read_b128 v[226:229], v149 offset:21504
	ds_read_b128 v[230:233], v149 offset:22528
	ds_read_b128 v[234:237], v149 offset:23552
	global_load_lds_dwordx4 v[144:145], off
	s_add_i32 m0, s54, 0x2000
	s_add_u32 s54, s24, 0x40000
	v_lshl_add_u64 v[238:239], s[24:25], 0, v[132:133]
	s_addc_u32 s55, s25, 0
	s_add_i32 s56, s56, s39
	global_load_lds_dwordx4 v[238:239], off
	v_lshl_add_u64 v[240:241], s[54:55], 0, v[136:137]
	s_mov_b32 m0, s56
	v_lshl_add_u64 v[242:243], s[26:27], 0, v[134:135]
	global_load_lds_dwordx4 v[240:241], off
	v_lshl_add_u64 v[240:241], s[54:55], 0, v[132:133]
	s_add_i32 m0, s56, 0x2000
	s_nop 0
	global_load_lds_dwordx4 v[240:241], off
	v_lshl_add_u64 v[240:241], s[26:27], 0, v[138:139]
	s_waitcnt vmcnt(6)
	s_waitcnt lgkmcnt(0)
	s_barrier
	s_setprio 1
	s_waitcnt lgkmcnt(0)
	v_mfma_f32_16x16x32_bf16 v[64:67], v[150:153], v[182:185], v[64:67]
	v_mfma_f32_16x16x32_bf16 v[56:59], v[158:161], v[182:185], v[56:59]
	v_mfma_f32_16x16x32_bf16 v[48:51], v[150:153], v[190:193], v[48:51]
	v_mfma_f32_16x16x32_bf16 v[40:43], v[158:161], v[190:193], v[40:43]
	v_mfma_f32_16x16x32_bf16 v[32:35], v[150:153], v[210:213], v[32:35]
	v_mfma_f32_16x16x32_bf16 v[24:27], v[158:161], v[210:213], v[24:27]
	v_mfma_f32_16x16x32_bf16 v[16:19], v[150:153], v[230:233], v[16:19]
	v_mfma_f32_16x16x32_bf16 v[8:11], v[158:161], v[230:233], v[8:11]
	v_mfma_f32_16x16x32_bf16 v[64:67], v[154:157], v[186:189], v[64:67]
	v_mfma_f32_16x16x32_bf16 v[56:59], v[162:165], v[186:189], v[56:59]
	v_mfma_f32_16x16x32_bf16 v[48:51], v[154:157], v[194:197], v[48:51]
	v_mfma_f32_16x16x32_bf16 v[40:43], v[162:165], v[194:197], v[40:43]
	v_mfma_f32_16x16x32_bf16 v[32:35], v[154:157], v[226:229], v[32:35]
	v_mfma_f32_16x16x32_bf16 v[24:27], v[162:165], v[226:229], v[24:27]
	v_mfma_f32_16x16x32_bf16 v[16:19], v[154:157], v[234:237], v[16:19]
	v_mfma_f32_16x16x32_bf16 v[8:11], v[162:165], v[234:237], v[8:11]
	s_setprio 0
	s_setprio 1
	v_mfma_f32_16x16x32_bf16 v[60:63], v[166:169], v[182:185], v[60:63]
	v_mfma_f32_16x16x32_bf16 v[52:55], v[174:177], v[182:185], v[52:55]
	v_mfma_f32_16x16x32_bf16 v[44:47], v[166:169], v[190:193], v[44:47]
	v_mfma_f32_16x16x32_bf16 v[36:39], v[174:177], v[190:193], v[36:39]
	v_mfma_f32_16x16x32_bf16 v[28:31], v[166:169], v[210:213], v[28:31]
	v_mfma_f32_16x16x32_bf16 v[20:23], v[174:177], v[210:213], v[20:23]
	v_mfma_f32_16x16x32_bf16 v[12:15], v[166:169], v[230:233], v[12:15]
	v_mfma_f32_16x16x32_bf16 v[4:7], v[174:177], v[230:233], v[4:7]
	v_mfma_f32_16x16x32_bf16 v[60:63], v[170:173], v[186:189], v[60:63]
	v_mfma_f32_16x16x32_bf16 v[52:55], v[178:181], v[186:189], v[52:55]
	v_mfma_f32_16x16x32_bf16 v[44:47], v[170:173], v[194:197], v[44:47]
	v_mfma_f32_16x16x32_bf16 v[36:39], v[178:181], v[194:197], v[36:39]
	v_mfma_f32_16x16x32_bf16 v[28:31], v[170:173], v[226:229], v[28:31]
	v_mfma_f32_16x16x32_bf16 v[20:23], v[178:181], v[226:229], v[20:23]
	v_mfma_f32_16x16x32_bf16 v[12:15], v[170:173], v[234:237], v[12:15]
	v_mfma_f32_16x16x32_bf16 v[4:7], v[178:181], v[234:237], v[4:7]
	s_setprio 0
	s_barrier
; #define PG8_STAGE(bufoff, gbase, voff) do { _Pragma("unroll") for (int _i = 0; _i < 2; ++_i) \
;         __builtin_amdgcn_global_load_lds((const unsigned*)((const char*)(gbase) + (voff)[_i]), (PG8_LAS unsigned*)(lds + (bufoff) + ldsw + _i * 8192), 16, 0, 0); } while (0)
; #define PG8_LDA(dst, b, h) do { _Pragma("unroll") for (int m = 0; m < 4; ++m) _Pragma("unroll") for (int k = 0; k < 2; ++k) dst[m][k] = *(const PG8_LAS bf16x8*)(lds + PG8_SA(b, h) + aoff + m * 2048 + k * 1024); } while (0)
; #define PG8_LDB(dst, b, h) do { _Pragma("unroll") for (int n = 0; n < 2; ++n) _Pragma("unroll") for (int k = 0; k < 2; ++k) dst[n][k] = *(const PG8_LAS bf16x8*)(lds + PG8_SB(b, h) + boff + n * 2048 + k * 1024); } while (0)
; #define PG8_MMA(ai, bj, At, Bt) do { __builtin_amdgcn_s_setprio(1); _Pragma("unroll") for (int m = 0; m < 4; ++m) _Pragma("unroll") for (int n = 0; n < 2; ++n) _Pragma("unroll") for (int k = 0; k < 2; ++k) \
;         acc[ai][bj][m][n] = __builtin_amdgcn_mfma_f32_16x16x32_bf16(Bt[n][k], At[m][k], acc[ai][bj][m][n], 0, 0, 0); __builtin_amdgcn_s_setprio(0); } while (0)
; #define PG8_WAIT_V(n) asm volatile("s_waitcnt vmcnt(" #n ")" ::: "memory")
; #define PG8_WAIT_L(n) asm volatile("s_waitcnt lgkmcnt(" #n ")" ::: "memory")
; #define PG8_BAR __builtin_amdgcn_s_barrier()
; #define PG8_SCHED __builtin_amdgcn_sched_barrier(0)
; template <class Epi, class Sched, bool ALIGN_EPI = false, bool SP2 = false>
; __device__ __forceinline__ void gemm_phase(PG8_LAS unsigned char* lds, const Gemm g, const Sched& S, const Epi& E) {
;     ...
;             PG8_LDB(B0, 1, 0); PG8_LDB(B1, 1, 1); PG8_SCHED; PG8_LDA(At, 1, 0); PG8_STAGE(PG8_SA(0, 1), a2 + hstepA, voffA);
;             PG8_WAIT_V(8); PG8_WAIT_L(0); PG8_BAR; PG8_MMA(0, 0, At, B0); PG8_MMA(0, 1, At, B1); PG8_BAR; PG8_SCHED;
	s_add_i32 s54, 0, 0x18000
	s_add_i32 s55, 0, 0x1c000
	v_add_u32_e32 v162, s54, v147
	v_add_u32_e32 v178, s55, v147
	ds_read_b128 v[150:153], v162
	ds_read_b128 v[154:157], v162 offset:1024
	ds_read_b128 v[158:161], v162 offset:2048
	ds_read_b128 v[162:165], v162 offset:3072
	ds_read_b128 v[166:169], v178
	ds_read_b128 v[170:173], v178 offset:1024
	ds_read_b128 v[174:177], v178 offset:2048
	ds_read_b128 v[178:181], v178 offset:3072
	s_add_u32 s26, s26, 0x40000
	s_addc_u32 s27, s27, 0
	s_mov_b32 m0, s43
	v_lshl_add_u64 v[244:245], s[26:27], 0, v[138:139]
	ds_read_b128 v[182:185], v149 offset:32768
	ds_read_b128 v[186:189], v149 offset:33792
	ds_read_b128 v[190:193], v149 offset:34816
	ds_read_b128 v[194:197], v149 offset:35840
	ds_read_b128 v[210:213], v149 offset:36864
	ds_read_b128 v[226:229], v149 offset:37888
	ds_read_b128 v[230:233], v149 offset:38912
	ds_read_b128 v[234:237], v149 offset:39936
	s_mov_b32 m0, s41
	s_nop 0
	global_load_lds_dwordx4 v[240:241], off
	s_mov_b32 m0, s42
	s_nop 0
	global_load_lds_dwordx4 v[242:243], off
	s_mov_b32 m0, s43
	s_nop 0
	global_load_lds_dwordx4 v[244:245], off
	v_lshl_add_u64 v[244:245], s[26:27], 0, v[134:135]
	s_mov_b32 m0, s44
	s_nop 0
	global_load_lds_dwordx4 v[244:245], off
	s_waitcnt vmcnt(8)
	s_waitcnt lgkmcnt(0)
	s_barrier
	s_setprio 1
	s_waitcnt lgkmcnt(0)
	v_mfma_f32_16x16x32_bf16 v[128:131], v[150:153], v[182:185], v[128:131]
	v_mfma_f32_16x16x32_bf16 v[120:123], v[158:161], v[182:185], v[120:123]
	v_mfma_f32_16x16x32_bf16 v[112:115], v[150:153], v[190:193], v[112:115]
	v_mfma_f32_16x16x32_bf16 v[104:107], v[158:161], v[190:193], v[104:107]
	v_mfma_f32_16x16x32_bf16 v[96:99], v[150:153], v[210:213], v[96:99]
	v_mfma_f32_16x16x32_bf16 v[88:91], v[158:161], v[210:213], v[88:91]
	v_mfma_f32_16x16x32_bf16 v[80:83], v[150:153], v[230:233], v[80:83]
	v_mfma_f32_16x16x32_bf16 v[72:75], v[158:161], v[230:233], v[72:75]
	v_mfma_f32_16x16x32_bf16 v[128:131], v[154:157], v[186:189], v[128:131]
	v_mfma_f32_16x16x32_bf16 v[120:123], v[162:165], v[186:189], v[120:123]
	v_mfma_f32_16x16x32_bf16 v[112:115], v[154:157], v[194:197], v[112:115]
	v_mfma_f32_16x16x32_bf16 v[104:107], v[162:165], v[194:197], v[104:107]
	v_mfma_f32_16x16x32_bf16 v[96:99], v[154:157], v[226:229], v[96:99]
	v_mfma_f32_16x16x32_bf16 v[88:91], v[162:165], v[226:229], v[88:91]
	v_mfma_f32_16x16x32_bf16 v[80:83], v[154:157], v[234:237], v[80:83]
	v_mfma_f32_16x16x32_bf16 v[72:75], v[162:165], v[234:237], v[72:75]
	s_setprio 0
	s_setprio 1
	v_mfma_f32_16x16x32_bf16 v[124:127], v[166:169], v[182:185], v[124:127]
	v_mfma_f32_16x16x32_bf16 v[116:119], v[174:177], v[182:185], v[116:119]
	v_mfma_f32_16x16x32_bf16 v[108:111], v[166:169], v[190:193], v[108:111]
	v_mfma_f32_16x16x32_bf16 v[100:103], v[174:177], v[190:193], v[100:103]
	v_mfma_f32_16x16x32_bf16 v[92:95], v[166:169], v[210:213], v[92:95]
	v_mfma_f32_16x16x32_bf16 v[84:87], v[174:177], v[210:213], v[84:87]
	v_mfma_f32_16x16x32_bf16 v[76:79], v[166:169], v[230:233], v[76:79]
	v_mfma_f32_16x16x32_bf16 v[68:71], v[174:177], v[230:233], v[68:71]
	v_mfma_f32_16x16x32_bf16 v[124:127], v[170:173], v[186:189], v[124:127]
	v_mfma_f32_16x16x32_bf16 v[116:119], v[178:181], v[186:189], v[116:119]
	v_mfma_f32_16x16x32_bf16 v[108:111], v[170:173], v[194:197], v[108:111]
	v_mfma_f32_16x16x32_bf16 v[100:103], v[178:181], v[194:197], v[100:103]
	v_mfma_f32_16x16x32_bf16 v[92:95], v[170:173], v[226:229], v[92:95]
	v_mfma_f32_16x16x32_bf16 v[84:87], v[178:181], v[226:229], v[84:87]
	v_mfma_f32_16x16x32_bf16 v[76:79], v[170:173], v[234:237], v[76:79]
	v_mfma_f32_16x16x32_bf16 v[68:71], v[178:181], v[234:237], v[68:71]
	s_setprio 0
	s_barrier
; #define PG8_STAGE(bufoff, gbase, voff) do { _Pragma("unroll") for (int _i = 0; _i < 2; ++_i) \
;         __builtin_amdgcn_global_load_lds((const unsigned*)((const char*)(gbase) + (voff)[_i]), (PG8_LAS unsigned*)(lds + (bufoff) + ldsw + _i * 8192), 16, 0, 0); } while (0)
; #define PG8_LDA(dst, b, h) do { _Pragma("unroll") for (int m = 0; m < 4; ++m) _Pragma("unroll") for (int k = 0; k < 2; ++k) dst[m][k] = *(const PG8_LAS bf16x8*)(lds + PG8_SA(b, h) + aoff + m * 2048 + k * 1024); } while (0)
; #define PG8_MMA(ai, bj, At, Bt) do { __builtin_amdgcn_s_setprio(1); _Pragma("unroll") for (int m = 0; m < 4; ++m) _Pragma("unroll") for (int n = 0; n < 2; ++n) _Pragma("unroll") for (int k = 0; k < 2; ++k) \
;         acc[ai][bj][m][n] = __builtin_amdgcn_mfma_f32_16x16x32_bf16(Bt[n][k], At[m][k], acc[ai][bj][m][n], 0, 0, 0); __builtin_amdgcn_s_setprio(0); } while (0)
; #define PG8_WAIT_V(n) asm volatile("s_waitcnt vmcnt(" #n ")" ::: "memory")
; #define PG8_WAIT_L(n) asm volatile("s_waitcnt lgkmcnt(" #n ")" ::: "memory")
; #define PG8_BAR __builtin_amdgcn_s_barrier()
; #define PG8_SCHED __builtin_amdgcn_sched_barrier(0)
; template <class Epi, class Sched, bool ALIGN_EPI = false, bool SP2 = false>
; __device__ __forceinline__ void gemm_phase(PG8_LAS unsigned char* lds, const Gemm g, const Sched& S, const Epi& E) {
;     ...
;             PG8_WAIT_V(8); PG8_WAIT_L(0); PG8_BAR; PG8_MMA(0, 0, At, B0); PG8_MMA(0, 1, At, B1); PG8_BAR; PG8_SCHED;
;             PG8_LDA(At, 1, 1); PG8_STAGE(PG8_SB(1, 0), b3, voffB); PG8_STAGE(PG8_SB(1, 1), b3 + hstepB, voffB); PG8_STAGE(PG8_SA(1, 0), a3, voffA);
;             PG8_WAIT_V(8); PG8_WAIT_L(0); PG8_BAR; PG8_MMA(1, 0, At, B0); PG8_MMA(1, 1, At, B1); PG8_BAR; PG8_SCHED;
	s_add_i32 s26, s54, s39
	v_lshl_add_u64 v[144:145], v[144:145], 0, s[64:65]
	s_mov_b32 m0, s26
	ds_read_b128 v[182:185], v149 offset:49152
	ds_read_b128 v[186:189], v149 offset:50176
	ds_read_b128 v[190:193], v149 offset:51200
	ds_read_b128 v[194:197], v149 offset:52224
	ds_read_b128 v[210:213], v149 offset:53248
	ds_read_b128 v[226:229], v149 offset:54272
	ds_read_b128 v[230:233], v149 offset:55296
	ds_read_b128 v[234:237], v149 offset:56320
	global_load_lds_dwordx4 v[144:145], off
	s_add_i32 m0, s26, 0x2000
	s_add_u32 s24, s24, 0x40080
	v_lshl_add_u64 v[144:145], v[238:239], 0, s[64:65]
	s_addc_u32 s25, s25, 0
	s_add_i32 s26, s55, s39
	global_load_lds_dwordx4 v[144:145], off
	v_lshl_add_u64 v[144:145], s[24:25], 0, v[136:137]
	s_mov_b32 m0, s26
	s_nop 0
	global_load_lds_dwordx4 v[144:145], off
	v_lshl_add_u64 v[144:145], s[24:25], 0, v[132:133]
	s_add_i32 m0, s26, 0x2000
	s_nop 0
	global_load_lds_dwordx4 v[144:145], off
	s_waitcnt vmcnt(6)
	s_waitcnt lgkmcnt(0)
	s_barrier
	s_setprio 1
	s_waitcnt lgkmcnt(0)
	v_mfma_f32_16x16x32_bf16 v[64:67], v[150:153], v[182:185], v[64:67]
	v_mfma_f32_16x16x32_bf16 v[56:59], v[158:161], v[182:185], v[56:59]
	v_mfma_f32_16x16x32_bf16 v[48:51], v[150:153], v[190:193], v[48:51]
	v_mfma_f32_16x16x32_bf16 v[40:43], v[158:161], v[190:193], v[40:43]
	v_mfma_f32_16x16x32_bf16 v[32:35], v[150:153], v[210:213], v[32:35]
	v_mfma_f32_16x16x32_bf16 v[24:27], v[158:161], v[210:213], v[24:27]
	v_mfma_f32_16x16x32_bf16 v[16:19], v[150:153], v[230:233], v[16:19]
	v_mfma_f32_16x16x32_bf16 v[8:11], v[158:161], v[230:233], v[8:11]
	v_mfma_f32_16x16x32_bf16 v[64:67], v[154:157], v[186:189], v[64:67]
	v_mfma_f32_16x16x32_bf16 v[56:59], v[162:165], v[186:189], v[56:59]
	v_mfma_f32_16x16x32_bf16 v[48:51], v[154:157], v[194:197], v[48:51]
	v_mfma_f32_16x16x32_bf16 v[40:43], v[162:165], v[194:197], v[40:43]
	v_mfma_f32_16x16x32_bf16 v[32:35], v[154:157], v[226:229], v[32:35]
	v_mfma_f32_16x16x32_bf16 v[24:27], v[162:165], v[226:229], v[24:27]
	v_mfma_f32_16x16x32_bf16 v[16:19], v[154:157], v[234:237], v[16:19]
	v_mfma_f32_16x16x32_bf16 v[8:11], v[162:165], v[234:237], v[8:11]
	s_setprio 0
	s_setprio 1
	v_mfma_f32_16x16x32_bf16 v[60:63], v[166:169], v[182:185], v[60:63]
	v_mfma_f32_16x16x32_bf16 v[52:55], v[174:177], v[182:185], v[52:55]
	v_mfma_f32_16x16x32_bf16 v[44:47], v[166:169], v[190:193], v[44:47]
	v_mfma_f32_16x16x32_bf16 v[36:39], v[174:177], v[190:193], v[36:39]
	v_mfma_f32_16x16x32_bf16 v[28:31], v[166:169], v[210:213], v[28:31]
	v_mfma_f32_16x16x32_bf16 v[20:23], v[174:177], v[210:213], v[20:23]
	v_mfma_f32_16x16x32_bf16 v[12:15], v[166:169], v[230:233], v[12:15]
	v_mfma_f32_16x16x32_bf16 v[4:7], v[174:177], v[230:233], v[4:7]
	v_mfma_f32_16x16x32_bf16 v[60:63], v[170:173], v[186:189], v[60:63]
	v_mfma_f32_16x16x32_bf16 v[52:55], v[178:181], v[186:189], v[52:55]
	v_mfma_f32_16x16x32_bf16 v[44:47], v[170:173], v[194:197], v[44:47]
	v_mfma_f32_16x16x32_bf16 v[36:39], v[178:181], v[194:197], v[36:39]
	v_mfma_f32_16x16x32_bf16 v[28:31], v[170:173], v[226:229], v[28:31]
	v_mfma_f32_16x16x32_bf16 v[20:23], v[178:181], v[226:229], v[20:23]
	v_mfma_f32_16x16x32_bf16 v[12:15], v[170:173], v[234:237], v[12:15]
	v_mfma_f32_16x16x32_bf16 v[4:7], v[178:181], v[234:237], v[4:7]
	s_setprio 0
	s_barrier
	s_add_i32 s53, s53, 2
	s_add_u32 s51, s51, 0x100
	s_addc_u32 s52, s52, 0
	s_add_u32 s22, s22, 0x100
	s_addc_u32 s23, s23, 0
	s_cmp_gt_u32 s53, 13
	s_cbranch_scc0 .LBB0_153

; #define PG8_WAIT_V(n) asm volatile("s_waitcnt vmcnt(" #n ")" ::: "memory")
;     __host__ __device__ bool next(int i, Unit& u) const {
;         const long L = (long)i * G + c; if (L >= nwg) return false;
;         int wgid = (int)L; { const int q = nwg / NXCD, r = nwg % NXCD, xcd = wgid % NXCD, off = wgid / NXCD; wgid = (xcd < r ? xcd * (q + 1) : r * (q + 1) + (xcd - r) * q) + off; }
;         const int nig = WGM * nN, gid = wgid / nig, fm = gid * WGM, gsz = (nM - fm) < WGM ? (nM - fm) : WGM;
;         u.pm = fm + ((wgid % nig) % gsz); u.pn = (wgid % nig) / gsz; return true;
; template <class Epi, class Sched, bool ALIGN_EPI = false, bool SP2 = false>
; __device__ __forceinline__ void gemm_phase(PG8_LAS unsigned char* lds, const Gemm g, const Sched& S, const Epi& E) {
;     ...
;     for (int i = 0; i < 2; ++i) { int R, C; stage_rc(tid * 16 + i * 8192, R, C); const int Rb = Epi::PERM ? ((R & ~31) + perm32(R & 31)) : R;
;         voffA[i] = (unsigned)(R * g.lda + C) * 2u; voffB[i] = (unsigned)(Rb * g.ldb + C) * 2u; }
;     const size_t kstep = (size_t)(BK * 2);
;     const size_t hstepA = (size_t)HALF * g.lda * 2, hstepB = (size_t)HALF * g.ldb * 2;
;     const size_t tstepA = 2 * hstepA, tstepB = 2 * hstepB;
;     const unsigned ldsw = (unsigned)wid * 1024u;
;     const int aoff = lds_byte(wr * 64 + fr, fq * 8), boff = lds_byte(wc * 32 + fr, fq * 8);
;     ...
;     Unit cur, nxt; int ui = 0;
;     if (!S.next(0, cur)) return;
;     f32x4 acc[2][2][4][2];
; #pragma unroll
;     for (int a = 0; a < 2; ++a)
; #pragma unroll
;         for (int b = 0; b < 2; ++b)
; #pragma unroll
;             for (int m = 0; m < 4; ++m)
; #pragma unroll
;                 for (int n = 0; n < 2; ++n) acc[a][b][m][n] = (f32x4){0.f, 0.f, 0.f, 0.f};
;     bf16x8 At[4][2], B0[2][2], B1[2][2];
;     const char* cA = (const char*)g.A + (size_t)cur.pm * tstepA; const char* cB = (const char*)g.Bt + (size_t)cur.pn * tstepB;
;     S.a_ready(cur);
;     if constexpr (SP2) {
;         PG8_STAGE(PG8_SB(0, 0), cB, voffB); PG8_STAGE(PG8_SB(0, 1), cB + hstepB, voffB); PG8_STAGE(PG8_SA(0, 0), cA, voffA); PG8_STAGE(PG8_SA(0, 1), cA + hstepA, voffA);
;         if (wr == 1) PG8_BAR;
;         PG8_WAIT_V(2); PG8_BAR;
;         PG8_STAGE(PG8_SB(1, 0), cB + kstep, voffB); PG8_STAGE(PG8_SA(1, 0), cA + kstep, voffA); PG8_STAGE(PG8_SB(1, 1), cB + hstepB + kstep, voffB);
;         PG8_WAIT_V(6); PG8_BAR;
;     } else {
.LBB0_653:
	v_ashrrev_i32_e32 v4, 31, v20
	v_lshrrev_b32_e32 v4, 26, v4
	v_add_u32_e32 v4, v20, v4
	v_ashrrev_i32_e32 v12, 6, v4
	v_bfe_i32 v4, v20, 27, 1
	v_lshlrev_b32_e32 v2, 4, v20
	v_lshrrev_b32_e32 v4, 22, v4
	v_add_u32_e32 v4, v2, v4
	v_and_b32_e32 v4, 0xfffffc00, v4
	v_sub_u32_e32 v4, v2, v4
	v_lshrrev_b32_e32 v5, 4, v4
	v_bitop3_b32 v4, v5, v4, 32 bitop3:0x6c
	v_readlane_b32 s4, v253, 55
	v_ashrrev_i32_e32 v6, 31, v4
	v_readlane_b32 s5, v253, 56
	s_mul_i32 s68, s4, 0x2c0000
	s_add_u32 s23, s2, 0x11000000
	v_lshrrev_b32_e32 v6, 26, v6
	s_addc_u32 s24, s3, 0
	s_lshl_b64 s[4:5], s[68:69], 1
	v_lshlrev_b32_e32 v5, 3, v12
	v_add_u32_e32 v6, v4, v6
	s_add_u32 s4, s2, s4
	v_and_b32_e32 v5, -16, v5
	v_ashrrev_i32_e32 v14, 6, v6
	v_and_b32_e32 v6, 0xc0, v6
	s_addc_u32 s5, s3, s5
	v_add_u32_e32 v5, v14, v5
	v_lshlrev_b32_e32 v7, 5, v12
	v_sub_u32_e32 v4, v4, v6
	s_add_u32 s25, s4, 0x6000000
	v_and_b32_e32 v13, 32, v7
	v_ashrrev_i16_sdwa v4, v1, sext(v4) dst_sel:DWORD dst_unused:UNUSED_PAD src0_sel:DWORD src1_sel:BYTE_0
	v_lshlrev_b32_e32 v6, 1, v5
	v_lshrrev_b32_e32 v7, 2, v5
	v_and_b32_e32 v8, 3, v14
	s_mov_b32 s8, 0xffffe0
	s_addc_u32 s26, s5, 0
	v_bfe_i32 v15, v4, 0, 16
	v_and_b32_e32 v6, 24, v6
	v_and_b32_e32 v7, 4, v7
	v_and_or_b32 v8, v5, s8, v8
	s_movk_i32 s5, 0xb00
	v_add_u32_e32 v4, v13, v15
	v_or3_b32 v6, v8, v7, v6
	v_mul_lo_u32 v5, v5, s5
	v_add_lshl_u32 v132, v4, v5, 1
	v_mul_u32_u24_e32 v5, 0xb00, v6
	v_add_u32_e32 v2, 0x2000, v2
	v_add_lshl_u32 v134, v5, v4, 1
	v_ashrrev_i32_e32 v4, 31, v2
	v_lshrrev_b32_e32 v4, 22, v4
	v_add_u32_e32 v4, v2, v4
	v_ashrrev_i32_e32 v16, 10, v4
	v_mul_i32_i24_e32 v4, 0x400, v16
	v_sub_u32_e32 v2, v2, v4
	v_lshrrev_b32_e32 v4, 4, v2
	v_bitop3_b32 v2, v4, v2, 32 bitop3:0x6c
	v_ashrrev_i32_e32 v5, 31, v2
	v_lshrrev_b32_e32 v5, 26, v5
	s_add_i32 s6, s6, s7
	v_lshlrev_b32_e32 v4, 3, v16
	v_add_u32_e32 v5, v2, v5
	s_ashr_i32 s7, s6, 31
	v_and_b32_e32 v4, -16, v4
	v_ashrrev_i32_e32 v18, 6, v5
	s_lshr_b32 s7, s7, 27
	v_add_u32_e32 v4, v18, v4
	v_and_b32_e32 v7, 3, v18
	s_add_i32 s7, s6, s7
	v_and_or_b32 v7, v4, s8, v7
	s_ashr_i32 s8, s7, 5
	s_and_b32 s7, s7, 0xffe0
	s_sub_i32 s6, s6, s7
	s_bfe_i32 s7, s6, 0x80000
	s_bfe_u32 s7, s7, 0x3000c
	s_add_i32 s7, s6, s7
	s_lshl_b32 s9, s8, 3
	s_bfe_i32 s8, s7, 0x80000
	s_and_b32 s7, s7, 0xf8
	s_sub_i32 s6, s6, s7
	s_sext_i32_i16 s11, s8
	s_sext_i32_i8 s6, s6
	s_ashr_i32 s4, s10, 6
	v_lshlrev_b32_e32 v6, 5, v16
	v_and_b32_e32 v5, 0xc0, v5
	s_add_i32 s42, s9, s6
	s_ashr_i32 s6, s11, 3
	v_and_b32_e32 v17, 32, v6
	v_sub_u32_e32 v2, v2, v5
	v_lshlrev_b32_e32 v5, 1, v4
	v_lshrrev_b32_e32 v6, 2, v4
	v_mul_lo_u32 v4, v4, s5
	s_ashr_i32 s5, s10, 8
	s_lshl_b32 s27, s4, 10
	s_lshr_b32 s8, s11, 3
	s_mul_hi_i32 s7, s6, 0x160000
	s_mul_i32 s6, s6, 0x160000
	v_ashrrev_i16_sdwa v2, v1, sext(v2) dst_sel:DWORD dst_unused:UNUSED_PAD src0_sel:DWORD src1_sel:BYTE_0
	s_add_u32 s16, s25, s6
	v_bfe_i32 v19, v2, 0, 16
	v_and_b32_e32 v5, 24, v5
	v_and_b32_e32 v6, 4, v6
	s_addc_u32 s17, s26, s7
	s_add_i32 s28, s27, 0
	v_add_u32_e32 v2, v17, v19
	v_or3_b32 v5, v7, v6, v5
	s_add_i32 m0, s28, 0x10000
	v_add_lshl_u32 v136, v2, v4, 1
	v_mul_u32_u24_e32 v4, 0xb00, v5
	global_load_lds_dwordx4 v134, s[16:17]
	s_add_i32 m0, s28, 0x12000
	v_add_lshl_u32 v138, v4, v2, 1
	s_add_u32 s6, s16, 0xb0000
	global_load_lds_dwordx4 v138, s[16:17]
	s_addc_u32 s7, s17, 0
	s_add_i32 m0, s28, 0x14000
	s_mul_i32 s12, s42, 0x160000
	global_load_lds_dwordx4 v134, s[6:7]
	s_add_i32 m0, s28, 0x16000
	s_mul_hi_i32 s9, s42, 0x160000
	s_add_u32 s14, s23, s12
	s_addc_u32 s15, s24, s9
	s_add_i32 s29, s28, 0x2000
	global_load_lds_dwordx4 v138, s[6:7]
	s_mov_b32 m0, s28
	s_add_u32 s6, s14, 0xb0000
	global_load_lds_dwordx4 v132, s[14:15]
	s_mov_b32 m0, s29
	s_addc_u32 s7, s15, 0
	s_add_i32 s30, s28, 0x4000
	global_load_lds_dwordx4 v136, s[14:15]
	s_mov_b32 m0, s30
	s_add_i32 s31, s28, 0x6000
	global_load_lds_dwordx4 v132, s[6:7]
	s_mov_b32 m0, s31
	v_mov_b32_e32 v135, v3
	global_load_lds_dwordx4 v136, s[6:7]
	v_mov_b32_e32 v139, v3
	v_mov_b32_e32 v133, v3
	v_mov_b32_e32 v137, v3
	s_cmp_eq_u32 s5, 1
	v_lshl_add_u64 v[10:11], s[16:17], 0, v[134:135]
	v_lshl_add_u64 v[8:9], s[16:17], 0, v[138:139]
	v_lshl_add_u64 v[4:5], s[14:15], 0, v[132:133]
	s_cselect_b64 s[6:7], -1, 0
	s_cmp_lg_u32 s5, 1
	v_lshl_add_u64 v[6:7], s[14:15], 0, v[136:137]
	v_lshl_add_u64 v[240:241], s[14:15], 0, v[132:133]
	v_lshl_add_u64 v[242:243], s[14:15], 0, v[136:137]
	s_cbranch_scc1 .LBB0_655
	s_barrier

; #define PG8_STAGE(bufoff, gbase, voff) do { _Pragma("unroll") for (int _i = 0; _i < 2; ++_i) \
;         __builtin_amdgcn_global_load_lds((const unsigned*)((const char*)(gbase) + (voff)[_i]), (PG8_LAS unsigned*)(lds + (bufoff) + ldsw + _i * 8192), 16, 0, 0); } while (0)
; #define PG8_LDA(dst, b, h) do { _Pragma("unroll") for (int m = 0; m < 4; ++m) _Pragma("unroll") for (int k = 0; k < 2; ++k) dst[m][k] = *(const PG8_LAS bf16x8*)(lds + PG8_SA(b, h) + aoff + m * 2048 + k * 1024); } while (0)
; #define PG8_LDB(dst, b, h) do { _Pragma("unroll") for (int n = 0; n < 2; ++n) _Pragma("unroll") for (int k = 0; k < 2; ++k) dst[n][k] = *(const PG8_LAS bf16x8*)(lds + PG8_SB(b, h) + boff + n * 2048 + k * 1024); } while (0)
; #define PG8_MMA(ai, bj, At, Bt) do { __builtin_amdgcn_s_setprio(1); _Pragma("unroll") for (int m = 0; m < 4; ++m) _Pragma("unroll") for (int n = 0; n < 2; ++n) _Pragma("unroll") for (int k = 0; k < 2; ++k) \
;         acc[ai][bj][m][n] = __builtin_amdgcn_mfma_f32_16x16x32_bf16(Bt[n][k], At[m][k], acc[ai][bj][m][n], 0, 0, 0); __builtin_amdgcn_s_setprio(0); } while (0)
; #define PG8_WAIT_V(n) asm volatile("s_waitcnt vmcnt(" #n ")" ::: "memory")
; #define PG8_WAIT_L(n) asm volatile("s_waitcnt lgkmcnt(" #n ")" ::: "memory")
; #define PG8_BAR __builtin_amdgcn_s_barrier()
; #define PG8_SCHED __builtin_amdgcn_sched_barrier(0)
; template <class Epi, class Sched, bool ALIGN_EPI = false, bool SP2 = false>
; __device__ __forceinline__ void gemm_phase(PG8_LAS unsigned char* lds, const Gemm g, const Sched& S, const Epi& E) {
;     ...
;             PG8_LDB(B0, 0, 0); PG8_LDB(B1, 0, 1); PG8_SCHED; PG8_LDA(At, 0, 0); PG8_STAGE(PG8_SA(1, 1), a1 + hstepA, voffA);
;             PG8_WAIT_V(8); PG8_WAIT_L(0); PG8_BAR; PG8_MMA(0, 0, At, B0); PG8_MMA(0, 1, At, B1); PG8_BAR; PG8_SCHED;
;             PG8_LDA(At, 0, 1); PG8_STAGE(PG8_SB(0, 0), b2, voffB); PG8_STAGE(PG8_SB(0, 1), b2 + hstepB, voffB); PG8_STAGE(PG8_SA(0, 0), a2, voffA);
;             PG8_WAIT_V(8); PG8_WAIT_L(0); PG8_BAR; PG8_MMA(1, 0, At, B0); PG8_MMA(1, 1, At, B1); PG8_BAR; PG8_SCHED;
.LBB0_669:
	s_add_u32 s16, s14, 0x100
	s_addc_u32 s17, s15, 0
	s_add_i32 s47, 0, 0x10000
	s_cmp_eq_u32 s46, 40
	s_cselect_b32 s21, s5, s17
	s_cselect_b32 s20, s4, s16
	v_add_u32_e32 v144, s47, v146
	s_cselect_b32 s19, s13, s45
	s_cselect_b32 s18, s12, s44
	s_add_i32 s48, 0, 0x14000
	ds_read_b128 v[150:153], v144
	ds_read_b128 v[154:157], v144 offset:1024
	ds_read_b128 v[158:161], v144 offset:2048
	ds_read_b128 v[162:165], v144 offset:3072
	v_add_u32_e32 v144, s48, v146
	ds_read_b128 v[166:169], v144
	ds_read_b128 v[170:173], v144 offset:1024
	ds_read_b128 v[174:177], v144 offset:2048
	ds_read_b128 v[178:181], v144 offset:3072
	v_lshl_add_u64 v[144:145], s[14:15], 0, v[142:143]
	s_add_i32 m0, s28, 0xc000
	ds_read_b128 v[182:185], v148
	ds_read_b128 v[186:189], v148 offset:1024
	ds_read_b128 v[190:193], v148 offset:2048
	ds_read_b128 v[194:197], v148 offset:3072
	ds_read_b128 v[210:213], v148 offset:4096
	ds_read_b128 v[226:229], v148 offset:5120
	ds_read_b128 v[230:233], v148 offset:6144
	ds_read_b128 v[234:237], v148 offset:7168
	v_lshl_add_u64 v[244:245], v[240:241], 0, s[64:65]
	s_mov_b32 m0, s33
	s_nop 0
	global_load_lds_dwordx4 v[244:245], off
	v_lshl_add_u64 v[244:245], v[242:243], 0, s[64:65]
	s_mov_b32 m0, s34
	s_nop 0
	global_load_lds_dwordx4 v[244:245], off
	s_add_i32 m0, s28, 0xc000
	s_nop 0
	global_load_lds_dwordx4 v[144:145], off
	v_lshl_add_u64 v[144:145], s[14:15], 0, v[140:141]
	s_add_i32 m0, s28, 0xe000
	s_nop 0
	global_load_lds_dwordx4 v[144:145], off
	s_waitcnt vmcnt(8)
	s_waitcnt lgkmcnt(0)
	s_barrier
	s_setprio 1
	s_waitcnt lgkmcnt(0)
	v_mfma_f32_16x16x32_bf16 v[128:131], v[150:153], v[182:185], v[128:131]
	v_mfma_f32_16x16x32_bf16 v[124:127], v[158:161], v[182:185], v[124:127]
	v_mfma_f32_16x16x32_bf16 v[120:123], v[150:153], v[190:193], v[120:123]
	v_mfma_f32_16x16x32_bf16 v[112:115], v[158:161], v[190:193], v[112:115]
	v_mfma_f32_16x16x32_bf16 v[104:107], v[150:153], v[210:213], v[104:107]
	v_mfma_f32_16x16x32_bf16 v[96:99], v[158:161], v[210:213], v[96:99]
	v_mfma_f32_16x16x32_bf16 v[88:91], v[150:153], v[230:233], v[88:91]
	v_mfma_f32_16x16x32_bf16 v[80:83], v[158:161], v[230:233], v[80:83]
	v_mfma_f32_16x16x32_bf16 v[128:131], v[154:157], v[186:189], v[128:131]
	v_mfma_f32_16x16x32_bf16 v[124:127], v[162:165], v[186:189], v[124:127]
	v_mfma_f32_16x16x32_bf16 v[120:123], v[154:157], v[194:197], v[120:123]
	v_mfma_f32_16x16x32_bf16 v[112:115], v[162:165], v[194:197], v[112:115]
	v_mfma_f32_16x16x32_bf16 v[104:107], v[154:157], v[226:229], v[104:107]
	v_mfma_f32_16x16x32_bf16 v[96:99], v[162:165], v[226:229], v[96:99]
	v_mfma_f32_16x16x32_bf16 v[88:91], v[154:157], v[234:237], v[88:91]
	v_mfma_f32_16x16x32_bf16 v[80:83], v[162:165], v[234:237], v[80:83]
	s_setprio 0
	s_setprio 1
	v_mfma_f32_16x16x32_bf16 v[116:119], v[166:169], v[182:185], v[116:119]
	v_mfma_f32_16x16x32_bf16 v[108:111], v[174:177], v[182:185], v[108:111]
	v_mfma_f32_16x16x32_bf16 v[100:103], v[166:169], v[190:193], v[100:103]
	v_mfma_f32_16x16x32_bf16 v[92:95], v[174:177], v[190:193], v[92:95]
	v_mfma_f32_16x16x32_bf16 v[84:87], v[166:169], v[210:213], v[84:87]
	v_mfma_f32_16x16x32_bf16 v[76:79], v[174:177], v[210:213], v[76:79]
	v_mfma_f32_16x16x32_bf16 v[72:75], v[166:169], v[230:233], v[72:75]
	v_mfma_f32_16x16x32_bf16 v[68:71], v[174:177], v[230:233], v[68:71]
	v_mfma_f32_16x16x32_bf16 v[116:119], v[170:173], v[186:189], v[116:119]
	v_mfma_f32_16x16x32_bf16 v[108:111], v[178:181], v[186:189], v[108:111]
	v_mfma_f32_16x16x32_bf16 v[100:103], v[170:173], v[194:197], v[100:103]
	v_mfma_f32_16x16x32_bf16 v[92:95], v[178:181], v[194:197], v[92:95]
	v_mfma_f32_16x16x32_bf16 v[84:87], v[170:173], v[226:229], v[84:87]
	v_mfma_f32_16x16x32_bf16 v[76:79], v[178:181], v[226:229], v[76:79]
	v_mfma_f32_16x16x32_bf16 v[72:75], v[170:173], v[234:237], v[72:75]
	v_mfma_f32_16x16x32_bf16 v[68:71], v[178:181], v[234:237], v[68:71]
	s_setprio 0
	s_barrier
	s_add_i32 s14, s47, s27
	v_lshl_add_u64 v[144:145], s[18:19], 0, v[134:135]
	s_mov_b32 m0, s14
	ds_read_b128 v[182:185], v148 offset:16384
	ds_read_b128 v[186:189], v148 offset:17408
	ds_read_b128 v[190:193], v148 offset:18432
	ds_read_b128 v[194:197], v148 offset:19456
	ds_read_b128 v[210:213], v148 offset:20480
	ds_read_b128 v[226:229], v148 offset:21504
	ds_read_b128 v[230:233], v148 offset:22528
	ds_read_b128 v[234:237], v148 offset:23552
	global_load_lds_dwordx4 v[144:145], off
	s_add_i32 m0, s14, 0x2000
	s_add_u32 s14, s18, 0xb0000
	v_lshl_add_u64 v[238:239], s[18:19], 0, v[138:139]
	s_addc_u32 s15, s19, 0
	s_add_i32 s47, s48, s27
	global_load_lds_dwordx4 v[238:239], off
	v_lshl_add_u64 v[240:241], s[14:15], 0, v[134:135]
	s_mov_b32 m0, s47
	v_lshl_add_u64 v[242:243], s[20:21], 0, v[136:137]
	global_load_lds_dwordx4 v[240:241], off
	v_lshl_add_u64 v[240:241], s[14:15], 0, v[138:139]
	s_add_i32 m0, s47, 0x2000
	s_nop 0
	global_load_lds_dwordx4 v[240:241], off
	v_lshl_add_u64 v[240:241], s[20:21], 0, v[132:133]
	s_waitcnt vmcnt(6)
	s_waitcnt lgkmcnt(0)
	s_barrier
; #define PG8_STAGE(bufoff, gbase, voff) do { _Pragma("unroll") for (int _i = 0; _i < 2; ++_i) \
;         __builtin_amdgcn_global_load_lds((const unsigned*)((const char*)(gbase) + (voff)[_i]), (PG8_LAS unsigned*)(lds + (bufoff) + ldsw + _i * 8192), 16, 0, 0); } while (0)
; #define PG8_LDA(dst, b, h) do { _Pragma("unroll") for (int m = 0; m < 4; ++m) _Pragma("unroll") for (int k = 0; k < 2; ++k) dst[m][k] = *(const PG8_LAS bf16x8*)(lds + PG8_SA(b, h) + aoff + m * 2048 + k * 1024); } while (0)
; #define PG8_LDB(dst, b, h) do { _Pragma("unroll") for (int n = 0; n < 2; ++n) _Pragma("unroll") for (int k = 0; k < 2; ++k) dst[n][k] = *(const PG8_LAS bf16x8*)(lds + PG8_SB(b, h) + boff + n * 2048 + k * 1024); } while (0)
; #define PG8_MMA(ai, bj, At, Bt) do { __builtin_amdgcn_s_setprio(1); _Pragma("unroll") for (int m = 0; m < 4; ++m) _Pragma("unroll") for (int n = 0; n < 2; ++n) _Pragma("unroll") for (int k = 0; k < 2; ++k) \
;         acc[ai][bj][m][n] = __builtin_amdgcn_mfma_f32_16x16x32_bf16(Bt[n][k], At[m][k], acc[ai][bj][m][n], 0, 0, 0); __builtin_amdgcn_s_setprio(0); } while (0)
; #define PG8_WAIT_V(n) asm volatile("s_waitcnt vmcnt(" #n ")" ::: "memory")
; #define PG8_WAIT_L(n) asm volatile("s_waitcnt lgkmcnt(" #n ")" ::: "memory")
; #define PG8_BAR __builtin_amdgcn_s_barrier()
; #define PG8_SCHED __builtin_amdgcn_sched_barrier(0)
; template <class Epi, class Sched, bool ALIGN_EPI = false, bool SP2 = false>
; __device__ __forceinline__ void gemm_phase(PG8_LAS unsigned char* lds, const Gemm g, const Sched& S, const Epi& E) {
;     ...
;             PG8_WAIT_V(8); PG8_WAIT_L(0); PG8_BAR; PG8_MMA(1, 0, At, B0); PG8_MMA(1, 1, At, B1); PG8_BAR; PG8_SCHED;
;             PG8_LDB(B0, 1, 0); PG8_LDB(B1, 1, 1); PG8_SCHED; PG8_LDA(At, 1, 0); PG8_STAGE(PG8_SA(0, 1), a2 + hstepA, voffA);
;             PG8_WAIT_V(8); PG8_WAIT_L(0); PG8_BAR; PG8_MMA(0, 0, At, B0); PG8_MMA(0, 1, At, B1); PG8_BAR; PG8_SCHED;
	s_setprio 1
	s_waitcnt lgkmcnt(0)
	v_mfma_f32_16x16x32_bf16 v[64:67], v[150:153], v[182:185], v[64:67]
	v_mfma_f32_16x16x32_bf16 v[60:63], v[158:161], v[182:185], v[60:63]
	v_mfma_f32_16x16x32_bf16 v[56:59], v[150:153], v[190:193], v[56:59]
	v_mfma_f32_16x16x32_bf16 v[48:51], v[158:161], v[190:193], v[48:51]
	v_mfma_f32_16x16x32_bf16 v[40:43], v[150:153], v[210:213], v[40:43]
	v_mfma_f32_16x16x32_bf16 v[32:35], v[158:161], v[210:213], v[32:35]
	v_mfma_f32_16x16x32_bf16 v[24:27], v[150:153], v[230:233], v[24:27]
	v_mfma_f32_16x16x32_bf16 v[16:19], v[158:161], v[230:233], v[16:19]
	v_mfma_f32_16x16x32_bf16 v[64:67], v[154:157], v[186:189], v[64:67]
	v_mfma_f32_16x16x32_bf16 v[60:63], v[162:165], v[186:189], v[60:63]
	v_mfma_f32_16x16x32_bf16 v[56:59], v[154:157], v[194:197], v[56:59]
	v_mfma_f32_16x16x32_bf16 v[48:51], v[162:165], v[194:197], v[48:51]
	v_mfma_f32_16x16x32_bf16 v[40:43], v[154:157], v[226:229], v[40:43]
	v_mfma_f32_16x16x32_bf16 v[32:35], v[162:165], v[226:229], v[32:35]
	v_mfma_f32_16x16x32_bf16 v[24:27], v[154:157], v[234:237], v[24:27]
	v_mfma_f32_16x16x32_bf16 v[16:19], v[162:165], v[234:237], v[16:19]
	s_setprio 0
	s_setprio 1
	v_mfma_f32_16x16x32_bf16 v[52:55], v[166:169], v[182:185], v[52:55]
	v_mfma_f32_16x16x32_bf16 v[44:47], v[174:177], v[182:185], v[44:47]
	v_mfma_f32_16x16x32_bf16 v[36:39], v[166:169], v[190:193], v[36:39]
	v_mfma_f32_16x16x32_bf16 v[28:31], v[174:177], v[190:193], v[28:31]
	v_mfma_f32_16x16x32_bf16 v[20:23], v[166:169], v[210:213], v[20:23]
	v_mfma_f32_16x16x32_bf16 v[12:15], v[174:177], v[210:213], v[12:15]
	v_mfma_f32_16x16x32_bf16 v[8:11], v[166:169], v[230:233], v[8:11]
	v_mfma_f32_16x16x32_bf16 v[4:7], v[174:177], v[230:233], v[4:7]
	v_mfma_f32_16x16x32_bf16 v[52:55], v[170:173], v[186:189], v[52:55]
	v_mfma_f32_16x16x32_bf16 v[44:47], v[178:181], v[186:189], v[44:47]
	v_mfma_f32_16x16x32_bf16 v[36:39], v[170:173], v[194:197], v[36:39]
	v_mfma_f32_16x16x32_bf16 v[28:31], v[178:181], v[194:197], v[28:31]
	v_mfma_f32_16x16x32_bf16 v[20:23], v[170:173], v[226:229], v[20:23]
	v_mfma_f32_16x16x32_bf16 v[12:15], v[178:181], v[226:229], v[12:15]
	v_mfma_f32_16x16x32_bf16 v[8:11], v[170:173], v[234:237], v[8:11]
	v_mfma_f32_16x16x32_bf16 v[4:7], v[178:181], v[234:237], v[4:7]
	s_setprio 0
	s_barrier
	s_add_i32 s47, 0, 0x18000
	v_add_u32_e32 v149, s47, v146
	s_add_i32 s48, 0, 0x1c000
	ds_read_b128 v[150:153], v149
	ds_read_b128 v[154:157], v149 offset:1024
	ds_read_b128 v[158:161], v149 offset:2048
	ds_read_b128 v[162:165], v149 offset:3072
	v_add_u32_e32 v149, s48, v146
	ds_read_b128 v[166:169], v149
	ds_read_b128 v[170:173], v149 offset:1024
	ds_read_b128 v[174:177], v149 offset:2048
	ds_read_b128 v[178:181], v149 offset:3072
	s_add_u32 s14, s20, 0xb0000
	s_addc_u32 s15, s21, 0
	s_mov_b32 m0, s30
	v_lshl_add_u64 v[244:245], s[14:15], 0, v[132:133]
	ds_read_b128 v[182:185], v148 offset:32768
	ds_read_b128 v[186:189], v148 offset:33792
	ds_read_b128 v[190:193], v148 offset:34816
	ds_read_b128 v[194:197], v148 offset:35840
	ds_read_b128 v[210:213], v148 offset:36864
	ds_read_b128 v[226:229], v148 offset:37888
	ds_read_b128 v[230:233], v148 offset:38912
	ds_read_b128 v[234:237], v148 offset:39936
	s_mov_b32 m0, s28
	s_nop 0
	global_load_lds_dwordx4 v[240:241], off
	s_mov_b32 m0, s29
	s_nop 0
	global_load_lds_dwordx4 v[242:243], off
	s_mov_b32 m0, s30
	s_nop 0
	global_load_lds_dwordx4 v[244:245], off
	v_lshl_add_u64 v[244:245], s[14:15], 0, v[136:137]
	s_mov_b32 m0, s31
	s_nop 0
	global_load_lds_dwordx4 v[244:245], off
	s_waitcnt vmcnt(8)
	s_waitcnt lgkmcnt(0)
	s_barrier
; #define PG8_STAGE(bufoff, gbase, voff) do { _Pragma("unroll") for (int _i = 0; _i < 2; ++_i) \
;         __builtin_amdgcn_global_load_lds((const unsigned*)((const char*)(gbase) + (voff)[_i]), (PG8_LAS unsigned*)(lds + (bufoff) + ldsw + _i * 8192), 16, 0, 0); } while (0)
; #define PG8_LDA(dst, b, h) do { _Pragma("unroll") for (int m = 0; m < 4; ++m) _Pragma("unroll") for (int k = 0; k < 2; ++k) dst[m][k] = *(const PG8_LAS bf16x8*)(lds + PG8_SA(b, h) + aoff + m * 2048 + k * 1024); } while (0)
; #define PG8_LDB(dst, b, h) do { _Pragma("unroll") for (int n = 0; n < 2; ++n) _Pragma("unroll") for (int k = 0; k < 2; ++k) dst[n][k] = *(const PG8_LAS bf16x8*)(lds + PG8_SB(b, h) + boff + n * 2048 + k * 1024); } while (0)
; #define PG8_MMA(ai, bj, At, Bt) do { __builtin_amdgcn_s_setprio(1); _Pragma("unroll") for (int m = 0; m < 4; ++m) _Pragma("unroll") for (int n = 0; n < 2; ++n) _Pragma("unroll") for (int k = 0; k < 2; ++k) \
;         acc[ai][bj][m][n] = __builtin_amdgcn_mfma_f32_16x16x32_bf16(Bt[n][k], At[m][k], acc[ai][bj][m][n], 0, 0, 0); __builtin_amdgcn_s_setprio(0); } while (0)
; #define PG8_WAIT_V(n) asm volatile("s_waitcnt vmcnt(" #n ")" ::: "memory")
; #define PG8_WAIT_L(n) asm volatile("s_waitcnt lgkmcnt(" #n ")" ::: "memory")
; #define PG8_BAR __builtin_amdgcn_s_barrier()
; #define PG8_SCHED __builtin_amdgcn_sched_barrier(0)
; template <class Epi, class Sched, bool ALIGN_EPI = false, bool SP2 = false>
; __device__ __forceinline__ void gemm_phase(PG8_LAS unsigned char* lds, const Gemm g, const Sched& S, const Epi& E) {
;     ...
;             PG8_LDB(B0, 1, 0); PG8_LDB(B1, 1, 1); PG8_SCHED; PG8_LDA(At, 1, 0); PG8_STAGE(PG8_SA(0, 1), a2 + hstepA, voffA);
;             PG8_WAIT_V(8); PG8_WAIT_L(0); PG8_BAR; PG8_MMA(0, 0, At, B0); PG8_MMA(0, 1, At, B1); PG8_BAR; PG8_SCHED;
;             PG8_LDA(At, 1, 1); PG8_STAGE(PG8_SB(1, 0), b3, voffB); PG8_STAGE(PG8_SB(1, 1), b3 + hstepB, voffB); PG8_STAGE(PG8_SA(1, 0), a3, voffA);
;             PG8_WAIT_V(8); PG8_WAIT_L(0); PG8_BAR; PG8_MMA(1, 0, At, B0); PG8_MMA(1, 1, At, B1); PG8_BAR; PG8_SCHED;
;     ...
;         if constexpr (ALIGN_EPI) { if (wr == 0) PG8_BAR; }
	s_setprio 1
	s_waitcnt lgkmcnt(0)
	v_mfma_f32_16x16x32_bf16 v[128:131], v[150:153], v[182:185], v[128:131]
	v_mfma_f32_16x16x32_bf16 v[124:127], v[158:161], v[182:185], v[124:127]
	v_mfma_f32_16x16x32_bf16 v[120:123], v[150:153], v[190:193], v[120:123]
	v_mfma_f32_16x16x32_bf16 v[112:115], v[158:161], v[190:193], v[112:115]
	v_mfma_f32_16x16x32_bf16 v[104:107], v[150:153], v[210:213], v[104:107]
	v_mfma_f32_16x16x32_bf16 v[96:99], v[158:161], v[210:213], v[96:99]
	v_mfma_f32_16x16x32_bf16 v[88:91], v[150:153], v[230:233], v[88:91]
	v_mfma_f32_16x16x32_bf16 v[80:83], v[158:161], v[230:233], v[80:83]
	v_mfma_f32_16x16x32_bf16 v[128:131], v[154:157], v[186:189], v[128:131]
	v_mfma_f32_16x16x32_bf16 v[124:127], v[162:165], v[186:189], v[124:127]
	v_mfma_f32_16x16x32_bf16 v[120:123], v[154:157], v[194:197], v[120:123]
	v_mfma_f32_16x16x32_bf16 v[112:115], v[162:165], v[194:197], v[112:115]
	v_mfma_f32_16x16x32_bf16 v[104:107], v[154:157], v[226:229], v[104:107]
	v_mfma_f32_16x16x32_bf16 v[96:99], v[162:165], v[226:229], v[96:99]
	v_mfma_f32_16x16x32_bf16 v[88:91], v[154:157], v[234:237], v[88:91]
	v_mfma_f32_16x16x32_bf16 v[80:83], v[162:165], v[234:237], v[80:83]
	s_setprio 0
	s_setprio 1
	v_mfma_f32_16x16x32_bf16 v[116:119], v[166:169], v[182:185], v[116:119]
	v_mfma_f32_16x16x32_bf16 v[108:111], v[174:177], v[182:185], v[108:111]
	v_mfma_f32_16x16x32_bf16 v[100:103], v[166:169], v[190:193], v[100:103]
	v_mfma_f32_16x16x32_bf16 v[92:95], v[174:177], v[190:193], v[92:95]
	v_mfma_f32_16x16x32_bf16 v[84:87], v[166:169], v[210:213], v[84:87]
	v_mfma_f32_16x16x32_bf16 v[76:79], v[174:177], v[210:213], v[76:79]
	v_mfma_f32_16x16x32_bf16 v[72:75], v[166:169], v[230:233], v[72:75]
	v_mfma_f32_16x16x32_bf16 v[68:71], v[174:177], v[230:233], v[68:71]
	v_mfma_f32_16x16x32_bf16 v[116:119], v[170:173], v[186:189], v[116:119]
	v_mfma_f32_16x16x32_bf16 v[108:111], v[178:181], v[186:189], v[108:111]
	v_mfma_f32_16x16x32_bf16 v[100:103], v[170:173], v[194:197], v[100:103]
	v_mfma_f32_16x16x32_bf16 v[92:95], v[178:181], v[194:197], v[92:95]
	v_mfma_f32_16x16x32_bf16 v[84:87], v[170:173], v[226:229], v[84:87]
	v_mfma_f32_16x16x32_bf16 v[76:79], v[178:181], v[226:229], v[76:79]
	v_mfma_f32_16x16x32_bf16 v[72:75], v[170:173], v[234:237], v[72:75]
	v_mfma_f32_16x16x32_bf16 v[68:71], v[178:181], v[234:237], v[68:71]
	s_setprio 0
	s_barrier
	s_add_i32 s14, s47, s27
	v_lshl_add_u64 v[144:145], v[144:145], 0, s[64:65]
	s_mov_b32 m0, s14
	ds_read_b128 v[182:185], v148 offset:49152
	ds_read_b128 v[186:189], v148 offset:50176
	ds_read_b128 v[190:193], v148 offset:51200
	ds_read_b128 v[194:197], v148 offset:52224
	ds_read_b128 v[210:213], v148 offset:53248
	ds_read_b128 v[226:229], v148 offset:54272
	ds_read_b128 v[230:233], v148 offset:55296
	ds_read_b128 v[234:237], v148 offset:56320
	global_load_lds_dwordx4 v[144:145], off
	s_add_i32 m0, s14, 0x2000
	s_add_u32 s14, s18, 0xb0080
	v_lshl_add_u64 v[144:145], v[238:239], 0, s[64:65]
	s_addc_u32 s15, s19, 0
	s_add_i32 s18, s48, s27
	global_load_lds_dwordx4 v[144:145], off
	v_lshl_add_u64 v[144:145], s[14:15], 0, v[134:135]
	s_mov_b32 m0, s18
	s_nop 0
	global_load_lds_dwordx4 v[144:145], off
	v_lshl_add_u64 v[144:145], s[14:15], 0, v[138:139]
	s_add_i32 m0, s18, 0x2000
	s_nop 0
	global_load_lds_dwordx4 v[144:145], off
	s_waitcnt vmcnt(6)
	s_waitcnt lgkmcnt(0)
	s_barrier
	s_setprio 1
	s_waitcnt lgkmcnt(0)
	v_mfma_f32_16x16x32_bf16 v[64:67], v[150:153], v[182:185], v[64:67]
	v_mfma_f32_16x16x32_bf16 v[60:63], v[158:161], v[182:185], v[60:63]
	v_mfma_f32_16x16x32_bf16 v[56:59], v[150:153], v[190:193], v[56:59]
	v_mfma_f32_16x16x32_bf16 v[48:51], v[158:161], v[190:193], v[48:51]
	v_mfma_f32_16x16x32_bf16 v[40:43], v[150:153], v[210:213], v[40:43]
	v_mfma_f32_16x16x32_bf16 v[32:35], v[158:161], v[210:213], v[32:35]
	v_mfma_f32_16x16x32_bf16 v[24:27], v[150:153], v[230:233], v[24:27]
	v_mfma_f32_16x16x32_bf16 v[16:19], v[158:161], v[230:233], v[16:19]
	v_mfma_f32_16x16x32_bf16 v[64:67], v[154:157], v[186:189], v[64:67]
	v_mfma_f32_16x16x32_bf16 v[60:63], v[162:165], v[186:189], v[60:63]
	v_mfma_f32_16x16x32_bf16 v[56:59], v[154:157], v[194:197], v[56:59]
	v_mfma_f32_16x16x32_bf16 v[48:51], v[162:165], v[194:197], v[48:51]
	v_mfma_f32_16x16x32_bf16 v[40:43], v[154:157], v[226:229], v[40:43]
	v_mfma_f32_16x16x32_bf16 v[32:35], v[162:165], v[226:229], v[32:35]
	v_mfma_f32_16x16x32_bf16 v[24:27], v[154:157], v[234:237], v[24:27]
	v_mfma_f32_16x16x32_bf16 v[16:19], v[162:165], v[234:237], v[16:19]
	s_setprio 0
	s_setprio 1
	v_mfma_f32_16x16x32_bf16 v[52:55], v[166:169], v[182:185], v[52:55]
	v_mfma_f32_16x16x32_bf16 v[44:47], v[174:177], v[182:185], v[44:47]
	v_mfma_f32_16x16x32_bf16 v[36:39], v[166:169], v[190:193], v[36:39]
	v_mfma_f32_16x16x32_bf16 v[28:31], v[174:177], v[190:193], v[28:31]
	v_mfma_f32_16x16x32_bf16 v[20:23], v[166:169], v[210:213], v[20:23]
	v_mfma_f32_16x16x32_bf16 v[12:15], v[174:177], v[210:213], v[12:15]
	v_mfma_f32_16x16x32_bf16 v[8:11], v[166:169], v[230:233], v[8:11]
	v_mfma_f32_16x16x32_bf16 v[4:7], v[174:177], v[230:233], v[4:7]
	v_mfma_f32_16x16x32_bf16 v[52:55], v[170:173], v[186:189], v[52:55]
	v_mfma_f32_16x16x32_bf16 v[44:47], v[178:181], v[186:189], v[44:47]
	v_mfma_f32_16x16x32_bf16 v[36:39], v[170:173], v[194:197], v[36:39]
	v_mfma_f32_16x16x32_bf16 v[28:31], v[178:181], v[194:197], v[28:31]
	v_mfma_f32_16x16x32_bf16 v[20:23], v[170:173], v[226:229], v[20:23]
	v_mfma_f32_16x16x32_bf16 v[12:15], v[178:181], v[226:229], v[12:15]
	v_mfma_f32_16x16x32_bf16 v[8:11], v[170:173], v[234:237], v[8:11]
	v_mfma_f32_16x16x32_bf16 v[4:7], v[178:181], v[234:237], v[4:7]
	s_setprio 0
	s_barrier
	s_add_i32 s46, s46, 2
	s_add_u32 s44, s44, 0x100
	s_addc_u32 s45, s45, 0
	s_cmp_gt_u32 s46, 41
	s_mov_b64 s[14:15], s[16:17]
	s_cbranch_scc0 .LBB0_669
	s_and_b64 vcc, exec, s[10:11]
	s_cbranch_vccz .LBB0_672
	s_barrier

; #define PG8_WAIT_V(n) asm volatile("s_waitcnt vmcnt(" #n ")" ::: "memory")
;     __host__ __device__ bool next(int i, Unit& u) const {
;         const long L = (long)i * G + c; if (L >= nwg) return false;
;         int wgid = (int)L; { const int q = nwg / NXCD, r = nwg % NXCD, xcd = wgid % NXCD, off = wgid / NXCD; wgid = (xcd < r ? xcd * (q + 1) : r * (q + 1) + (xcd - r) * q) + off; }
;         const int nig = WGM * nN, gid = wgid / nig, fm = gid * WGM, gsz = (nM - fm) < WGM ? (nM - fm) : WGM;
;         u.pm = fm + ((wgid % nig) % gsz); u.pn = (wgid % nig) / gsz; return true;
; template <class Epi, class Sched, bool ALIGN_EPI = false, bool SP2 = false>
; __device__ __forceinline__ void gemm_phase(PG8_LAS unsigned char* lds, const Gemm g, const Sched& S, const Epi& E) {
;     ...
;     for (int i = 0; i < 2; ++i) { int R, C; stage_rc(tid * 16 + i * 8192, R, C); const int Rb = Epi::PERM ? ((R & ~31) + perm32(R & 31)) : R;
;         voffA[i] = (unsigned)(R * g.lda + C) * 2u; voffB[i] = (unsigned)(Rb * g.ldb + C) * 2u; }
;     const size_t kstep = (size_t)(BK * 2);
;     const size_t hstepA = (size_t)HALF * g.lda * 2, hstepB = (size_t)HALF * g.ldb * 2;
;     const size_t tstepA = 2 * hstepA, tstepB = 2 * hstepB;
;     const unsigned ldsw = (unsigned)wid * 1024u;
;     const int aoff = lds_byte(wr * 64 + fr, fq * 8), boff = lds_byte(wc * 32 + fr, fq * 8);
;     ...
;     Unit cur, nxt; int ui = 0;
;     if (!S.next(0, cur)) return;
;     f32x4 acc[2][2][4][2];
; #pragma unroll
;     for (int a = 0; a < 2; ++a)
; #pragma unroll
;         for (int b = 0; b < 2; ++b)
; #pragma unroll
;             for (int m = 0; m < 4; ++m)
; #pragma unroll
;                 for (int n = 0; n < 2; ++n) acc[a][b][m][n] = (f32x4){0.f, 0.f, 0.f, 0.f};
;     bf16x8 At[4][2], B0[2][2], B1[2][2];
;     const char* cA = (const char*)g.A + (size_t)cur.pm * tstepA; const char* cB = (const char*)g.Bt + (size_t)cur.pn * tstepB;
;     S.a_ready(cur);
;     if constexpr (SP2) {
;         PG8_STAGE(PG8_SB(0, 0), cB, voffB); PG8_STAGE(PG8_SB(0, 1), cB + hstepB, voffB); PG8_STAGE(PG8_SA(0, 0), cA, voffA); PG8_STAGE(PG8_SA(0, 1), cA + hstepA, voffA);
;         if (wr == 1) PG8_BAR;
;         PG8_WAIT_V(2); PG8_BAR;
;         PG8_STAGE(PG8_SB(1, 0), cB + kstep, voffB); PG8_STAGE(PG8_SA(1, 0), cA + kstep, voffA); PG8_STAGE(PG8_SB(1, 1), cB + hstepB + kstep, voffB);
;         PG8_WAIT_V(6); PG8_BAR;
;     } else {
.LBB0_807:
	v_mov_b32_e32 v17, v0
	s_cmpk_gt_i32 s1, 0x2ff
	v_readfirstlane_b32 s15, v17
	s_cbranch_scc1 .LBB0_829
	v_lshlrev_b32_e32 v4, 4, v17
	v_add_u32_e32 v5, 0x2000, v4
	v_ashrrev_i32_e32 v2, 31, v5
	v_lshrrev_b32_e32 v2, 22, v2
	v_add_u32_e32 v2, v5, v2
	v_ashrrev_i32_e32 v2, 10, v2
	v_mul_i32_i24_e32 v6, 0x400, v2
	v_sub_u32_e32 v5, v5, v6
	v_lshrrev_b32_e32 v6, 4, v5
	v_bitop3_b32 v5, v6, v5, 32 bitop3:0x6c
	v_ashrrev_i32_e32 v6, 31, v5
	v_lshrrev_b32_e32 v6, 26, v6
	v_add_u32_e32 v6, v5, v6
	v_lshlrev_b32_e32 v7, 3, v2
	s_ashr_i32 s34, s1, 31
	v_ashrrev_i32_e32 v12, 6, v6
	v_and_b32_e32 v7, -16, v7
	s_lshr_b32 s12, s34, 29
	v_add_u32_e32 v7, v12, v7
	s_add_i32 s12, s1, s12
	s_ashr_i32 s16, s15, 6
	v_and_b32_e32 v8, 3, v12
	v_lshrrev_b32_e32 v9, 2, v7
	v_lshlrev_b32_e32 v10, 1, v7
	v_and_b32_e32 v6, 0xc0, v6
	s_ashr_i32 s13, s12, 3
	s_and_b32 s12, s12, -8
	s_ashr_i32 s17, s15, 8
	s_lshl_b32 s33, s16, 10
	v_and_or_b32 v8, v7, s75, v8
	v_and_b32_e32 v9, 4, v9
	v_and_b32_e32 v10, 24, v10
	v_sub_u32_e32 v5, v5, v6
	s_sub_i32 s12, s1, s12
	v_or3_b32 v8, v8, v9, v10
	v_lshlrev_b32_e32 v9, 5, v2
	v_ashrrev_i16_sdwa v5, v1, sext(v5) dst_sel:DWORD dst_unused:UNUSED_PAD src0_sel:DWORD src1_sel:BYTE_0
	s_cmp_lt_i32 s12, 0
	s_movk_i32 s14, 0x61
	v_and_b32_e32 v9, 32, v9
	v_bfe_i32 v13, v5, 0, 16
	s_cselect_b32 s14, s14, 0x60
	v_add_lshl_u32 v5, v9, v13, 1
	s_mul_i32 s12, s12, s14
	v_lshl_add_u32 v132, v8, 11, v5
	v_lshl_add_u32 v134, v7, 11, v5
	v_bfe_i32 v5, v17, 27, 1
	s_add_i32 s12, s12, s13
	v_lshrrev_b32_e32 v5, 22, v5
	s_mul_hi_i32 s13, s12, 0x2aaaaaab
	v_add_u32_e32 v5, v4, v5
	s_lshr_b32 s14, s13, 31
	s_ashr_i32 s13, s13, 4
	v_and_b32_e32 v5, 0xfffffc00, v5
	s_add_i32 s13, s13, s14
	v_sub_u32_e32 v4, v4, v5
	s_lshl_b32 s18, s13, 3
	s_mulk_i32 s13, 0x60
	v_lshrrev_b32_e32 v5, 4, v4
	v_ashrrev_i32_e32 v6, 31, v17
	s_sub_i32 s12, s12, s13
	v_bitop3_b32 v4, v5, v4, 32 bitop3:0x6c
	v_lshrrev_b32_e32 v6, 26, v6
	s_bfe_i32 s13, s12, 0x80000
	v_ashrrev_i32_e32 v5, 31, v4
	v_add_u32_e32 v6, v17, v6
	s_bfe_u32 s13, s13, 0x3000c
	v_lshrrev_b32_e32 v5, 26, v5
	v_ashrrev_i32_e32 v15, 6, v6
	s_add_i32 s13, s12, s13
	v_add_u32_e32 v5, v4, v5
	v_lshlrev_b32_e32 v6, 3, v15
	s_bfe_i32 s14, s13, 0x80000
	s_and_b32 s13, s13, 0xf8
	v_ashrrev_i32_e32 v14, 6, v5
	v_and_b32_e32 v6, -16, v6
	s_sub_i32 s12, s12, s13
	v_add_u32_e32 v6, v14, v6
	s_sext_i32_i16 s14, s14
	s_sext_i32_i8 s12, s12
	v_and_b32_e32 v7, 3, v14
	v_lshrrev_b32_e32 v8, 2, v6
	v_lshlrev_b32_e32 v9, 1, v6
	v_and_b32_e32 v5, 0xc0, v5
	s_lshr_b32 s14, s14, 3
	s_add_i32 s24, s18, s12
	v_and_or_b32 v7, v6, s75, v7
	v_and_b32_e32 v8, 4, v8
	v_and_b32_e32 v9, 24, v9
	v_sub_u32_e32 v4, v4, v5
	s_ashr_i32 s25, s24, 31
	s_bfe_i64 s[18:19], s[14:15], 0x100000
	v_or3_b32 v7, v7, v8, v9
	v_lshlrev_b32_e32 v8, 5, v15
	v_ashrrev_i16_sdwa v4, v1, sext(v4) dst_sel:DWORD dst_unused:UNUSED_PAD src0_sel:DWORD src1_sel:BYTE_0
	s_lshl_b64 s[12:13], s[24:25], 19
	s_lshl_b64 s[18:19], s[18:19], 19
	v_and_b32_e32 v8, 32, v8
	v_bfe_i32 v16, v4, 0, 16
	s_add_u32 s26, s10, s18
	v_add_lshl_u32 v4, v8, v16, 1
	s_addc_u32 s27, s11, s19
	s_add_i32 s35, s33, 0
	v_lshl_add_u32 v136, v7, 11, v4
	s_add_i32 m0, s35, 0x10000
	v_lshl_add_u32 v138, v6, 11, v4
	global_load_lds_dwordx4 v136, s[26:27]
	s_add_i32 m0, s35, 0x12000
	s_add_u32 s18, s26, 0x40000
	global_load_lds_dwordx4 v132, s[26:27]
	s_addc_u32 s19, s27, 0
	s_add_i32 m0, s35, 0x14000
	v_mov_b32_e32 v137, v3
	global_load_lds_dwordx4 v136, s[18:19]
	s_add_i32 m0, s35, 0x16000
	s_add_u32 s28, s8, s12
	s_addc_u32 s29, s9, s13
	s_add_i32 s37, s35, 0x2000
	global_load_lds_dwordx4 v132, s[18:19]
	s_mov_b32 m0, s35
	s_add_u32 s12, s28, 0x40000
	global_load_lds_dwordx4 v138, s[28:29]
	s_mov_b32 m0, s37
	s_addc_u32 s13, s29, 0
	s_add_i32 s39, s35, 0x4000
	global_load_lds_dwordx4 v134, s[28:29]
	s_mov_b32 m0, s39
	s_add_i32 s40, s35, 0x6000
	global_load_lds_dwordx4 v138, s[12:13]
	s_mov_b32 m0, s40
	v_mov_b32_e32 v133, v3
	global_load_lds_dwordx4 v134, s[12:13]
	v_mov_b32_e32 v139, v3
	v_mov_b32_e32 v135, v3
	s_cmp_eq_u32 s17, 1
	v_lshl_add_u64 v[10:11], s[26:27], 0, v[136:137]
	v_lshl_add_u64 v[8:9], s[26:27], 0, v[132:133]
	v_lshl_add_u64 v[4:5], s[28:29], 0, v[138:139]
	s_cselect_b64 s[12:13], -1, 0
	s_cmp_lg_u32 s17, 1
	v_lshl_add_u64 v[6:7], s[28:29], 0, v[134:135]
	v_lshl_add_u64 v[244:245], s[28:29], 0, v[138:139]
	v_lshl_add_u64 v[246:247], s[28:29], 0, v[134:135]
	s_cbranch_scc1 .LBB0_810
	s_barrier

; #define PG8_STAGE(bufoff, gbase, voff) do { _Pragma("unroll") for (int _i = 0; _i < 2; ++_i) \
;         __builtin_amdgcn_global_load_lds((const unsigned*)((const char*)(gbase) + (voff)[_i]), (PG8_LAS unsigned*)(lds + (bufoff) + ldsw + _i * 8192), 16, 0, 0); } while (0)
; #define PG8_LDA(dst, b, h) do { _Pragma("unroll") for (int m = 0; m < 4; ++m) _Pragma("unroll") for (int k = 0; k < 2; ++k) dst[m][k] = *(const PG8_LAS bf16x8*)(lds + PG8_SA(b, h) + aoff + m * 2048 + k * 1024); } while (0)
; #define PG8_LDB(dst, b, h) do { _Pragma("unroll") for (int n = 0; n < 2; ++n) _Pragma("unroll") for (int k = 0; k < 2; ++k) dst[n][k] = *(const PG8_LAS bf16x8*)(lds + PG8_SB(b, h) + boff + n * 2048 + k * 1024); } while (0)
; #define PG8_MMA(ai, bj, At, Bt) do { __builtin_amdgcn_s_setprio(1); _Pragma("unroll") for (int m = 0; m < 4; ++m) _Pragma("unroll") for (int n = 0; n < 2; ++n) _Pragma("unroll") for (int k = 0; k < 2; ++k) \
;         acc[ai][bj][m][n] = __builtin_amdgcn_mfma_f32_16x16x32_bf16(Bt[n][k], At[m][k], acc[ai][bj][m][n], 0, 0, 0); __builtin_amdgcn_s_setprio(0); } while (0)
; #define PG8_WAIT_V(n) asm volatile("s_waitcnt vmcnt(" #n ")" ::: "memory")
; #define PG8_WAIT_L(n) asm volatile("s_waitcnt lgkmcnt(" #n ")" ::: "memory")
; #define PG8_BAR __builtin_amdgcn_s_barrier()
; #define PG8_SCHED __builtin_amdgcn_sched_barrier(0)
; template <class Epi, class Sched, bool ALIGN_EPI = false, bool SP2 = false>
; __device__ __forceinline__ void gemm_phase(PG8_LAS unsigned char* lds, const Gemm g, const Sched& S, const Epi& E) {
;     ...
;             PG8_LDB(B0, 0, 0); PG8_LDB(B1, 0, 1); PG8_SCHED; PG8_LDA(At, 0, 0); PG8_STAGE(PG8_SA(1, 1), a1 + hstepA, voffA);
;             PG8_WAIT_V(8); PG8_WAIT_L(0); PG8_BAR; PG8_MMA(0, 0, At, B0); PG8_MMA(0, 1, At, B1); PG8_BAR; PG8_SCHED;
;             PG8_LDA(At, 0, 1); PG8_STAGE(PG8_SB(0, 0), b2, voffB); PG8_STAGE(PG8_SB(0, 1), b2 + hstepB, voffB); PG8_STAGE(PG8_SA(0, 0), a2, voffA);
;             PG8_WAIT_V(8); PG8_WAIT_L(0); PG8_BAR; PG8_MMA(1, 0, At, B0); PG8_MMA(1, 1, At, B1); PG8_BAR; PG8_SCHED;
.LBB0_816:
	s_add_u32 s28, s26, 0xfffc0080
	s_addc_u32 s29, s27, -1
	s_add_i32 s52, 0, 0x10000
	s_cmp_eq_u32 s51, 12
	s_cselect_b32 s31, s19, s29
	s_cselect_b32 s30, s25, s28
	v_add_u32_e32 v2, s52, v153
	s_cselect_b32 s29, s17, s50
	s_cselect_b32 s28, s48, s49
	s_add_i32 s54, 0, 0x14000
	ds_read_b128 v[148:151], v2
	ds_read_b128 v[156:159], v2 offset:1024
	ds_read_b128 v[160:163], v2 offset:2048
	ds_read_b128 v[164:167], v2 offset:3072
	v_add_u32_e32 v2, s54, v153
	ds_read_b128 v[168:171], v2
	ds_read_b128 v[172:175], v2 offset:1024
	ds_read_b128 v[176:179], v2 offset:2048
	ds_read_b128 v[180:183], v2 offset:3072
	v_lshl_add_u64 v[196:197], s[26:27], 0, v[144:145]
	s_add_i32 m0, s35, 0xc000
	ds_read_b128 v[184:187], v154
	ds_read_b128 v[188:191], v154 offset:1024
	ds_read_b128 v[192:195], v154 offset:2048
	ds_read_b128 v[210:213], v154 offset:3072
	ds_read_b128 v[226:229], v154 offset:4096
	ds_read_b128 v[230:233], v154 offset:5120
	ds_read_b128 v[234:237], v154 offset:6144
	ds_read_b128 v[238:241], v154 offset:7168
	v_lshl_add_u64 v[248:249], v[244:245], 0, s[64:65]
	s_mov_b32 m0, s43
	s_nop 0
	global_load_lds_dwordx4 v[248:249], off
	v_lshl_add_u64 v[248:249], v[246:247], 0, s[64:65]
	s_mov_b32 m0, s44
	s_nop 0
	global_load_lds_dwordx4 v[248:249], off
	s_add_i32 m0, s35, 0xc000
	s_nop 0
	global_load_lds_dwordx4 v[196:197], off
	v_lshl_add_u64 v[196:197], s[26:27], 0, v[142:143]
	s_add_i32 m0, s35, 0xe000
	s_nop 0
	global_load_lds_dwordx4 v[196:197], off
	s_waitcnt vmcnt(8)
	s_waitcnt lgkmcnt(0)
	s_barrier
	s_setprio 1
	s_waitcnt lgkmcnt(0)
	v_mfma_f32_16x16x32_bf16 v[128:131], v[148:151], v[184:187], v[128:131]
	v_mfma_f32_16x16x32_bf16 v[124:127], v[160:163], v[184:187], v[124:127]
	v_mfma_f32_16x16x32_bf16 v[116:119], v[148:151], v[192:195], v[116:119]
	v_mfma_f32_16x16x32_bf16 v[108:111], v[160:163], v[192:195], v[108:111]
	v_mfma_f32_16x16x32_bf16 v[100:103], v[148:151], v[226:229], v[100:103]
	v_mfma_f32_16x16x32_bf16 v[92:95], v[160:163], v[226:229], v[92:95]
	v_mfma_f32_16x16x32_bf16 v[84:87], v[148:151], v[234:237], v[84:87]
	v_mfma_f32_16x16x32_bf16 v[76:79], v[160:163], v[234:237], v[76:79]
	v_mfma_f32_16x16x32_bf16 v[128:131], v[156:159], v[188:191], v[128:131]
	v_mfma_f32_16x16x32_bf16 v[124:127], v[164:167], v[188:191], v[124:127]
	v_mfma_f32_16x16x32_bf16 v[116:119], v[156:159], v[210:213], v[116:119]
	v_mfma_f32_16x16x32_bf16 v[108:111], v[164:167], v[210:213], v[108:111]
	v_mfma_f32_16x16x32_bf16 v[100:103], v[156:159], v[230:233], v[100:103]
	v_mfma_f32_16x16x32_bf16 v[92:95], v[164:167], v[230:233], v[92:95]
	v_mfma_f32_16x16x32_bf16 v[84:87], v[156:159], v[238:241], v[84:87]
	v_mfma_f32_16x16x32_bf16 v[76:79], v[164:167], v[238:241], v[76:79]
	s_setprio 0
	s_setprio 1
	v_mfma_f32_16x16x32_bf16 v[120:123], v[168:171], v[184:187], v[120:123]
	v_mfma_f32_16x16x32_bf16 v[112:115], v[176:179], v[184:187], v[112:115]
	v_mfma_f32_16x16x32_bf16 v[104:107], v[168:171], v[192:195], v[104:107]
	v_mfma_f32_16x16x32_bf16 v[96:99], v[176:179], v[192:195], v[96:99]
	v_mfma_f32_16x16x32_bf16 v[88:91], v[168:171], v[226:229], v[88:91]
	v_mfma_f32_16x16x32_bf16 v[80:83], v[176:179], v[226:229], v[80:83]
	v_mfma_f32_16x16x32_bf16 v[72:75], v[168:171], v[234:237], v[72:75]
	v_mfma_f32_16x16x32_bf16 v[68:71], v[176:179], v[234:237], v[68:71]
	v_mfma_f32_16x16x32_bf16 v[120:123], v[172:175], v[188:191], v[120:123]
	v_mfma_f32_16x16x32_bf16 v[112:115], v[180:183], v[188:191], v[112:115]
	v_mfma_f32_16x16x32_bf16 v[104:107], v[172:175], v[210:213], v[104:107]
	v_mfma_f32_16x16x32_bf16 v[96:99], v[180:183], v[210:213], v[96:99]
	v_mfma_f32_16x16x32_bf16 v[88:91], v[172:175], v[230:233], v[88:91]
	v_mfma_f32_16x16x32_bf16 v[80:83], v[180:183], v[230:233], v[80:83]
	v_mfma_f32_16x16x32_bf16 v[72:75], v[172:175], v[238:241], v[72:75]
	v_mfma_f32_16x16x32_bf16 v[68:71], v[180:183], v[238:241], v[68:71]
	s_setprio 0
	s_barrier
	s_add_i32 s52, s52, s33
	v_lshl_add_u64 v[196:197], s[28:29], 0, v[136:137]
	s_mov_b32 m0, s52
	ds_read_b128 v[184:187], v154 offset:16384
	ds_read_b128 v[188:191], v154 offset:17408
	ds_read_b128 v[192:195], v154 offset:18432
	ds_read_b128 v[210:213], v154 offset:19456
	ds_read_b128 v[226:229], v154 offset:20480
	ds_read_b128 v[230:233], v154 offset:21504
	ds_read_b128 v[234:237], v154 offset:22528
	ds_read_b128 v[238:241], v154 offset:23552
	global_load_lds_dwordx4 v[196:197], off
	s_add_i32 m0, s52, 0x2000
	s_add_u32 s52, s28, 0x40000
	v_lshl_add_u64 v[242:243], s[28:29], 0, v[132:133]
	s_addc_u32 s53, s29, 0
	s_add_i32 s54, s54, s33
	global_load_lds_dwordx4 v[242:243], off
	v_lshl_add_u64 v[244:245], s[52:53], 0, v[136:137]
	s_mov_b32 m0, s54
	v_lshl_add_u64 v[246:247], s[30:31], 0, v[134:135]
	global_load_lds_dwordx4 v[244:245], off
	v_lshl_add_u64 v[244:245], s[52:53], 0, v[132:133]
	s_add_i32 m0, s54, 0x2000
	s_nop 0
	global_load_lds_dwordx4 v[244:245], off
	v_lshl_add_u64 v[244:245], s[30:31], 0, v[138:139]
	s_waitcnt vmcnt(6)
	s_waitcnt lgkmcnt(0)
	s_barrier
; #define PG8_STAGE(bufoff, gbase, voff) do { _Pragma("unroll") for (int _i = 0; _i < 2; ++_i) \
;         __builtin_amdgcn_global_load_lds((const unsigned*)((const char*)(gbase) + (voff)[_i]), (PG8_LAS unsigned*)(lds + (bufoff) + ldsw + _i * 8192), 16, 0, 0); } while (0)
; #define PG8_LDA(dst, b, h) do { _Pragma("unroll") for (int m = 0; m < 4; ++m) _Pragma("unroll") for (int k = 0; k < 2; ++k) dst[m][k] = *(const PG8_LAS bf16x8*)(lds + PG8_SA(b, h) + aoff + m * 2048 + k * 1024); } while (0)
; #define PG8_LDB(dst, b, h) do { _Pragma("unroll") for (int n = 0; n < 2; ++n) _Pragma("unroll") for (int k = 0; k < 2; ++k) dst[n][k] = *(const PG8_LAS bf16x8*)(lds + PG8_SB(b, h) + boff + n * 2048 + k * 1024); } while (0)
; #define PG8_MMA(ai, bj, At, Bt) do { __builtin_amdgcn_s_setprio(1); _Pragma("unroll") for (int m = 0; m < 4; ++m) _Pragma("unroll") for (int n = 0; n < 2; ++n) _Pragma("unroll") for (int k = 0; k < 2; ++k) \
;         acc[ai][bj][m][n] = __builtin_amdgcn_mfma_f32_16x16x32_bf16(Bt[n][k], At[m][k], acc[ai][bj][m][n], 0, 0, 0); __builtin_amdgcn_s_setprio(0); } while (0)
; #define PG8_WAIT_V(n) asm volatile("s_waitcnt vmcnt(" #n ")" ::: "memory")
; #define PG8_WAIT_L(n) asm volatile("s_waitcnt lgkmcnt(" #n ")" ::: "memory")
; #define PG8_BAR __builtin_amdgcn_s_barrier()
; #define PG8_SCHED __builtin_amdgcn_sched_barrier(0)
; template <class Epi, class Sched, bool ALIGN_EPI = false, bool SP2 = false>
; __device__ __forceinline__ void gemm_phase(PG8_LAS unsigned char* lds, const Gemm g, const Sched& S, const Epi& E) {
;     ...
;             PG8_WAIT_V(8); PG8_WAIT_L(0); PG8_BAR; PG8_MMA(1, 0, At, B0); PG8_MMA(1, 1, At, B1); PG8_BAR; PG8_SCHED;
;             PG8_LDB(B0, 1, 0); PG8_LDB(B1, 1, 1); PG8_SCHED; PG8_LDA(At, 1, 0); PG8_STAGE(PG8_SA(0, 1), a2 + hstepA, voffA);
;             PG8_WAIT_V(8); PG8_WAIT_L(0); PG8_BAR; PG8_MMA(0, 0, At, B0); PG8_MMA(0, 1, At, B1); PG8_BAR; PG8_SCHED;
	s_setprio 1
	s_waitcnt lgkmcnt(0)
	v_mfma_f32_16x16x32_bf16 v[64:67], v[148:151], v[184:187], v[64:67]
	v_mfma_f32_16x16x32_bf16 v[60:63], v[160:163], v[184:187], v[60:63]
	v_mfma_f32_16x16x32_bf16 v[52:55], v[148:151], v[192:195], v[52:55]
	v_mfma_f32_16x16x32_bf16 v[44:47], v[160:163], v[192:195], v[44:47]
	v_mfma_f32_16x16x32_bf16 v[36:39], v[148:151], v[226:229], v[36:39]
	v_mfma_f32_16x16x32_bf16 v[28:31], v[160:163], v[226:229], v[28:31]
	v_mfma_f32_16x16x32_bf16 v[20:23], v[148:151], v[234:237], v[20:23]
	v_mfma_f32_16x16x32_bf16 v[12:15], v[160:163], v[234:237], v[12:15]
	v_mfma_f32_16x16x32_bf16 v[64:67], v[156:159], v[188:191], v[64:67]
	v_mfma_f32_16x16x32_bf16 v[60:63], v[164:167], v[188:191], v[60:63]
	v_mfma_f32_16x16x32_bf16 v[52:55], v[156:159], v[210:213], v[52:55]
	v_mfma_f32_16x16x32_bf16 v[44:47], v[164:167], v[210:213], v[44:47]
	v_mfma_f32_16x16x32_bf16 v[36:39], v[156:159], v[230:233], v[36:39]
	v_mfma_f32_16x16x32_bf16 v[28:31], v[164:167], v[230:233], v[28:31]
	v_mfma_f32_16x16x32_bf16 v[20:23], v[156:159], v[238:241], v[20:23]
	v_mfma_f32_16x16x32_bf16 v[12:15], v[164:167], v[238:241], v[12:15]
	s_setprio 0
	s_setprio 1
	v_mfma_f32_16x16x32_bf16 v[56:59], v[168:171], v[184:187], v[56:59]
	v_mfma_f32_16x16x32_bf16 v[48:51], v[176:179], v[184:187], v[48:51]
	v_mfma_f32_16x16x32_bf16 v[40:43], v[168:171], v[192:195], v[40:43]
	v_mfma_f32_16x16x32_bf16 v[32:35], v[176:179], v[192:195], v[32:35]
	v_mfma_f32_16x16x32_bf16 v[24:27], v[168:171], v[226:229], v[24:27]
	v_mfma_f32_16x16x32_bf16 v[16:19], v[176:179], v[226:229], v[16:19]
	v_mfma_f32_16x16x32_bf16 v[8:11], v[168:171], v[234:237], v[8:11]
	v_mfma_f32_16x16x32_bf16 v[4:7], v[176:179], v[234:237], v[4:7]
	v_mfma_f32_16x16x32_bf16 v[56:59], v[172:175], v[188:191], v[56:59]
	v_mfma_f32_16x16x32_bf16 v[48:51], v[180:183], v[188:191], v[48:51]
	v_mfma_f32_16x16x32_bf16 v[40:43], v[172:175], v[210:213], v[40:43]
	v_mfma_f32_16x16x32_bf16 v[32:35], v[180:183], v[210:213], v[32:35]
	v_mfma_f32_16x16x32_bf16 v[24:27], v[172:175], v[230:233], v[24:27]
	v_mfma_f32_16x16x32_bf16 v[16:19], v[180:183], v[230:233], v[16:19]
	v_mfma_f32_16x16x32_bf16 v[8:11], v[172:175], v[238:241], v[8:11]
	v_mfma_f32_16x16x32_bf16 v[4:7], v[180:183], v[238:241], v[4:7]
	s_setprio 0
	s_barrier
	s_add_i32 s52, 0, 0x18000
	v_add_u32_e32 v2, s52, v153
	s_add_i32 s53, 0, 0x1c000
	ds_read_b128 v[148:151], v2
	ds_read_b128 v[156:159], v2 offset:1024
	ds_read_b128 v[160:163], v2 offset:2048
	ds_read_b128 v[164:167], v2 offset:3072
	v_add_u32_e32 v2, s53, v153
	ds_read_b128 v[168:171], v2
	ds_read_b128 v[172:175], v2 offset:1024
	ds_read_b128 v[176:179], v2 offset:2048
	ds_read_b128 v[180:183], v2 offset:3072
	s_add_u32 s30, s30, 0x40000
	s_addc_u32 s31, s31, 0
	s_mov_b32 m0, s39
	v_lshl_add_u64 v[248:249], s[30:31], 0, v[138:139]
	ds_read_b128 v[184:187], v154 offset:32768
	ds_read_b128 v[188:191], v154 offset:33792
	ds_read_b128 v[192:195], v154 offset:34816
	ds_read_b128 v[210:213], v154 offset:35840
	ds_read_b128 v[226:229], v154 offset:36864
	ds_read_b128 v[230:233], v154 offset:37888
	ds_read_b128 v[234:237], v154 offset:38912
	ds_read_b128 v[238:241], v154 offset:39936
	s_mov_b32 m0, s35
	s_nop 0
	global_load_lds_dwordx4 v[244:245], off
	s_mov_b32 m0, s37
	s_nop 0
	global_load_lds_dwordx4 v[246:247], off
	s_mov_b32 m0, s39
	s_nop 0
	global_load_lds_dwordx4 v[248:249], off
	v_lshl_add_u64 v[248:249], s[30:31], 0, v[134:135]
	s_mov_b32 m0, s40
	s_nop 0
	global_load_lds_dwordx4 v[248:249], off
	s_waitcnt vmcnt(8)
	s_waitcnt lgkmcnt(0)
	s_barrier
	s_setprio 1
	s_waitcnt lgkmcnt(0)
	v_mfma_f32_16x16x32_bf16 v[128:131], v[148:151], v[184:187], v[128:131]
	v_mfma_f32_16x16x32_bf16 v[124:127], v[160:163], v[184:187], v[124:127]
	v_mfma_f32_16x16x32_bf16 v[116:119], v[148:151], v[192:195], v[116:119]
	v_mfma_f32_16x16x32_bf16 v[108:111], v[160:163], v[192:195], v[108:111]
	v_mfma_f32_16x16x32_bf16 v[100:103], v[148:151], v[226:229], v[100:103]
	v_mfma_f32_16x16x32_bf16 v[92:95], v[160:163], v[226:229], v[92:95]
	v_mfma_f32_16x16x32_bf16 v[84:87], v[148:151], v[234:237], v[84:87]
	v_mfma_f32_16x16x32_bf16 v[76:79], v[160:163], v[234:237], v[76:79]
	v_mfma_f32_16x16x32_bf16 v[128:131], v[156:159], v[188:191], v[128:131]
	v_mfma_f32_16x16x32_bf16 v[124:127], v[164:167], v[188:191], v[124:127]
	v_mfma_f32_16x16x32_bf16 v[116:119], v[156:159], v[210:213], v[116:119]
	v_mfma_f32_16x16x32_bf16 v[108:111], v[164:167], v[210:213], v[108:111]
	v_mfma_f32_16x16x32_bf16 v[100:103], v[156:159], v[230:233], v[100:103]
	v_mfma_f32_16x16x32_bf16 v[92:95], v[164:167], v[230:233], v[92:95]
	v_mfma_f32_16x16x32_bf16 v[84:87], v[156:159], v[238:241], v[84:87]
	v_mfma_f32_16x16x32_bf16 v[76:79], v[164:167], v[238:241], v[76:79]
	s_setprio 0
	s_setprio 1
	v_mfma_f32_16x16x32_bf16 v[120:123], v[168:171], v[184:187], v[120:123]
	v_mfma_f32_16x16x32_bf16 v[112:115], v[176:179], v[184:187], v[112:115]
	v_mfma_f32_16x16x32_bf16 v[104:107], v[168:171], v[192:195], v[104:107]
	v_mfma_f32_16x16x32_bf16 v[96:99], v[176:179], v[192:195], v[96:99]
	v_mfma_f32_16x16x32_bf16 v[88:91], v[168:171], v[226:229], v[88:91]
	v_mfma_f32_16x16x32_bf16 v[80:83], v[176:179], v[226:229], v[80:83]
	v_mfma_f32_16x16x32_bf16 v[72:75], v[168:171], v[234:237], v[72:75]
	v_mfma_f32_16x16x32_bf16 v[68:71], v[176:179], v[234:237], v[68:71]
	v_mfma_f32_16x16x32_bf16 v[120:123], v[172:175], v[188:191], v[120:123]
	v_mfma_f32_16x16x32_bf16 v[112:115], v[180:183], v[188:191], v[112:115]
	v_mfma_f32_16x16x32_bf16 v[104:107], v[172:175], v[210:213], v[104:107]
	v_mfma_f32_16x16x32_bf16 v[96:99], v[180:183], v[210:213], v[96:99]
	v_mfma_f32_16x16x32_bf16 v[88:91], v[172:175], v[230:233], v[88:91]
	v_mfma_f32_16x16x32_bf16 v[80:83], v[180:183], v[230:233], v[80:83]
	v_mfma_f32_16x16x32_bf16 v[72:75], v[172:175], v[238:241], v[72:75]
	v_mfma_f32_16x16x32_bf16 v[68:71], v[180:183], v[238:241], v[68:71]
	s_setprio 0
	s_barrier
; #define PG8_STAGE(bufoff, gbase, voff) do { _Pragma("unroll") for (int _i = 0; _i < 2; ++_i) \
;         __builtin_amdgcn_global_load_lds((const unsigned*)((const char*)(gbase) + (voff)[_i]), (PG8_LAS unsigned*)(lds + (bufoff) + ldsw + _i * 8192), 16, 0, 0); } while (0)
; #define PG8_LDA(dst, b, h) do { _Pragma("unroll") for (int m = 0; m < 4; ++m) _Pragma("unroll") for (int k = 0; k < 2; ++k) dst[m][k] = *(const PG8_LAS bf16x8*)(lds + PG8_SA(b, h) + aoff + m * 2048 + k * 1024); } while (0)
; #define PG8_MMA(ai, bj, At, Bt) do { __builtin_amdgcn_s_setprio(1); _Pragma("unroll") for (int m = 0; m < 4; ++m) _Pragma("unroll") for (int n = 0; n < 2; ++n) _Pragma("unroll") for (int k = 0; k < 2; ++k) \
;         acc[ai][bj][m][n] = __builtin_amdgcn_mfma_f32_16x16x32_bf16(Bt[n][k], At[m][k], acc[ai][bj][m][n], 0, 0, 0); __builtin_amdgcn_s_setprio(0); } while (0)
; #define PG8_WAIT_V(n) asm volatile("s_waitcnt vmcnt(" #n ")" ::: "memory")
; #define PG8_WAIT_L(n) asm volatile("s_waitcnt lgkmcnt(" #n ")" ::: "memory")
; #define PG8_BAR __builtin_amdgcn_s_barrier()
; #define PG8_SCHED __builtin_amdgcn_sched_barrier(0)
; template <class Epi, class Sched, bool ALIGN_EPI = false, bool SP2 = false>
; __device__ __forceinline__ void gemm_phase(PG8_LAS unsigned char* lds, const Gemm g, const Sched& S, const Epi& E) {
;     ...
;             PG8_WAIT_V(8); PG8_WAIT_L(0); PG8_BAR; PG8_MMA(0, 0, At, B0); PG8_MMA(0, 1, At, B1); PG8_BAR; PG8_SCHED;
;             PG8_LDA(At, 1, 1); PG8_STAGE(PG8_SB(1, 0), b3, voffB); PG8_STAGE(PG8_SB(1, 1), b3 + hstepB, voffB); PG8_STAGE(PG8_SA(1, 0), a3, voffA);
;             PG8_WAIT_V(8); PG8_WAIT_L(0); PG8_BAR; PG8_MMA(1, 0, At, B0); PG8_MMA(1, 1, At, B1); PG8_BAR; PG8_SCHED;
;     __device__ __forceinline__ void operator()(const f32x4 (&acc)[2][2][4][2], const Unit& u, int wr, int wc, int fr, int fq) const {
;         const int row0 = u.pm * BM + wr * 64 + fr, ct0 = wc * 32 + 8 * fq;
;         if (u.pn < 12) {
	s_add_i32 s30, s52, s33
	v_lshl_add_u64 v[196:197], v[196:197], 0, s[64:65]
	s_mov_b32 m0, s30
	ds_read_b128 v[184:187], v154 offset:49152
	ds_read_b128 v[188:191], v154 offset:50176
	ds_read_b128 v[192:195], v154 offset:51200
	ds_read_b128 v[210:213], v154 offset:52224
	ds_read_b128 v[226:229], v154 offset:53248
	ds_read_b128 v[230:233], v154 offset:54272
	ds_read_b128 v[234:237], v154 offset:55296
	ds_read_b128 v[238:241], v154 offset:56320
	global_load_lds_dwordx4 v[196:197], off
	s_add_i32 m0, s30, 0x2000
	s_add_u32 s28, s28, 0x40080
	v_lshl_add_u64 v[196:197], v[242:243], 0, s[64:65]
	s_addc_u32 s29, s29, 0
	s_add_i32 s30, s53, s33
	global_load_lds_dwordx4 v[196:197], off
	v_lshl_add_u64 v[196:197], s[28:29], 0, v[136:137]
	s_mov_b32 m0, s30
	s_nop 0
	global_load_lds_dwordx4 v[196:197], off
	v_lshl_add_u64 v[196:197], s[28:29], 0, v[132:133]
	s_add_i32 m0, s30, 0x2000
	s_nop 0
	global_load_lds_dwordx4 v[196:197], off
	s_waitcnt vmcnt(6)
	s_waitcnt lgkmcnt(0)
	s_barrier
	s_setprio 1
	s_waitcnt lgkmcnt(0)
	v_mfma_f32_16x16x32_bf16 v[64:67], v[148:151], v[184:187], v[64:67]
	v_mfma_f32_16x16x32_bf16 v[60:63], v[160:163], v[184:187], v[60:63]
	v_mfma_f32_16x16x32_bf16 v[52:55], v[148:151], v[192:195], v[52:55]
	v_mfma_f32_16x16x32_bf16 v[44:47], v[160:163], v[192:195], v[44:47]
	v_mfma_f32_16x16x32_bf16 v[36:39], v[148:151], v[226:229], v[36:39]
	v_mfma_f32_16x16x32_bf16 v[28:31], v[160:163], v[226:229], v[28:31]
	v_mfma_f32_16x16x32_bf16 v[20:23], v[148:151], v[234:237], v[20:23]
	v_mfma_f32_16x16x32_bf16 v[12:15], v[160:163], v[234:237], v[12:15]
	v_mfma_f32_16x16x32_bf16 v[64:67], v[156:159], v[188:191], v[64:67]
	v_mfma_f32_16x16x32_bf16 v[60:63], v[164:167], v[188:191], v[60:63]
	v_mfma_f32_16x16x32_bf16 v[52:55], v[156:159], v[210:213], v[52:55]
	v_mfma_f32_16x16x32_bf16 v[44:47], v[164:167], v[210:213], v[44:47]
	v_mfma_f32_16x16x32_bf16 v[36:39], v[156:159], v[230:233], v[36:39]
	v_mfma_f32_16x16x32_bf16 v[28:31], v[164:167], v[230:233], v[28:31]
	v_mfma_f32_16x16x32_bf16 v[20:23], v[156:159], v[238:241], v[20:23]
	v_mfma_f32_16x16x32_bf16 v[12:15], v[164:167], v[238:241], v[12:15]
	s_setprio 0
	s_setprio 1
	v_mfma_f32_16x16x32_bf16 v[56:59], v[168:171], v[184:187], v[56:59]
	v_mfma_f32_16x16x32_bf16 v[48:51], v[176:179], v[184:187], v[48:51]
	v_mfma_f32_16x16x32_bf16 v[40:43], v[168:171], v[192:195], v[40:43]
	v_mfma_f32_16x16x32_bf16 v[32:35], v[176:179], v[192:195], v[32:35]
	v_mfma_f32_16x16x32_bf16 v[24:27], v[168:171], v[226:229], v[24:27]
	v_mfma_f32_16x16x32_bf16 v[16:19], v[176:179], v[226:229], v[16:19]
	v_mfma_f32_16x16x32_bf16 v[8:11], v[168:171], v[234:237], v[8:11]
	v_mfma_f32_16x16x32_bf16 v[4:7], v[176:179], v[234:237], v[4:7]
	v_mfma_f32_16x16x32_bf16 v[56:59], v[172:175], v[188:191], v[56:59]
	v_mfma_f32_16x16x32_bf16 v[48:51], v[180:183], v[188:191], v[48:51]
	v_mfma_f32_16x16x32_bf16 v[40:43], v[172:175], v[210:213], v[40:43]
	v_mfma_f32_16x16x32_bf16 v[32:35], v[180:183], v[210:213], v[32:35]
	v_mfma_f32_16x16x32_bf16 v[24:27], v[172:175], v[230:233], v[24:27]
	v_mfma_f32_16x16x32_bf16 v[16:19], v[180:183], v[230:233], v[16:19]
	v_mfma_f32_16x16x32_bf16 v[8:11], v[172:175], v[238:241], v[8:11]
	v_mfma_f32_16x16x32_bf16 v[4:7], v[180:183], v[238:241], v[4:7]
	s_setprio 0
	s_barrier
	s_add_i32 s51, s51, 2
	s_add_u32 s49, s49, 0x100
	s_addc_u32 s50, s50, 0
	s_add_u32 s26, s26, 0x100
	s_addc_u32 s27, s27, 0
	s_cmp_gt_u32 s51, 13
	s_cbranch_scc0 .LBB0_816
	s_and_b64 vcc, exec, s[14:15]
	s_cbranch_vccnz .LBB0_821
	v_lshl_add_u32 v150, s24, 8, v152
	s_cmp_gt_i32 s47, 11
	s_mov_b64 s[24:25], -1
	s_cbranch_scc1 .LBB0_822

; #define PG8_WAIT_V(n) asm volatile("s_waitcnt vmcnt(" #n ")" ::: "memory")
;     __host__ __device__ bool next(int i, Unit& u) const {
;         const long L = (long)i * G + c; if (L >= nwg) return false;
;         int wgid = (int)L; { const int q = nwg / NXCD, r = nwg % NXCD, xcd = wgid % NXCD, off = wgid / NXCD; wgid = (xcd < r ? xcd * (q + 1) : r * (q + 1) + (xcd - r) * q) + off; }
;         const int nig = WGM * nN, gid = wgid / nig, fm = gid * WGM, gsz = (nM - fm) < WGM ? (nM - fm) : WGM;
;         u.pm = fm + ((wgid % nig) % gsz); u.pn = (wgid % nig) / gsz; return true;
; template <class Epi, class Sched, bool ALIGN_EPI = false, bool SP2 = false>
; __device__ __forceinline__ void gemm_phase(PG8_LAS unsigned char* lds, const Gemm g, const Sched& S, const Epi& E) {
;     ...
;     for (int i = 0; i < 2; ++i) { int R, C; stage_rc(tid * 16 + i * 8192, R, C); const int Rb = Epi::PERM ? ((R & ~31) + perm32(R & 31)) : R;
;         voffA[i] = (unsigned)(R * g.lda + C) * 2u; voffB[i] = (unsigned)(Rb * g.ldb + C) * 2u; }
;     const size_t kstep = (size_t)(BK * 2);
;     const size_t hstepA = (size_t)HALF * g.lda * 2, hstepB = (size_t)HALF * g.ldb * 2;
;     const size_t tstepA = 2 * hstepA, tstepB = 2 * hstepB;
;     const unsigned ldsw = (unsigned)wid * 1024u;
;     const int aoff = lds_byte(wr * 64 + fr, fq * 8), boff = lds_byte(wc * 32 + fr, fq * 8);
;     ...
;     Unit cur, nxt; int ui = 0;
;     if (!S.next(0, cur)) return;
;     f32x4 acc[2][2][4][2];
; #pragma unroll
;     for (int a = 0; a < 2; ++a)
; #pragma unroll
;         for (int b = 0; b < 2; ++b)
; #pragma unroll
;             for (int m = 0; m < 4; ++m)
; #pragma unroll
;                 for (int n = 0; n < 2; ++n) acc[a][b][m][n] = (f32x4){0.f, 0.f, 0.f, 0.f};
;     bf16x8 At[4][2], B0[2][2], B1[2][2];
;     const char* cA = (const char*)g.A + (size_t)cur.pm * tstepA; const char* cB = (const char*)g.Bt + (size_t)cur.pn * tstepB;
;     S.a_ready(cur);
;     if constexpr (SP2) {
;         PG8_STAGE(PG8_SB(0, 0), cB, voffB); PG8_STAGE(PG8_SB(0, 1), cB + hstepB, voffB); PG8_STAGE(PG8_SA(0, 0), cA, voffA); PG8_STAGE(PG8_SA(0, 1), cA + hstepA, voffA);
;         if (wr == 1) PG8_BAR;
;         PG8_WAIT_V(2); PG8_BAR;
;         PG8_STAGE(PG8_SB(1, 0), cB + kstep, voffB); PG8_STAGE(PG8_SA(1, 0), cA + kstep, voffA); PG8_STAGE(PG8_SB(1, 1), cB + hstepB + kstep, voffB);
;         PG8_WAIT_V(6); PG8_BAR;
;     } else {
.LBB0_1081:
	v_ashrrev_i32_e32 v4, 31, v18
	v_lshrrev_b32_e32 v4, 26, v4
	v_add_u32_e32 v4, v18, v4
	v_ashrrev_i32_e32 v12, 6, v4
	v_bfe_i32 v4, v18, 27, 1
	v_lshlrev_b32_e32 v2, 4, v18
	v_lshrrev_b32_e32 v4, 22, v4
	v_add_u32_e32 v4, v2, v4
	v_and_b32_e32 v4, 0xfffffc00, v4
	v_sub_u32_e32 v4, v2, v4
	v_lshrrev_b32_e32 v5, 4, v4
	v_bitop3_b32 v4, v5, v4, 32 bitop3:0x6c
	v_ashrrev_i32_e32 v6, 31, v4
	v_lshrrev_b32_e32 v6, 26, v6
	s_add_u32 s29, s4, 0xf000000
	v_readlane_b32 s7, v252, 0
	v_add_u32_e32 v6, v4, v6
	s_addc_u32 s30, s5, 0
	s_lshl_b32 s7, s7, 21
	v_lshlrev_b32_e32 v5, 3, v12
	v_ashrrev_i32_e32 v13, 6, v6
	v_and_b32_e32 v6, 0xc0, v6
	s_add_u32 s7, s4, s7
	v_and_b32_e32 v5, -16, v5
	v_sub_u32_e32 v4, v4, v6
	s_addc_u32 s9, s5, 0
	v_add_u32_e32 v5, v13, v5
	v_ashrrev_i16_sdwa v4, v1, sext(v4) dst_sel:DWORD dst_unused:UNUSED_PAD src0_sel:DWORD src1_sel:BYTE_0
	s_add_u32 s31, s7, 0xa800000
	v_lshlrev_b32_e32 v7, 5, v12
	v_bfe_i32 v14, v4, 0, 16
	v_lshlrev_b32_e32 v4, 1, v5
	v_lshrrev_b32_e32 v6, 2, v5
	v_and_b32_e32 v8, 3, v13
	s_addc_u32 s33, s9, 0
	v_and_b32_e32 v7, 32, v7
	v_and_b32_e32 v4, 24, v4
	v_and_b32_e32 v6, 4, v6
	v_and_or_b32 v8, v5, s75, v8
	s_add_i32 s6, s8, s6
	v_or3_b32 v4, v8, v6, v4
	v_add_lshl_u32 v6, v7, v14, 1
	v_add_u32_e32 v2, 0x2000, v2
	s_ashr_i32 s7, s6, 31
	v_lshl_add_u32 v134, v4, 11, v6
	v_ashrrev_i32_e32 v4, 31, v2
	s_lshr_b32 s7, s7, 27
	v_lshrrev_b32_e32 v4, 22, v4
	s_add_i32 s7, s6, s7
	v_add_u32_e32 v4, v2, v4
	s_ashr_i32 s8, s7, 5
	s_and_b32 s7, s7, 0xffe0
	v_ashrrev_i32_e32 v15, 10, v4
	s_sub_i32 s6, s6, s7
	v_mul_i32_i24_e32 v4, 0x400, v15
	s_bfe_i32 s7, s6, 0x80000
	v_sub_u32_e32 v2, v2, v4
	s_bfe_u32 s7, s7, 0x3000c
	v_lshrrev_b32_e32 v4, 4, v2
	s_add_i32 s7, s6, s7
	v_bitop3_b32 v2, v4, v2, 32 bitop3:0x6c
	s_lshl_b32 s9, s8, 3
	s_bfe_i32 s8, s7, 0x80000
	s_and_b32 s7, s7, 0xf8
	v_lshl_add_u32 v132, v5, 11, v6
	v_ashrrev_i32_e32 v5, 31, v2
	s_sub_i32 s6, s6, s7
	v_lshrrev_b32_e32 v5, 26, v5
	s_sext_i32_i16 s8, s8
	s_sext_i32_i8 s6, s6
	v_add_u32_e32 v5, v2, v5
	s_lshr_b32 s8, s8, 3
	s_add_i32 s16, s9, s6
	s_ashr_i32 s11, s10, 6
	v_lshlrev_b32_e32 v4, 3, v15
	v_ashrrev_i32_e32 v16, 6, v5
	v_and_b32_e32 v5, 0xc0, v5
	s_ashr_i32 s17, s16, 31
	s_bfe_i64 s[14:15], s[8:9], 0x100000
	v_and_b32_e32 v4, -16, v4
	v_sub_u32_e32 v2, v2, v5
	s_ashr_i32 s12, s10, 8
	s_lshl_b32 s34, s11, 10
	s_lshl_b64 s[6:7], s[16:17], 19
	s_lshl_b64 s[14:15], s[14:15], 19
	v_add_u32_e32 v4, v16, v4
	v_ashrrev_i16_sdwa v2, v1, sext(v2) dst_sel:DWORD dst_unused:UNUSED_PAD src0_sel:DWORD src1_sel:BYTE_0
	s_add_u32 s22, s31, s14
	v_lshlrev_b32_e32 v6, 5, v15
	v_bfe_i32 v17, v2, 0, 16
	v_lshlrev_b32_e32 v2, 1, v4
	v_lshrrev_b32_e32 v5, 2, v4
	v_and_b32_e32 v7, 3, v16
	s_addc_u32 s23, s33, s15
	s_add_i32 s17, s34, 0
	v_and_b32_e32 v6, 32, v6
	v_and_b32_e32 v2, 24, v2
	v_and_b32_e32 v5, 4, v5
	v_and_or_b32 v7, v4, s75, v7
	s_add_i32 m0, s17, 0x10000
	v_or3_b32 v2, v7, v5, v2
	v_add_lshl_u32 v5, v6, v17, 1
	global_load_lds_dwordx4 v134, s[22:23]
	s_add_i32 m0, s17, 0x12000
	v_lshl_add_u32 v138, v2, 11, v5
	s_add_u32 s14, s22, 0x40000
	global_load_lds_dwordx4 v138, s[22:23]
	s_addc_u32 s15, s23, 0
	s_add_i32 m0, s17, 0x14000
	v_lshl_add_u32 v136, v4, 11, v5
	global_load_lds_dwordx4 v134, s[14:15]
	s_add_i32 m0, s17, 0x16000
	s_add_u32 s24, s29, s6
	s_addc_u32 s25, s30, s7
	s_add_i32 s35, s17, 0x2000
	global_load_lds_dwordx4 v138, s[14:15]
	s_mov_b32 m0, s17
	s_add_u32 s6, s24, 0x40000
	global_load_lds_dwordx4 v132, s[24:25]
	s_mov_b32 m0, s35
	s_addc_u32 s7, s25, 0
	s_add_i32 s37, s17, 0x4000
	global_load_lds_dwordx4 v136, s[24:25]
	s_mov_b32 m0, s37
	s_add_i32 s38, s17, 0x6000
	global_load_lds_dwordx4 v132, s[6:7]
	s_mov_b32 m0, s38
	v_mov_b32_e32 v135, v3
	global_load_lds_dwordx4 v136, s[6:7]
	v_mov_b32_e32 v139, v3
	v_mov_b32_e32 v133, v3
	v_mov_b32_e32 v137, v3
	s_cmp_eq_u32 s12, 1
	v_lshl_add_u64 v[10:11], s[22:23], 0, v[134:135]
	v_lshl_add_u64 v[8:9], s[22:23], 0, v[138:139]
	v_lshl_add_u64 v[4:5], s[24:25], 0, v[132:133]
	s_cselect_b64 s[6:7], -1, 0
	s_cmp_lg_u32 s12, 1
	v_lshl_add_u64 v[6:7], s[24:25], 0, v[136:137]
	v_lshl_add_u64 v[240:241], s[24:25], 0, v[132:133]
	v_lshl_add_u64 v[242:243], s[24:25], 0, v[136:137]
	s_cbranch_scc1 .LBB0_1083
	s_barrier

; #define PG8_STAGE(bufoff, gbase, voff) do { _Pragma("unroll") for (int _i = 0; _i < 2; ++_i) \
;         __builtin_amdgcn_global_load_lds((const unsigned*)((const char*)(gbase) + (voff)[_i]), (PG8_LAS unsigned*)(lds + (bufoff) + ldsw + _i * 8192), 16, 0, 0); } while (0)
; #define PG8_LDA(dst, b, h) do { _Pragma("unroll") for (int m = 0; m < 4; ++m) _Pragma("unroll") for (int k = 0; k < 2; ++k) dst[m][k] = *(const PG8_LAS bf16x8*)(lds + PG8_SA(b, h) + aoff + m * 2048 + k * 1024); } while (0)
; #define PG8_LDB(dst, b, h) do { _Pragma("unroll") for (int n = 0; n < 2; ++n) _Pragma("unroll") for (int k = 0; k < 2; ++k) dst[n][k] = *(const PG8_LAS bf16x8*)(lds + PG8_SB(b, h) + boff + n * 2048 + k * 1024); } while (0)
; #define PG8_MMA(ai, bj, At, Bt) do { __builtin_amdgcn_s_setprio(1); _Pragma("unroll") for (int m = 0; m < 4; ++m) _Pragma("unroll") for (int n = 0; n < 2; ++n) _Pragma("unroll") for (int k = 0; k < 2; ++k) \
;         acc[ai][bj][m][n] = __builtin_amdgcn_mfma_f32_16x16x32_bf16(Bt[n][k], At[m][k], acc[ai][bj][m][n], 0, 0, 0); __builtin_amdgcn_s_setprio(0); } while (0)
; #define PG8_WAIT_V(n) asm volatile("s_waitcnt vmcnt(" #n ")" ::: "memory")
; #define PG8_WAIT_L(n) asm volatile("s_waitcnt lgkmcnt(" #n ")" ::: "memory")
; #define PG8_BAR __builtin_amdgcn_s_barrier()
; #define PG8_SCHED __builtin_amdgcn_sched_barrier(0)
; template <class Epi, class Sched, bool ALIGN_EPI = false, bool SP2 = false>
; __device__ __forceinline__ void gemm_phase(PG8_LAS unsigned char* lds, const Gemm g, const Sched& S, const Epi& E) {
;     ...
;             PG8_LDB(B0, 0, 0); PG8_LDB(B1, 0, 1); PG8_SCHED; PG8_LDA(At, 0, 0); PG8_STAGE(PG8_SA(1, 1), a1 + hstepA, voffA);
;             PG8_WAIT_V(8); PG8_WAIT_L(0); PG8_BAR; PG8_MMA(0, 0, At, B0); PG8_MMA(0, 1, At, B1); PG8_BAR; PG8_SCHED;
;             PG8_LDA(At, 0, 1); PG8_STAGE(PG8_SB(0, 0), b2, voffB); PG8_STAGE(PG8_SB(0, 1), b2 + hstepB, voffB); PG8_STAGE(PG8_SA(0, 0), a2, voffA);
;             PG8_WAIT_V(8); PG8_WAIT_L(0); PG8_BAR; PG8_MMA(1, 0, At, B0); PG8_MMA(1, 1, At, B1); PG8_BAR; PG8_SCHED;
.LBB0_1093:
	s_add_u32 s24, s22, 0xfffc0080
	s_addc_u32 s25, s23, -1
	s_add_i32 s49, 0, 0x10000
	s_cmp_eq_u32 s48, 12
	s_cselect_b32 s27, s15, s25
	s_cselect_b32 s26, s44, s24
	v_add_u32_e32 v144, s49, v146
	s_cselect_b32 s25, s13, s47
	s_cselect_b32 s24, s45, s46
	s_add_i32 s52, 0, 0x14000
	ds_read_b128 v[150:153], v144
	ds_read_b128 v[154:157], v144 offset:1024
	ds_read_b128 v[158:161], v144 offset:2048
	ds_read_b128 v[162:165], v144 offset:3072
	v_add_u32_e32 v144, s52, v146
	ds_read_b128 v[166:169], v144
	ds_read_b128 v[170:173], v144 offset:1024
	ds_read_b128 v[174:177], v144 offset:2048
	ds_read_b128 v[178:181], v144 offset:3072
	v_lshl_add_u64 v[144:145], s[22:23], 0, v[142:143]
	s_add_i32 m0, s17, 0xc000
	ds_read_b128 v[182:185], v148
	ds_read_b128 v[186:189], v148 offset:1024
	ds_read_b128 v[190:193], v148 offset:2048
	ds_read_b128 v[194:197], v148 offset:3072
	ds_read_b128 v[210:213], v148 offset:4096
	ds_read_b128 v[226:229], v148 offset:5120
	ds_read_b128 v[230:233], v148 offset:6144
	ds_read_b128 v[234:237], v148 offset:7168
	v_lshl_add_u64 v[244:245], v[240:241], 0, s[64:65]
	s_mov_b32 m0, s39
	s_nop 0
	global_load_lds_dwordx4 v[244:245], off
	v_lshl_add_u64 v[244:245], v[242:243], 0, s[64:65]
	s_mov_b32 m0, s40
	s_nop 0
	global_load_lds_dwordx4 v[244:245], off
	s_add_i32 m0, s17, 0xc000
	s_nop 0
	global_load_lds_dwordx4 v[144:145], off
	v_lshl_add_u64 v[144:145], s[22:23], 0, v[140:141]
	s_add_i32 m0, s17, 0xe000
	s_nop 0
	global_load_lds_dwordx4 v[144:145], off
	s_waitcnt vmcnt(8)
	s_waitcnt lgkmcnt(0)
	s_barrier
	s_setprio 1
	s_waitcnt lgkmcnt(0)
	v_mfma_f32_16x16x32_bf16 v[128:131], v[150:153], v[182:185], v[128:131]
	v_mfma_f32_16x16x32_bf16 v[124:127], v[158:161], v[182:185], v[124:127]
	v_mfma_f32_16x16x32_bf16 v[120:123], v[150:153], v[190:193], v[120:123]
	v_mfma_f32_16x16x32_bf16 v[112:115], v[158:161], v[190:193], v[112:115]
	v_mfma_f32_16x16x32_bf16 v[104:107], v[150:153], v[210:213], v[104:107]
	v_mfma_f32_16x16x32_bf16 v[96:99], v[158:161], v[210:213], v[96:99]
	v_mfma_f32_16x16x32_bf16 v[88:91], v[150:153], v[230:233], v[88:91]
	v_mfma_f32_16x16x32_bf16 v[80:83], v[158:161], v[230:233], v[80:83]
	v_mfma_f32_16x16x32_bf16 v[128:131], v[154:157], v[186:189], v[128:131]
	v_mfma_f32_16x16x32_bf16 v[124:127], v[162:165], v[186:189], v[124:127]
	v_mfma_f32_16x16x32_bf16 v[120:123], v[154:157], v[194:197], v[120:123]
	v_mfma_f32_16x16x32_bf16 v[112:115], v[162:165], v[194:197], v[112:115]
	v_mfma_f32_16x16x32_bf16 v[104:107], v[154:157], v[226:229], v[104:107]
	v_mfma_f32_16x16x32_bf16 v[96:99], v[162:165], v[226:229], v[96:99]
	v_mfma_f32_16x16x32_bf16 v[88:91], v[154:157], v[234:237], v[88:91]
	v_mfma_f32_16x16x32_bf16 v[80:83], v[162:165], v[234:237], v[80:83]
	s_setprio 0
	s_setprio 1
	v_mfma_f32_16x16x32_bf16 v[116:119], v[166:169], v[182:185], v[116:119]
	v_mfma_f32_16x16x32_bf16 v[108:111], v[174:177], v[182:185], v[108:111]
	v_mfma_f32_16x16x32_bf16 v[100:103], v[166:169], v[190:193], v[100:103]
	v_mfma_f32_16x16x32_bf16 v[92:95], v[174:177], v[190:193], v[92:95]
	v_mfma_f32_16x16x32_bf16 v[84:87], v[166:169], v[210:213], v[84:87]
	v_mfma_f32_16x16x32_bf16 v[76:79], v[174:177], v[210:213], v[76:79]
	v_mfma_f32_16x16x32_bf16 v[72:75], v[166:169], v[230:233], v[72:75]
	v_mfma_f32_16x16x32_bf16 v[68:71], v[174:177], v[230:233], v[68:71]
	v_mfma_f32_16x16x32_bf16 v[116:119], v[170:173], v[186:189], v[116:119]
	v_mfma_f32_16x16x32_bf16 v[108:111], v[178:181], v[186:189], v[108:111]
	v_mfma_f32_16x16x32_bf16 v[100:103], v[170:173], v[194:197], v[100:103]
	v_mfma_f32_16x16x32_bf16 v[92:95], v[178:181], v[194:197], v[92:95]
	v_mfma_f32_16x16x32_bf16 v[84:87], v[170:173], v[226:229], v[84:87]
	v_mfma_f32_16x16x32_bf16 v[76:79], v[178:181], v[226:229], v[76:79]
	v_mfma_f32_16x16x32_bf16 v[72:75], v[170:173], v[234:237], v[72:75]
	v_mfma_f32_16x16x32_bf16 v[68:71], v[178:181], v[234:237], v[68:71]
	s_setprio 0
	s_barrier
	s_add_i32 s49, s49, s34
	v_lshl_add_u64 v[144:145], s[24:25], 0, v[134:135]
	s_mov_b32 m0, s49
	ds_read_b128 v[182:185], v148 offset:16384
	ds_read_b128 v[186:189], v148 offset:17408
	ds_read_b128 v[190:193], v148 offset:18432
	ds_read_b128 v[194:197], v148 offset:19456
	ds_read_b128 v[210:213], v148 offset:20480
	ds_read_b128 v[226:229], v148 offset:21504
	ds_read_b128 v[230:233], v148 offset:22528
	ds_read_b128 v[234:237], v148 offset:23552
	global_load_lds_dwordx4 v[144:145], off
	s_add_i32 m0, s49, 0x2000
	s_add_u32 s50, s24, 0x40000
	v_lshl_add_u64 v[238:239], s[24:25], 0, v[138:139]
	s_addc_u32 s51, s25, 0
	s_add_i32 s49, s52, s34
	global_load_lds_dwordx4 v[238:239], off
	v_lshl_add_u64 v[240:241], s[50:51], 0, v[134:135]
	s_mov_b32 m0, s49
	v_lshl_add_u64 v[242:243], s[26:27], 0, v[136:137]
	global_load_lds_dwordx4 v[240:241], off
	v_lshl_add_u64 v[240:241], s[50:51], 0, v[138:139]
	s_add_i32 m0, s49, 0x2000
	s_nop 0
	global_load_lds_dwordx4 v[240:241], off
	v_lshl_add_u64 v[240:241], s[26:27], 0, v[132:133]
	s_waitcnt vmcnt(6)
	s_waitcnt lgkmcnt(0)
	s_barrier
; #define PG8_STAGE(bufoff, gbase, voff) do { _Pragma("unroll") for (int _i = 0; _i < 2; ++_i) \
;         __builtin_amdgcn_global_load_lds((const unsigned*)((const char*)(gbase) + (voff)[_i]), (PG8_LAS unsigned*)(lds + (bufoff) + ldsw + _i * 8192), 16, 0, 0); } while (0)
; #define PG8_LDA(dst, b, h) do { _Pragma("unroll") for (int m = 0; m < 4; ++m) _Pragma("unroll") for (int k = 0; k < 2; ++k) dst[m][k] = *(const PG8_LAS bf16x8*)(lds + PG8_SA(b, h) + aoff + m * 2048 + k * 1024); } while (0)
; #define PG8_LDB(dst, b, h) do { _Pragma("unroll") for (int n = 0; n < 2; ++n) _Pragma("unroll") for (int k = 0; k < 2; ++k) dst[n][k] = *(const PG8_LAS bf16x8*)(lds + PG8_SB(b, h) + boff + n * 2048 + k * 1024); } while (0)
; #define PG8_MMA(ai, bj, At, Bt) do { __builtin_amdgcn_s_setprio(1); _Pragma("unroll") for (int m = 0; m < 4; ++m) _Pragma("unroll") for (int n = 0; n < 2; ++n) _Pragma("unroll") for (int k = 0; k < 2; ++k) \
;         acc[ai][bj][m][n] = __builtin_amdgcn_mfma_f32_16x16x32_bf16(Bt[n][k], At[m][k], acc[ai][bj][m][n], 0, 0, 0); __builtin_amdgcn_s_setprio(0); } while (0)
; #define PG8_WAIT_V(n) asm volatile("s_waitcnt vmcnt(" #n ")" ::: "memory")
; #define PG8_WAIT_L(n) asm volatile("s_waitcnt lgkmcnt(" #n ")" ::: "memory")
; #define PG8_BAR __builtin_amdgcn_s_barrier()
; #define PG8_SCHED __builtin_amdgcn_sched_barrier(0)
; template <class Epi, class Sched, bool ALIGN_EPI = false, bool SP2 = false>
; __device__ __forceinline__ void gemm_phase(PG8_LAS unsigned char* lds, const Gemm g, const Sched& S, const Epi& E) {
;     ...
;             PG8_WAIT_V(8); PG8_WAIT_L(0); PG8_BAR; PG8_MMA(1, 0, At, B0); PG8_MMA(1, 1, At, B1); PG8_BAR; PG8_SCHED;
;             PG8_LDB(B0, 1, 0); PG8_LDB(B1, 1, 1); PG8_SCHED; PG8_LDA(At, 1, 0); PG8_STAGE(PG8_SA(0, 1), a2 + hstepA, voffA);
;             PG8_WAIT_V(8); PG8_WAIT_L(0); PG8_BAR; PG8_MMA(0, 0, At, B0); PG8_MMA(0, 1, At, B1); PG8_BAR; PG8_SCHED;
	s_setprio 1
	s_waitcnt lgkmcnt(0)
	v_mfma_f32_16x16x32_bf16 v[64:67], v[150:153], v[182:185], v[64:67]
	v_mfma_f32_16x16x32_bf16 v[60:63], v[158:161], v[182:185], v[60:63]
	v_mfma_f32_16x16x32_bf16 v[56:59], v[150:153], v[190:193], v[56:59]
	v_mfma_f32_16x16x32_bf16 v[48:51], v[158:161], v[190:193], v[48:51]
	v_mfma_f32_16x16x32_bf16 v[40:43], v[150:153], v[210:213], v[40:43]
	v_mfma_f32_16x16x32_bf16 v[32:35], v[158:161], v[210:213], v[32:35]
	v_mfma_f32_16x16x32_bf16 v[24:27], v[150:153], v[230:233], v[24:27]
	v_mfma_f32_16x16x32_bf16 v[16:19], v[158:161], v[230:233], v[16:19]
	v_mfma_f32_16x16x32_bf16 v[64:67], v[154:157], v[186:189], v[64:67]
	v_mfma_f32_16x16x32_bf16 v[60:63], v[162:165], v[186:189], v[60:63]
	v_mfma_f32_16x16x32_bf16 v[56:59], v[154:157], v[194:197], v[56:59]
	v_mfma_f32_16x16x32_bf16 v[48:51], v[162:165], v[194:197], v[48:51]
	v_mfma_f32_16x16x32_bf16 v[40:43], v[154:157], v[226:229], v[40:43]
	v_mfma_f32_16x16x32_bf16 v[32:35], v[162:165], v[226:229], v[32:35]
	v_mfma_f32_16x16x32_bf16 v[24:27], v[154:157], v[234:237], v[24:27]
	v_mfma_f32_16x16x32_bf16 v[16:19], v[162:165], v[234:237], v[16:19]
	s_setprio 0
	s_setprio 1
	v_mfma_f32_16x16x32_bf16 v[52:55], v[166:169], v[182:185], v[52:55]
	v_mfma_f32_16x16x32_bf16 v[44:47], v[174:177], v[182:185], v[44:47]
	v_mfma_f32_16x16x32_bf16 v[36:39], v[166:169], v[190:193], v[36:39]
	v_mfma_f32_16x16x32_bf16 v[28:31], v[174:177], v[190:193], v[28:31]
	v_mfma_f32_16x16x32_bf16 v[20:23], v[166:169], v[210:213], v[20:23]
	v_mfma_f32_16x16x32_bf16 v[12:15], v[174:177], v[210:213], v[12:15]
	v_mfma_f32_16x16x32_bf16 v[8:11], v[166:169], v[230:233], v[8:11]
	v_mfma_f32_16x16x32_bf16 v[4:7], v[174:177], v[230:233], v[4:7]
	v_mfma_f32_16x16x32_bf16 v[52:55], v[170:173], v[186:189], v[52:55]
	v_mfma_f32_16x16x32_bf16 v[44:47], v[178:181], v[186:189], v[44:47]
	v_mfma_f32_16x16x32_bf16 v[36:39], v[170:173], v[194:197], v[36:39]
	v_mfma_f32_16x16x32_bf16 v[28:31], v[178:181], v[194:197], v[28:31]
	v_mfma_f32_16x16x32_bf16 v[20:23], v[170:173], v[226:229], v[20:23]
	v_mfma_f32_16x16x32_bf16 v[12:15], v[178:181], v[226:229], v[12:15]
	v_mfma_f32_16x16x32_bf16 v[8:11], v[170:173], v[234:237], v[8:11]
	v_mfma_f32_16x16x32_bf16 v[4:7], v[178:181], v[234:237], v[4:7]
	s_setprio 0
	s_barrier
	s_add_i32 s49, 0, 0x18000
	v_add_u32_e32 v149, s49, v146
	s_add_i32 s50, 0, 0x1c000
	ds_read_b128 v[150:153], v149
	ds_read_b128 v[154:157], v149 offset:1024
	ds_read_b128 v[158:161], v149 offset:2048
	ds_read_b128 v[162:165], v149 offset:3072
	v_add_u32_e32 v149, s50, v146
	ds_read_b128 v[166:169], v149
	ds_read_b128 v[170:173], v149 offset:1024
	ds_read_b128 v[174:177], v149 offset:2048
	ds_read_b128 v[178:181], v149 offset:3072
	s_add_u32 s26, s26, 0x40000
	s_addc_u32 s27, s27, 0
	s_mov_b32 m0, s37
	v_lshl_add_u64 v[244:245], s[26:27], 0, v[132:133]
	ds_read_b128 v[182:185], v148 offset:32768
	ds_read_b128 v[186:189], v148 offset:33792
	ds_read_b128 v[190:193], v148 offset:34816
	ds_read_b128 v[194:197], v148 offset:35840
	ds_read_b128 v[210:213], v148 offset:36864
	ds_read_b128 v[226:229], v148 offset:37888
	ds_read_b128 v[230:233], v148 offset:38912
	ds_read_b128 v[234:237], v148 offset:39936
	s_mov_b32 m0, s17
	s_nop 0
	global_load_lds_dwordx4 v[240:241], off
	s_mov_b32 m0, s35
	s_nop 0
	global_load_lds_dwordx4 v[242:243], off
	s_mov_b32 m0, s37
	s_nop 0
	global_load_lds_dwordx4 v[244:245], off
	v_lshl_add_u64 v[244:245], s[26:27], 0, v[136:137]
	s_mov_b32 m0, s38
	s_nop 0
	global_load_lds_dwordx4 v[244:245], off
	s_waitcnt vmcnt(8)
	s_waitcnt lgkmcnt(0)
	s_barrier
; #define PG8_STAGE(bufoff, gbase, voff) do { _Pragma("unroll") for (int _i = 0; _i < 2; ++_i) \
;         __builtin_amdgcn_global_load_lds((const unsigned*)((const char*)(gbase) + (voff)[_i]), (PG8_LAS unsigned*)(lds + (bufoff) + ldsw + _i * 8192), 16, 0, 0); } while (0)
; #define PG8_LDA(dst, b, h) do { _Pragma("unroll") for (int m = 0; m < 4; ++m) _Pragma("unroll") for (int k = 0; k < 2; ++k) dst[m][k] = *(const PG8_LAS bf16x8*)(lds + PG8_SA(b, h) + aoff + m * 2048 + k * 1024); } while (0)
; #define PG8_MMA(ai, bj, At, Bt) do { __builtin_amdgcn_s_setprio(1); _Pragma("unroll") for (int m = 0; m < 4; ++m) _Pragma("unroll") for (int n = 0; n < 2; ++n) _Pragma("unroll") for (int k = 0; k < 2; ++k) \
;         acc[ai][bj][m][n] = __builtin_amdgcn_mfma_f32_16x16x32_bf16(Bt[n][k], At[m][k], acc[ai][bj][m][n], 0, 0, 0); __builtin_amdgcn_s_setprio(0); } while (0)
; #define PG8_WAIT_V(n) asm volatile("s_waitcnt vmcnt(" #n ")" ::: "memory")
; #define PG8_WAIT_L(n) asm volatile("s_waitcnt lgkmcnt(" #n ")" ::: "memory")
; #define PG8_BAR __builtin_amdgcn_s_barrier()
; #define PG8_SCHED __builtin_amdgcn_sched_barrier(0)
; template <class Epi, class Sched, bool ALIGN_EPI = false, bool SP2 = false>
; __device__ __forceinline__ void gemm_phase(PG8_LAS unsigned char* lds, const Gemm g, const Sched& S, const Epi& E) {
;     ...
;             PG8_WAIT_V(8); PG8_WAIT_L(0); PG8_BAR; PG8_MMA(0, 0, At, B0); PG8_MMA(0, 1, At, B1); PG8_BAR; PG8_SCHED;
;             PG8_LDA(At, 1, 1); PG8_STAGE(PG8_SB(1, 0), b3, voffB); PG8_STAGE(PG8_SB(1, 1), b3 + hstepB, voffB); PG8_STAGE(PG8_SA(1, 0), a3, voffA);
;             PG8_WAIT_V(8); PG8_WAIT_L(0); PG8_BAR; PG8_MMA(1, 0, At, B0); PG8_MMA(1, 1, At, B1); PG8_BAR; PG8_SCHED;
;     ...
;         if constexpr (ALIGN_EPI) { if (wr == 0) PG8_BAR; }
	s_setprio 1
	s_waitcnt lgkmcnt(0)
	v_mfma_f32_16x16x32_bf16 v[128:131], v[150:153], v[182:185], v[128:131]
	v_mfma_f32_16x16x32_bf16 v[124:127], v[158:161], v[182:185], v[124:127]
	v_mfma_f32_16x16x32_bf16 v[120:123], v[150:153], v[190:193], v[120:123]
	v_mfma_f32_16x16x32_bf16 v[112:115], v[158:161], v[190:193], v[112:115]
	v_mfma_f32_16x16x32_bf16 v[104:107], v[150:153], v[210:213], v[104:107]
	v_mfma_f32_16x16x32_bf16 v[96:99], v[158:161], v[210:213], v[96:99]
	v_mfma_f32_16x16x32_bf16 v[88:91], v[150:153], v[230:233], v[88:91]
	v_mfma_f32_16x16x32_bf16 v[80:83], v[158:161], v[230:233], v[80:83]
	v_mfma_f32_16x16x32_bf16 v[128:131], v[154:157], v[186:189], v[128:131]
	v_mfma_f32_16x16x32_bf16 v[124:127], v[162:165], v[186:189], v[124:127]
	v_mfma_f32_16x16x32_bf16 v[120:123], v[154:157], v[194:197], v[120:123]
	v_mfma_f32_16x16x32_bf16 v[112:115], v[162:165], v[194:197], v[112:115]
	v_mfma_f32_16x16x32_bf16 v[104:107], v[154:157], v[226:229], v[104:107]
	v_mfma_f32_16x16x32_bf16 v[96:99], v[162:165], v[226:229], v[96:99]
	v_mfma_f32_16x16x32_bf16 v[88:91], v[154:157], v[234:237], v[88:91]
	v_mfma_f32_16x16x32_bf16 v[80:83], v[162:165], v[234:237], v[80:83]
	s_setprio 0
	s_setprio 1
	v_mfma_f32_16x16x32_bf16 v[116:119], v[166:169], v[182:185], v[116:119]
	v_mfma_f32_16x16x32_bf16 v[108:111], v[174:177], v[182:185], v[108:111]
	v_mfma_f32_16x16x32_bf16 v[100:103], v[166:169], v[190:193], v[100:103]
	v_mfma_f32_16x16x32_bf16 v[92:95], v[174:177], v[190:193], v[92:95]
	v_mfma_f32_16x16x32_bf16 v[84:87], v[166:169], v[210:213], v[84:87]
	v_mfma_f32_16x16x32_bf16 v[76:79], v[174:177], v[210:213], v[76:79]
	v_mfma_f32_16x16x32_bf16 v[72:75], v[166:169], v[230:233], v[72:75]
	v_mfma_f32_16x16x32_bf16 v[68:71], v[174:177], v[230:233], v[68:71]
	v_mfma_f32_16x16x32_bf16 v[116:119], v[170:173], v[186:189], v[116:119]
	v_mfma_f32_16x16x32_bf16 v[108:111], v[178:181], v[186:189], v[108:111]
	v_mfma_f32_16x16x32_bf16 v[100:103], v[170:173], v[194:197], v[100:103]
	v_mfma_f32_16x16x32_bf16 v[92:95], v[178:181], v[194:197], v[92:95]
	v_mfma_f32_16x16x32_bf16 v[84:87], v[170:173], v[226:229], v[84:87]
	v_mfma_f32_16x16x32_bf16 v[76:79], v[178:181], v[226:229], v[76:79]
	v_mfma_f32_16x16x32_bf16 v[72:75], v[170:173], v[234:237], v[72:75]
	v_mfma_f32_16x16x32_bf16 v[68:71], v[178:181], v[234:237], v[68:71]
	s_setprio 0
	s_barrier
	s_add_i32 s26, s49, s34
	v_lshl_add_u64 v[144:145], v[144:145], 0, s[64:65]
	s_mov_b32 m0, s26
	ds_read_b128 v[182:185], v148 offset:49152
	ds_read_b128 v[186:189], v148 offset:50176
	ds_read_b128 v[190:193], v148 offset:51200
	ds_read_b128 v[194:197], v148 offset:52224
	ds_read_b128 v[210:213], v148 offset:53248
	ds_read_b128 v[226:229], v148 offset:54272
	ds_read_b128 v[230:233], v148 offset:55296
	ds_read_b128 v[234:237], v148 offset:56320
	global_load_lds_dwordx4 v[144:145], off
	s_add_i32 m0, s26, 0x2000
	s_add_u32 s24, s24, 0x40080
	v_lshl_add_u64 v[144:145], v[238:239], 0, s[64:65]
	s_addc_u32 s25, s25, 0
	s_add_i32 s26, s50, s34
	global_load_lds_dwordx4 v[144:145], off
	v_lshl_add_u64 v[144:145], s[24:25], 0, v[134:135]
	s_mov_b32 m0, s26
	s_nop 0
	global_load_lds_dwordx4 v[144:145], off
	v_lshl_add_u64 v[144:145], s[24:25], 0, v[138:139]
	s_add_i32 m0, s26, 0x2000
	s_nop 0
	global_load_lds_dwordx4 v[144:145], off
	s_waitcnt vmcnt(6)
	s_waitcnt lgkmcnt(0)
	s_barrier
	s_setprio 1
	s_waitcnt lgkmcnt(0)
	v_mfma_f32_16x16x32_bf16 v[64:67], v[150:153], v[182:185], v[64:67]
	v_mfma_f32_16x16x32_bf16 v[60:63], v[158:161], v[182:185], v[60:63]
	v_mfma_f32_16x16x32_bf16 v[56:59], v[150:153], v[190:193], v[56:59]
	v_mfma_f32_16x16x32_bf16 v[48:51], v[158:161], v[190:193], v[48:51]
	v_mfma_f32_16x16x32_bf16 v[40:43], v[150:153], v[210:213], v[40:43]
	v_mfma_f32_16x16x32_bf16 v[32:35], v[158:161], v[210:213], v[32:35]
	v_mfma_f32_16x16x32_bf16 v[24:27], v[150:153], v[230:233], v[24:27]
	v_mfma_f32_16x16x32_bf16 v[16:19], v[158:161], v[230:233], v[16:19]
	v_mfma_f32_16x16x32_bf16 v[64:67], v[154:157], v[186:189], v[64:67]
	v_mfma_f32_16x16x32_bf16 v[60:63], v[162:165], v[186:189], v[60:63]
	v_mfma_f32_16x16x32_bf16 v[56:59], v[154:157], v[194:197], v[56:59]
	v_mfma_f32_16x16x32_bf16 v[48:51], v[162:165], v[194:197], v[48:51]
	v_mfma_f32_16x16x32_bf16 v[40:43], v[154:157], v[226:229], v[40:43]
	v_mfma_f32_16x16x32_bf16 v[32:35], v[162:165], v[226:229], v[32:35]
	v_mfma_f32_16x16x32_bf16 v[24:27], v[154:157], v[234:237], v[24:27]
	v_mfma_f32_16x16x32_bf16 v[16:19], v[162:165], v[234:237], v[16:19]
	s_setprio 0
	s_setprio 1
	v_mfma_f32_16x16x32_bf16 v[52:55], v[166:169], v[182:185], v[52:55]
	v_mfma_f32_16x16x32_bf16 v[44:47], v[174:177], v[182:185], v[44:47]
	v_mfma_f32_16x16x32_bf16 v[36:39], v[166:169], v[190:193], v[36:39]
	v_mfma_f32_16x16x32_bf16 v[28:31], v[174:177], v[190:193], v[28:31]
	v_mfma_f32_16x16x32_bf16 v[20:23], v[166:169], v[210:213], v[20:23]
	v_mfma_f32_16x16x32_bf16 v[12:15], v[174:177], v[210:213], v[12:15]
	v_mfma_f32_16x16x32_bf16 v[8:11], v[166:169], v[230:233], v[8:11]
	v_mfma_f32_16x16x32_bf16 v[4:7], v[174:177], v[230:233], v[4:7]
	v_mfma_f32_16x16x32_bf16 v[52:55], v[170:173], v[186:189], v[52:55]
	v_mfma_f32_16x16x32_bf16 v[44:47], v[178:181], v[186:189], v[44:47]
	v_mfma_f32_16x16x32_bf16 v[36:39], v[170:173], v[194:197], v[36:39]
	v_mfma_f32_16x16x32_bf16 v[28:31], v[178:181], v[194:197], v[28:31]
	v_mfma_f32_16x16x32_bf16 v[20:23], v[170:173], v[226:229], v[20:23]
	v_mfma_f32_16x16x32_bf16 v[12:15], v[178:181], v[226:229], v[12:15]
	v_mfma_f32_16x16x32_bf16 v[8:11], v[170:173], v[234:237], v[8:11]
	v_mfma_f32_16x16x32_bf16 v[4:7], v[178:181], v[234:237], v[4:7]
	s_setprio 0
	s_barrier
	s_add_i32 s48, s48, 2
	s_add_u32 s46, s46, 0x100
	s_addc_u32 s47, s47, 0
	s_add_u32 s22, s22, 0x100
	s_addc_u32 s23, s23, 0
	s_cmp_gt_u32 s48, 13
	s_cbranch_scc0 .LBB0_1093
	s_and_b64 vcc, exec, s[10:11]
	s_cbranch_vccz .LBB0_1096
	s_barrier

; #define PG8_WAIT_V(n) asm volatile("s_waitcnt vmcnt(" #n ")" ::: "memory")
;     __host__ __device__ bool next(int i, Unit& u) const {
;         const long L = (long)i * G + c; if (L >= nwg) return false;
;         int wgid = (int)L; { const int q = nwg / NXCD, r = nwg % NXCD, xcd = wgid % NXCD, off = wgid / NXCD; wgid = (xcd < r ? xcd * (q + 1) : r * (q + 1) + (xcd - r) * q) + off; }
;         const int nig = WGM * nN, gid = wgid / nig, fm = gid * WGM, gsz = (nM - fm) < WGM ? (nM - fm) : WGM;
;         u.pm = fm + ((wgid % nig) % gsz); u.pn = (wgid % nig) / gsz; return true;
; template <class Epi, class Sched, bool ALIGN_EPI = false, bool SP2 = false>
; __device__ __forceinline__ void gemm_phase(PG8_LAS unsigned char* lds, const Gemm g, const Sched& S, const Epi& E) {
;     ...
;     for (int i = 0; i < 2; ++i) { int R, C; stage_rc(tid * 16 + i * 8192, R, C); const int Rb = Epi::PERM ? ((R & ~31) + perm32(R & 31)) : R;
;         voffA[i] = (unsigned)(R * g.lda + C) * 2u; voffB[i] = (unsigned)(Rb * g.ldb + C) * 2u; }
;     const size_t kstep = (size_t)(BK * 2);
;     const size_t hstepA = (size_t)HALF * g.lda * 2, hstepB = (size_t)HALF * g.ldb * 2;
;     const size_t tstepA = 2 * hstepA, tstepB = 2 * hstepB;
;     const unsigned ldsw = (unsigned)wid * 1024u;
;     const int aoff = lds_byte(wr * 64 + fr, fq * 8), boff = lds_byte(wc * 32 + fr, fq * 8);
;     ...
;     Unit cur, nxt; int ui = 0;
;     if (!S.next(0, cur)) return;
;     f32x4 acc[2][2][4][2];
; #pragma unroll
;     for (int a = 0; a < 2; ++a)
; #pragma unroll
;         for (int b = 0; b < 2; ++b)
; #pragma unroll
;             for (int m = 0; m < 4; ++m)
; #pragma unroll
;                 for (int n = 0; n < 2; ++n) acc[a][b][m][n] = (f32x4){0.f, 0.f, 0.f, 0.f};
;     bf16x8 At[4][2], B0[2][2], B1[2][2];
;     const char* cA = (const char*)g.A + (size_t)cur.pm * tstepA; const char* cB = (const char*)g.Bt + (size_t)cur.pn * tstepB;
;     S.a_ready(cur);
;     if constexpr (SP2) {
;         PG8_STAGE(PG8_SB(0, 0), cB, voffB); PG8_STAGE(PG8_SB(0, 1), cB + hstepB, voffB); PG8_STAGE(PG8_SA(0, 0), cA, voffA); PG8_STAGE(PG8_SA(0, 1), cA + hstepA, voffA);
;         if (wr == 1) PG8_BAR;
;         PG8_WAIT_V(2); PG8_BAR;
;         PG8_STAGE(PG8_SB(1, 0), cB + kstep, voffB); PG8_STAGE(PG8_SA(1, 0), cA + kstep, voffA); PG8_STAGE(PG8_SB(1, 1), cB + hstepB + kstep, voffB);
;         PG8_WAIT_V(6); PG8_BAR;
;     } else {
.LBB0_1155:
	v_ashrrev_i32_e32 v4, 31, v16
	v_lshrrev_b32_e32 v4, 26, v4
	v_add_u32_e32 v4, v16, v4
	v_ashrrev_i32_e32 v12, 6, v4
	v_bfe_i32 v4, v16, 27, 1
	v_lshlrev_b32_e32 v2, 4, v16
	v_lshrrev_b32_e32 v4, 22, v4
	v_add_u32_e32 v4, v2, v4
	v_and_b32_e32 v4, 0xfffffc00, v4
	v_sub_u32_e32 v4, v2, v4
	v_lshrrev_b32_e32 v5, 4, v4
	v_bitop3_b32 v4, v5, v4, 32 bitop3:0x6c
	v_ashrrev_i32_e32 v6, 31, v4
	v_lshrrev_b32_e32 v6, 26, v6
	v_add_u32_e32 v6, v4, v6
	v_lshlrev_b32_e32 v5, 3, v12
	v_ashrrev_i32_e32 v13, 6, v6
	v_and_b32_e32 v6, 0xc0, v6
	v_and_b32_e32 v5, -16, v5
	v_sub_u32_e32 v4, v4, v6
	v_add_u32_e32 v5, v13, v5
	v_ashrrev_i16_sdwa v4, v1, sext(v4) dst_sel:DWORD dst_unused:UNUSED_PAD src0_sel:DWORD src1_sel:BYTE_0
	v_lshlrev_b32_e32 v7, 5, v12
	v_bfe_i32 v14, v4, 0, 16
	v_lshlrev_b32_e32 v4, 1, v5
	v_lshrrev_b32_e32 v6, 2, v5
	v_and_b32_e32 v8, 3, v13
	v_and_b32_e32 v7, 32, v7
	v_and_b32_e32 v4, 24, v4
	v_and_b32_e32 v6, 4, v6
	v_and_or_b32 v8, v5, s75, v8
	v_or3_b32 v4, v8, v6, v4
	v_add_lshl_u32 v6, v7, v14, 1
	v_add_u32_e32 v2, 0x2000, v2
	v_lshl_add_u32 v134, v4, 11, v6
	v_ashrrev_i32_e32 v4, 31, v2
	v_lshrrev_b32_e32 v4, 22, v4
	v_add_u32_e32 v4, v2, v4
	v_ashrrev_i32_e32 v15, 10, v4
	v_mul_i32_i24_e32 v4, 0x400, v15
	v_readlane_b32 s0, v252, 0
	v_sub_u32_e32 v2, v2, v4
	s_mul_i32 s68, s0, 0x2c0000
	s_add_u32 s0, s14, 0xb000000
	v_lshrrev_b32_e32 v4, 4, v2
	s_addc_u32 s1, s15, 0
	s_lshl_b64 s[2:3], s[68:69], 1
	v_bitop3_b32 v2, v4, v2, 32 bitop3:0x6c
	s_add_u32 s2, s14, s2
	v_lshl_add_u32 v132, v5, 11, v6
	v_ashrrev_i32_e32 v5, 31, v2
	s_addc_u32 s3, s15, s3
	v_lshrrev_b32_e32 v5, 26, v5
	s_add_u32 s28, s2, 0x8c00000
	v_add_u32_e32 v5, v2, v5
	s_addc_u32 s29, s3, 0
	s_ashr_i32 s23, s12, 6
	v_lshlrev_b32_e32 v4, 3, v15
	v_ashrrev_i32_e32 v17, 6, v5
	v_and_b32_e32 v5, 0xc0, v5
	s_ashr_i32 s21, s20, 31
	s_ashr_i32 s19, s18, 31
	v_and_b32_e32 v4, -16, v4
	v_sub_u32_e32 v2, v2, v5
	s_ashr_i32 s2, s12, 8
	s_lshl_b32 s30, s23, 10
	s_lshl_b64 s[6:7], s[20:21], 19
	s_lshl_b64 s[4:5], s[18:19], 19
	v_add_u32_e32 v4, v17, v4
	v_ashrrev_i16_sdwa v2, v1, sext(v2) dst_sel:DWORD dst_unused:UNUSED_PAD src0_sel:DWORD src1_sel:BYTE_0
	s_add_u32 s4, s28, s4
	v_lshlrev_b32_e32 v6, 5, v15
	v_bfe_i32 v18, v2, 0, 16
	v_lshlrev_b32_e32 v2, 1, v4
	v_lshrrev_b32_e32 v5, 2, v4
	v_and_b32_e32 v7, 3, v17
	s_addc_u32 s5, s29, s5
	s_add_i32 s31, s30, 0
	v_and_b32_e32 v6, 32, v6
	v_and_b32_e32 v2, 24, v2
	v_and_b32_e32 v5, 4, v5
	v_and_or_b32 v7, v4, s75, v7
	s_add_i32 m0, s31, 0x10000
	v_or3_b32 v2, v7, v5, v2
	v_add_lshl_u32 v5, v6, v18, 1
	global_load_lds_dwordx4 v134, s[4:5]
	s_add_i32 m0, s31, 0x12000
	v_lshl_add_u32 v138, v2, 11, v5
	s_add_u32 s8, s4, 0x40000
	global_load_lds_dwordx4 v138, s[4:5]
	s_addc_u32 s9, s5, 0
	s_add_i32 m0, s31, 0x14000
	v_lshl_add_u32 v136, v4, 11, v5
	global_load_lds_dwordx4 v134, s[8:9]
	s_add_i32 m0, s31, 0x16000
	s_add_u32 s6, s0, s6
	s_addc_u32 s7, s1, s7
	s_add_i32 s33, s31, 0x2000
	global_load_lds_dwordx4 v138, s[8:9]
	s_mov_b32 m0, s31
	s_add_u32 s8, s6, 0x40000
	global_load_lds_dwordx4 v132, s[6:7]
	s_mov_b32 m0, s33
	s_addc_u32 s9, s7, 0
	s_add_i32 s34, s31, 0x4000
	global_load_lds_dwordx4 v136, s[6:7]
	s_mov_b32 m0, s34
	s_add_i32 s35, s31, 0x6000
	global_load_lds_dwordx4 v132, s[8:9]
	s_mov_b32 m0, s35
	v_mov_b32_e32 v135, v3
	global_load_lds_dwordx4 v136, s[8:9]
	v_mov_b32_e32 v139, v3
	v_mov_b32_e32 v133, v3
	v_mov_b32_e32 v137, v3
	s_cmp_eq_u32 s2, 1
	v_lshl_add_u64 v[10:11], s[4:5], 0, v[134:135]
	v_lshl_add_u64 v[8:9], s[4:5], 0, v[138:139]
	v_lshl_add_u64 v[4:5], s[6:7], 0, v[132:133]
	s_cselect_b64 s[8:9], -1, 0
	s_cmp_lg_u32 s2, 1
	v_lshl_add_u64 v[6:7], s[6:7], 0, v[136:137]
	v_lshl_add_u64 v[244:245], s[6:7], 0, v[132:133]
	v_lshl_add_u64 v[246:247], s[6:7], 0, v[136:137]
	s_cbranch_scc1 .LBB0_1157
	s_barrier

; #define PG8_STR(x) PG8_STR2(x)
; #define PG8_STAGE(bufoff, gbase, voff) do { _Pragma("unroll") for (int _i = 0; _i < 2; ++_i) \
;         __builtin_amdgcn_global_load_lds((const unsigned*)((const char*)(gbase) + (voff)[_i]), (PG8_LAS unsigned*)(lds + (bufoff) + ldsw + _i * 8192), 16, 0, 0); } while (0)
; #define PG8_LDA(dst, b, h) do { _Pragma("unroll") for (int m = 0; m < 4; ++m) _Pragma("unroll") for (int k = 0; k < 2; ++k) dst[m][k] = *(const PG8_LAS bf16x8*)(lds + PG8_SA(b, h) + aoff + m * 2048 + k * 1024); } while (0)
; #define PG8_WAIT_V(n) asm volatile("s_waitcnt vmcnt(" #n ")" ::: "memory")
; template <class Epi, class Sched, bool ALIGN_EPI = false, bool SP2 = false>
; __device__ __forceinline__ void gemm_phase(PG8_LAS unsigned char* lds, const Gemm g, const Sched& S, const Epi& E) {
;     ...
;         for (int t = 0; t < nt; t += 2) {
;     ...
;             asm volatile(".p2align 6\n\t.rept " PG8_STR(KLOOP_ALIGN) "\n\ts_nop 0\n\t.endr");
;     ...
;             const bool last = (t == nt - 2);
;             const char* a1 = cA + (size_t)(t + 1) * kstep;
;             const char* a2 = last ? nA : cA + (size_t)(t + 2) * kstep; const char* b2 = last ? nB : cB + (size_t)(t + 2) * kstep;
;             const char* a3 = a2 + kstep; const char* b3 = b2 + kstep;
;             if (last && has_next) S.a_ready(nxt);
;             if constexpr (SP2) {
;             PG8_LDB(B0, 0, 0); PG8_LDB(B1, 0, 1); PG8_SCHED; PG8_LDA(At, 0, 0); PG8_STAGE(PG8_SA(1, 1), a1 + hstepA, voffA);
;             PG8_WAIT_V(8); PG8_WAIT_L(0); PG8_BAR; PG8_MMA(0, 0, At, B0); PG8_MMA(0, 1, At, B1); PG8_BAR; PG8_SCHED;
;             PG8_LDA(At, 0, 1); PG8_STAGE(PG8_SB(0, 0), b2, voffB); PG8_STAGE(PG8_SB(0, 1), b2 + hstepB, voffB); PG8_STAGE(PG8_SA(0, 0), a2, voffA);
;             PG8_WAIT_V(8); PG8_WAIT_L(0); PG8_BAR; PG8_MMA(1, 0, At, B0); PG8_MMA(1, 1, At, B1); PG8_BAR; PG8_SCHED;
;             PG8_LDB(B0, 1, 0); PG8_LDB(B1, 1, 1); PG8_SCHED; PG8_LDA(At, 1, 0); PG8_STAGE(PG8_SA(0, 1), a2 + hstepA, voffA);
;             PG8_WAIT_V(8); PG8_WAIT_L(0); PG8_BAR; PG8_MMA(0, 0, At, B0); PG8_MMA(0, 1, At, B1); PG8_BAR; PG8_SCHED;
;             PG8_LDA(At, 1, 1); PG8_STAGE(PG8_SB(1, 0), b3, voffB); PG8_STAGE(PG8_SB(1, 1), b3 + hstepB, voffB); PG8_STAGE(PG8_SA(1, 0), a3, voffA);
;             PG8_WAIT_V(8); PG8_WAIT_L(0); PG8_BAR; PG8_MMA(1, 0, At, B0); PG8_MMA(1, 1, At, B1); PG8_BAR; PG8_SCHED;
.LBB0_1161:
	s_add_u32 s24, s22, 0xfffc0080
	s_addc_u32 s25, s23, -1
	s_add_i32 s49, 0, 0x10000
	s_cmp_eq_u32 s48, 12
	s_cselect_b32 s27, s19, s25
	s_cselect_b32 s26, s21, s24
	v_add_u32_e32 v149, s49, v154
	s_cselect_b32 s25, s44, s47
	s_cselect_b32 s24, s45, s46
	s_add_i32 s52, 0, 0x14000
	ds_read_b128 v[150:153], v149
	ds_read_b128 v[156:159], v149 offset:1024
	ds_read_b128 v[160:163], v149 offset:2048
	ds_read_b128 v[164:167], v149 offset:3072
	v_add_u32_e32 v149, s52, v154
	ds_read_b128 v[168:171], v149
	ds_read_b128 v[172:175], v149 offset:1024
	ds_read_b128 v[176:179], v149 offset:2048
	ds_read_b128 v[180:183], v149 offset:3072
	v_lshl_add_u64 v[196:197], s[22:23], 0, v[146:147]
	s_add_i32 m0, s31, 0xc000
	ds_read_b128 v[184:187], v155
	ds_read_b128 v[188:191], v155 offset:1024
	ds_read_b128 v[192:195], v155 offset:2048
	ds_read_b128 v[210:213], v155 offset:3072
	ds_read_b128 v[226:229], v155 offset:4096
	ds_read_b128 v[230:233], v155 offset:5120
	ds_read_b128 v[234:237], v155 offset:6144
	ds_read_b128 v[238:241], v155 offset:7168
	v_lshl_add_u64 v[248:249], v[244:245], 0, s[64:65]
	s_mov_b32 m0, s38
	s_nop 0
	global_load_lds_dwordx4 v[248:249], off
	v_lshl_add_u64 v[248:249], v[246:247], 0, s[64:65]
	s_mov_b32 m0, s39
	s_nop 0
	global_load_lds_dwordx4 v[248:249], off
	s_add_i32 m0, s31, 0xc000
	s_nop 0
	global_load_lds_dwordx4 v[196:197], off
	v_lshl_add_u64 v[196:197], s[22:23], 0, v[144:145]
	s_add_i32 m0, s31, 0xe000
	s_nop 0
	global_load_lds_dwordx4 v[196:197], off
	s_waitcnt vmcnt(8)
	s_waitcnt lgkmcnt(0)
	s_barrier
	s_setprio 1
	s_waitcnt lgkmcnt(0)
	v_mfma_f32_16x16x32_bf16 v[128:131], v[150:153], v[184:187], v[128:131]
	v_mfma_f32_16x16x32_bf16 v[124:127], v[160:163], v[184:187], v[124:127]
	v_mfma_f32_16x16x32_bf16 v[112:115], v[150:153], v[192:195], v[112:115]
	v_mfma_f32_16x16x32_bf16 v[108:111], v[160:163], v[192:195], v[108:111]
	v_mfma_f32_16x16x32_bf16 v[96:99], v[150:153], v[226:229], v[96:99]
	v_mfma_f32_16x16x32_bf16 v[92:95], v[160:163], v[226:229], v[92:95]
	v_mfma_f32_16x16x32_bf16 v[80:83], v[150:153], v[234:237], v[80:83]
	v_mfma_f32_16x16x32_bf16 v[76:79], v[160:163], v[234:237], v[76:79]
	v_mfma_f32_16x16x32_bf16 v[128:131], v[156:159], v[188:191], v[128:131]
	v_mfma_f32_16x16x32_bf16 v[124:127], v[164:167], v[188:191], v[124:127]
	v_mfma_f32_16x16x32_bf16 v[112:115], v[156:159], v[210:213], v[112:115]
	v_mfma_f32_16x16x32_bf16 v[108:111], v[164:167], v[210:213], v[108:111]
	v_mfma_f32_16x16x32_bf16 v[96:99], v[156:159], v[230:233], v[96:99]
	v_mfma_f32_16x16x32_bf16 v[92:95], v[164:167], v[230:233], v[92:95]
	v_mfma_f32_16x16x32_bf16 v[80:83], v[156:159], v[238:241], v[80:83]
	v_mfma_f32_16x16x32_bf16 v[76:79], v[164:167], v[238:241], v[76:79]
	s_setprio 0
	s_setprio 1
	v_mfma_f32_16x16x32_bf16 v[120:123], v[168:171], v[184:187], v[120:123]
	v_mfma_f32_16x16x32_bf16 v[116:119], v[176:179], v[184:187], v[116:119]
	v_mfma_f32_16x16x32_bf16 v[104:107], v[168:171], v[192:195], v[104:107]
	v_mfma_f32_16x16x32_bf16 v[100:103], v[176:179], v[192:195], v[100:103]
	v_mfma_f32_16x16x32_bf16 v[88:91], v[168:171], v[226:229], v[88:91]
	v_mfma_f32_16x16x32_bf16 v[84:87], v[176:179], v[226:229], v[84:87]
	v_mfma_f32_16x16x32_bf16 v[72:75], v[168:171], v[234:237], v[72:75]
	v_mfma_f32_16x16x32_bf16 v[68:71], v[176:179], v[234:237], v[68:71]
	v_mfma_f32_16x16x32_bf16 v[120:123], v[172:175], v[188:191], v[120:123]
	v_mfma_f32_16x16x32_bf16 v[116:119], v[180:183], v[188:191], v[116:119]
	v_mfma_f32_16x16x32_bf16 v[104:107], v[172:175], v[210:213], v[104:107]
	v_mfma_f32_16x16x32_bf16 v[100:103], v[180:183], v[210:213], v[100:103]
	v_mfma_f32_16x16x32_bf16 v[88:91], v[172:175], v[230:233], v[88:91]
	v_mfma_f32_16x16x32_bf16 v[84:87], v[180:183], v[230:233], v[84:87]
	v_mfma_f32_16x16x32_bf16 v[72:75], v[172:175], v[238:241], v[72:75]
	v_mfma_f32_16x16x32_bf16 v[68:71], v[180:183], v[238:241], v[68:71]
	s_setprio 0
	s_barrier
	s_add_i32 s49, s49, s30
	v_lshl_add_u64 v[196:197], s[24:25], 0, v[134:135]
	s_mov_b32 m0, s49
	ds_read_b128 v[184:187], v155 offset:16384
	ds_read_b128 v[188:191], v155 offset:17408
	ds_read_b128 v[192:195], v155 offset:18432
	ds_read_b128 v[210:213], v155 offset:19456
	ds_read_b128 v[226:229], v155 offset:20480
	ds_read_b128 v[230:233], v155 offset:21504
	ds_read_b128 v[234:237], v155 offset:22528
	ds_read_b128 v[238:241], v155 offset:23552
	global_load_lds_dwordx4 v[196:197], off
	s_add_i32 m0, s49, 0x2000
	s_add_u32 s50, s24, 0x40000
	v_lshl_add_u64 v[242:243], s[24:25], 0, v[138:139]
	s_addc_u32 s51, s25, 0
	s_add_i32 s49, s52, s30
	global_load_lds_dwordx4 v[242:243], off
	v_lshl_add_u64 v[244:245], s[50:51], 0, v[134:135]
	s_mov_b32 m0, s49
	v_lshl_add_u64 v[246:247], s[26:27], 0, v[136:137]
	global_load_lds_dwordx4 v[244:245], off
	v_lshl_add_u64 v[244:245], s[50:51], 0, v[138:139]
	s_add_i32 m0, s49, 0x2000
	s_nop 0
	global_load_lds_dwordx4 v[244:245], off
	v_lshl_add_u64 v[244:245], s[26:27], 0, v[132:133]
	s_waitcnt vmcnt(6)
	s_waitcnt lgkmcnt(0)
	s_barrier
; #define PG8_STAGE(bufoff, gbase, voff) do { _Pragma("unroll") for (int _i = 0; _i < 2; ++_i) \
;         __builtin_amdgcn_global_load_lds((const unsigned*)((const char*)(gbase) + (voff)[_i]), (PG8_LAS unsigned*)(lds + (bufoff) + ldsw + _i * 8192), 16, 0, 0); } while (0)
; #define PG8_LDA(dst, b, h) do { _Pragma("unroll") for (int m = 0; m < 4; ++m) _Pragma("unroll") for (int k = 0; k < 2; ++k) dst[m][k] = *(const PG8_LAS bf16x8*)(lds + PG8_SA(b, h) + aoff + m * 2048 + k * 1024); } while (0)
; #define PG8_LDB(dst, b, h) do { _Pragma("unroll") for (int n = 0; n < 2; ++n) _Pragma("unroll") for (int k = 0; k < 2; ++k) dst[n][k] = *(const PG8_LAS bf16x8*)(lds + PG8_SB(b, h) + boff + n * 2048 + k * 1024); } while (0)
; #define PG8_MMA(ai, bj, At, Bt) do { __builtin_amdgcn_s_setprio(1); _Pragma("unroll") for (int m = 0; m < 4; ++m) _Pragma("unroll") for (int n = 0; n < 2; ++n) _Pragma("unroll") for (int k = 0; k < 2; ++k) \
;         acc[ai][bj][m][n] = __builtin_amdgcn_mfma_f32_16x16x32_bf16(Bt[n][k], At[m][k], acc[ai][bj][m][n], 0, 0, 0); __builtin_amdgcn_s_setprio(0); } while (0)
; #define PG8_WAIT_V(n) asm volatile("s_waitcnt vmcnt(" #n ")" ::: "memory")
; #define PG8_WAIT_L(n) asm volatile("s_waitcnt lgkmcnt(" #n ")" ::: "memory")
; #define PG8_BAR __builtin_amdgcn_s_barrier()
; #define PG8_SCHED __builtin_amdgcn_sched_barrier(0)
; template <class Epi, class Sched, bool ALIGN_EPI = false, bool SP2 = false>
; __device__ __forceinline__ void gemm_phase(PG8_LAS unsigned char* lds, const Gemm g, const Sched& S, const Epi& E) {
;     ...
;             PG8_LDB(B0, 0, 0); PG8_LDB(B1, 0, 1); PG8_SCHED; PG8_LDA(At, 0, 0); PG8_STAGE(PG8_SA(1, 1), a1 + hstepA, voffA);
;             PG8_WAIT_V(8); PG8_WAIT_L(0); PG8_BAR; PG8_MMA(0, 0, At, B0); PG8_MMA(0, 1, At, B1); PG8_BAR; PG8_SCHED;
;             PG8_LDA(At, 0, 1); PG8_STAGE(PG8_SB(0, 0), b2, voffB); PG8_STAGE(PG8_SB(0, 1), b2 + hstepB, voffB); PG8_STAGE(PG8_SA(0, 0), a2, voffA);
;             PG8_WAIT_V(8); PG8_WAIT_L(0); PG8_BAR; PG8_MMA(1, 0, At, B0); PG8_MMA(1, 1, At, B1); PG8_BAR; PG8_SCHED;
;             PG8_LDB(B0, 1, 0); PG8_LDB(B1, 1, 1); PG8_SCHED; PG8_LDA(At, 1, 0); PG8_STAGE(PG8_SA(0, 1), a2 + hstepA, voffA);
;             PG8_WAIT_V(8); PG8_WAIT_L(0); PG8_BAR; PG8_MMA(0, 0, At, B0); PG8_MMA(0, 1, At, B1); PG8_BAR; PG8_SCHED;
	s_setprio 1
	s_waitcnt lgkmcnt(0)
	v_mfma_f32_16x16x32_bf16 v[64:67], v[150:153], v[184:187], v[64:67]
	v_mfma_f32_16x16x32_bf16 v[60:63], v[160:163], v[184:187], v[60:63]
	v_mfma_f32_16x16x32_bf16 v[52:55], v[150:153], v[192:195], v[52:55]
	v_mfma_f32_16x16x32_bf16 v[44:47], v[160:163], v[192:195], v[44:47]
	v_mfma_f32_16x16x32_bf16 v[36:39], v[150:153], v[226:229], v[36:39]
	v_mfma_f32_16x16x32_bf16 v[28:31], v[160:163], v[226:229], v[28:31]
	v_mfma_f32_16x16x32_bf16 v[20:23], v[150:153], v[234:237], v[20:23]
	v_mfma_f32_16x16x32_bf16 v[12:15], v[160:163], v[234:237], v[12:15]
	v_mfma_f32_16x16x32_bf16 v[64:67], v[156:159], v[188:191], v[64:67]
	v_mfma_f32_16x16x32_bf16 v[60:63], v[164:167], v[188:191], v[60:63]
	v_mfma_f32_16x16x32_bf16 v[52:55], v[156:159], v[210:213], v[52:55]
	v_mfma_f32_16x16x32_bf16 v[44:47], v[164:167], v[210:213], v[44:47]
	v_mfma_f32_16x16x32_bf16 v[36:39], v[156:159], v[230:233], v[36:39]
	v_mfma_f32_16x16x32_bf16 v[28:31], v[164:167], v[230:233], v[28:31]
	v_mfma_f32_16x16x32_bf16 v[20:23], v[156:159], v[238:241], v[20:23]
	v_mfma_f32_16x16x32_bf16 v[12:15], v[164:167], v[238:241], v[12:15]
	s_setprio 0
	s_setprio 1
	v_mfma_f32_16x16x32_bf16 v[56:59], v[168:171], v[184:187], v[56:59]
	v_mfma_f32_16x16x32_bf16 v[48:51], v[176:179], v[184:187], v[48:51]
	v_mfma_f32_16x16x32_bf16 v[40:43], v[168:171], v[192:195], v[40:43]
	v_mfma_f32_16x16x32_bf16 v[32:35], v[176:179], v[192:195], v[32:35]
	v_mfma_f32_16x16x32_bf16 v[24:27], v[168:171], v[226:229], v[24:27]
	v_mfma_f32_16x16x32_bf16 v[16:19], v[176:179], v[226:229], v[16:19]
	v_mfma_f32_16x16x32_bf16 v[8:11], v[168:171], v[234:237], v[8:11]
	v_mfma_f32_16x16x32_bf16 v[4:7], v[176:179], v[234:237], v[4:7]
	v_mfma_f32_16x16x32_bf16 v[56:59], v[172:175], v[188:191], v[56:59]
	v_mfma_f32_16x16x32_bf16 v[48:51], v[180:183], v[188:191], v[48:51]
	v_mfma_f32_16x16x32_bf16 v[40:43], v[172:175], v[210:213], v[40:43]
	v_mfma_f32_16x16x32_bf16 v[32:35], v[180:183], v[210:213], v[32:35]
	v_mfma_f32_16x16x32_bf16 v[24:27], v[172:175], v[230:233], v[24:27]
	v_mfma_f32_16x16x32_bf16 v[16:19], v[180:183], v[230:233], v[16:19]
	v_mfma_f32_16x16x32_bf16 v[8:11], v[172:175], v[238:241], v[8:11]
	v_mfma_f32_16x16x32_bf16 v[4:7], v[180:183], v[238:241], v[4:7]
	s_setprio 0
	s_barrier
	s_add_i32 s49, 0, 0x18000
	v_add_u32_e32 v149, s49, v154
	s_add_i32 s50, 0, 0x1c000
	ds_read_b128 v[150:153], v149
	ds_read_b128 v[156:159], v149 offset:1024
	ds_read_b128 v[160:163], v149 offset:2048
	ds_read_b128 v[164:167], v149 offset:3072
	v_add_u32_e32 v149, s50, v154
	ds_read_b128 v[168:171], v149
	ds_read_b128 v[172:175], v149 offset:1024
	ds_read_b128 v[176:179], v149 offset:2048
	ds_read_b128 v[180:183], v149 offset:3072
	s_add_u32 s26, s26, 0x40000
	s_addc_u32 s27, s27, 0
	s_mov_b32 m0, s34
	v_lshl_add_u64 v[248:249], s[26:27], 0, v[132:133]
	ds_read_b128 v[184:187], v155 offset:32768
	ds_read_b128 v[188:191], v155 offset:33792
	ds_read_b128 v[192:195], v155 offset:34816
	ds_read_b128 v[210:213], v155 offset:35840
	ds_read_b128 v[226:229], v155 offset:36864
	ds_read_b128 v[230:233], v155 offset:37888
	ds_read_b128 v[234:237], v155 offset:38912
	ds_read_b128 v[238:241], v155 offset:39936
	s_mov_b32 m0, s31
	s_nop 0
	global_load_lds_dwordx4 v[244:245], off
	s_mov_b32 m0, s33
	s_nop 0
	global_load_lds_dwordx4 v[246:247], off
	s_mov_b32 m0, s34
	s_nop 0
	global_load_lds_dwordx4 v[248:249], off
	v_lshl_add_u64 v[248:249], s[26:27], 0, v[136:137]
	s_mov_b32 m0, s35
	s_nop 0
	global_load_lds_dwordx4 v[248:249], off
	s_waitcnt vmcnt(8)
	s_waitcnt lgkmcnt(0)
	s_barrier
; #define PG8_STAGE(bufoff, gbase, voff) do { _Pragma("unroll") for (int _i = 0; _i < 2; ++_i) \
;         __builtin_amdgcn_global_load_lds((const unsigned*)((const char*)(gbase) + (voff)[_i]), (PG8_LAS unsigned*)(lds + (bufoff) + ldsw + _i * 8192), 16, 0, 0); } while (0)
; #define PG8_LDA(dst, b, h) do { _Pragma("unroll") for (int m = 0; m < 4; ++m) _Pragma("unroll") for (int k = 0; k < 2; ++k) dst[m][k] = *(const PG8_LAS bf16x8*)(lds + PG8_SA(b, h) + aoff + m * 2048 + k * 1024); } while (0)
; #define PG8_MMA(ai, bj, At, Bt) do { __builtin_amdgcn_s_setprio(1); _Pragma("unroll") for (int m = 0; m < 4; ++m) _Pragma("unroll") for (int n = 0; n < 2; ++n) _Pragma("unroll") for (int k = 0; k < 2; ++k) \
;         acc[ai][bj][m][n] = __builtin_amdgcn_mfma_f32_16x16x32_bf16(Bt[n][k], At[m][k], acc[ai][bj][m][n], 0, 0, 0); __builtin_amdgcn_s_setprio(0); } while (0)
; #define PG8_WAIT_V(n) asm volatile("s_waitcnt vmcnt(" #n ")" ::: "memory")
; #define PG8_WAIT_L(n) asm volatile("s_waitcnt lgkmcnt(" #n ")" ::: "memory")
; #define PG8_BAR __builtin_amdgcn_s_barrier()
; #define PG8_SCHED __builtin_amdgcn_sched_barrier(0)
; template <class Epi, class Sched, bool ALIGN_EPI = false, bool SP2 = false>
; __device__ __forceinline__ void gemm_phase(PG8_LAS unsigned char* lds, const Gemm g, const Sched& S, const Epi& E) {
;     ...
;             PG8_WAIT_V(8); PG8_WAIT_L(0); PG8_BAR; PG8_MMA(0, 0, At, B0); PG8_MMA(0, 1, At, B1); PG8_BAR; PG8_SCHED;
;             PG8_LDA(At, 1, 1); PG8_STAGE(PG8_SB(1, 0), b3, voffB); PG8_STAGE(PG8_SB(1, 1), b3 + hstepB, voffB); PG8_STAGE(PG8_SA(1, 0), a3, voffA);
;             PG8_WAIT_V(8); PG8_WAIT_L(0); PG8_BAR; PG8_MMA(1, 0, At, B0); PG8_MMA(1, 1, At, B1); PG8_BAR; PG8_SCHED;
;     ...
;         if constexpr (ALIGN_EPI) { if (wr == 0) PG8_BAR; }
	s_setprio 1
	s_waitcnt lgkmcnt(0)
	v_mfma_f32_16x16x32_bf16 v[128:131], v[150:153], v[184:187], v[128:131]
	v_mfma_f32_16x16x32_bf16 v[124:127], v[160:163], v[184:187], v[124:127]
	v_mfma_f32_16x16x32_bf16 v[112:115], v[150:153], v[192:195], v[112:115]
	v_mfma_f32_16x16x32_bf16 v[108:111], v[160:163], v[192:195], v[108:111]
	v_mfma_f32_16x16x32_bf16 v[96:99], v[150:153], v[226:229], v[96:99]
	v_mfma_f32_16x16x32_bf16 v[92:95], v[160:163], v[226:229], v[92:95]
	v_mfma_f32_16x16x32_bf16 v[80:83], v[150:153], v[234:237], v[80:83]
	v_mfma_f32_16x16x32_bf16 v[76:79], v[160:163], v[234:237], v[76:79]
	v_mfma_f32_16x16x32_bf16 v[128:131], v[156:159], v[188:191], v[128:131]
	v_mfma_f32_16x16x32_bf16 v[124:127], v[164:167], v[188:191], v[124:127]
	v_mfma_f32_16x16x32_bf16 v[112:115], v[156:159], v[210:213], v[112:115]
	v_mfma_f32_16x16x32_bf16 v[108:111], v[164:167], v[210:213], v[108:111]
	v_mfma_f32_16x16x32_bf16 v[96:99], v[156:159], v[230:233], v[96:99]
	v_mfma_f32_16x16x32_bf16 v[92:95], v[164:167], v[230:233], v[92:95]
	v_mfma_f32_16x16x32_bf16 v[80:83], v[156:159], v[238:241], v[80:83]
	v_mfma_f32_16x16x32_bf16 v[76:79], v[164:167], v[238:241], v[76:79]
	s_setprio 0
	s_setprio 1
	v_mfma_f32_16x16x32_bf16 v[120:123], v[168:171], v[184:187], v[120:123]
	v_mfma_f32_16x16x32_bf16 v[116:119], v[176:179], v[184:187], v[116:119]
	v_mfma_f32_16x16x32_bf16 v[104:107], v[168:171], v[192:195], v[104:107]
	v_mfma_f32_16x16x32_bf16 v[100:103], v[176:179], v[192:195], v[100:103]
	v_mfma_f32_16x16x32_bf16 v[88:91], v[168:171], v[226:229], v[88:91]
	v_mfma_f32_16x16x32_bf16 v[84:87], v[176:179], v[226:229], v[84:87]
	v_mfma_f32_16x16x32_bf16 v[72:75], v[168:171], v[234:237], v[72:75]
	v_mfma_f32_16x16x32_bf16 v[68:71], v[176:179], v[234:237], v[68:71]
	v_mfma_f32_16x16x32_bf16 v[120:123], v[172:175], v[188:191], v[120:123]
	v_mfma_f32_16x16x32_bf16 v[116:119], v[180:183], v[188:191], v[116:119]
	v_mfma_f32_16x16x32_bf16 v[104:107], v[172:175], v[210:213], v[104:107]
	v_mfma_f32_16x16x32_bf16 v[100:103], v[180:183], v[210:213], v[100:103]
	v_mfma_f32_16x16x32_bf16 v[88:91], v[172:175], v[230:233], v[88:91]
	v_mfma_f32_16x16x32_bf16 v[84:87], v[180:183], v[230:233], v[84:87]
	v_mfma_f32_16x16x32_bf16 v[72:75], v[172:175], v[238:241], v[72:75]
	v_mfma_f32_16x16x32_bf16 v[68:71], v[180:183], v[238:241], v[68:71]
	s_setprio 0
	s_barrier
	s_add_i32 s26, s49, s30
	v_lshl_add_u64 v[196:197], v[196:197], 0, s[64:65]
	s_mov_b32 m0, s26
	ds_read_b128 v[184:187], v155 offset:49152
	ds_read_b128 v[188:191], v155 offset:50176
	ds_read_b128 v[192:195], v155 offset:51200
	ds_read_b128 v[210:213], v155 offset:52224
	ds_read_b128 v[226:229], v155 offset:53248
	ds_read_b128 v[230:233], v155 offset:54272
	ds_read_b128 v[234:237], v155 offset:55296
	ds_read_b128 v[238:241], v155 offset:56320
	global_load_lds_dwordx4 v[196:197], off
	s_add_i32 m0, s26, 0x2000
	s_add_u32 s24, s24, 0x40080
	v_lshl_add_u64 v[196:197], v[242:243], 0, s[64:65]
	s_addc_u32 s25, s25, 0
	s_add_i32 s26, s50, s30
	global_load_lds_dwordx4 v[196:197], off
	v_lshl_add_u64 v[196:197], s[24:25], 0, v[134:135]
	s_mov_b32 m0, s26
	s_nop 0
	global_load_lds_dwordx4 v[196:197], off
	v_lshl_add_u64 v[196:197], s[24:25], 0, v[138:139]
	s_add_i32 m0, s26, 0x2000
	s_nop 0
	global_load_lds_dwordx4 v[196:197], off
	s_waitcnt vmcnt(6)
	s_waitcnt lgkmcnt(0)
	s_barrier
	s_setprio 1
	s_waitcnt lgkmcnt(0)
	v_mfma_f32_16x16x32_bf16 v[64:67], v[150:153], v[184:187], v[64:67]
	v_mfma_f32_16x16x32_bf16 v[60:63], v[160:163], v[184:187], v[60:63]
	v_mfma_f32_16x16x32_bf16 v[52:55], v[150:153], v[192:195], v[52:55]
	v_mfma_f32_16x16x32_bf16 v[44:47], v[160:163], v[192:195], v[44:47]
	v_mfma_f32_16x16x32_bf16 v[36:39], v[150:153], v[226:229], v[36:39]
	v_mfma_f32_16x16x32_bf16 v[28:31], v[160:163], v[226:229], v[28:31]
	v_mfma_f32_16x16x32_bf16 v[20:23], v[150:153], v[234:237], v[20:23]
	v_mfma_f32_16x16x32_bf16 v[12:15], v[160:163], v[234:237], v[12:15]
	v_mfma_f32_16x16x32_bf16 v[64:67], v[156:159], v[188:191], v[64:67]
	v_mfma_f32_16x16x32_bf16 v[60:63], v[164:167], v[188:191], v[60:63]
	v_mfma_f32_16x16x32_bf16 v[52:55], v[156:159], v[210:213], v[52:55]
	v_mfma_f32_16x16x32_bf16 v[44:47], v[164:167], v[210:213], v[44:47]
	v_mfma_f32_16x16x32_bf16 v[36:39], v[156:159], v[230:233], v[36:39]
	v_mfma_f32_16x16x32_bf16 v[28:31], v[164:167], v[230:233], v[28:31]
	v_mfma_f32_16x16x32_bf16 v[20:23], v[156:159], v[238:241], v[20:23]
	v_mfma_f32_16x16x32_bf16 v[12:15], v[164:167], v[238:241], v[12:15]
	s_setprio 0
	s_setprio 1
	v_mfma_f32_16x16x32_bf16 v[56:59], v[168:171], v[184:187], v[56:59]
	v_mfma_f32_16x16x32_bf16 v[48:51], v[176:179], v[184:187], v[48:51]
	v_mfma_f32_16x16x32_bf16 v[40:43], v[168:171], v[192:195], v[40:43]
	v_mfma_f32_16x16x32_bf16 v[32:35], v[176:179], v[192:195], v[32:35]
	v_mfma_f32_16x16x32_bf16 v[24:27], v[168:171], v[226:229], v[24:27]
	v_mfma_f32_16x16x32_bf16 v[16:19], v[176:179], v[226:229], v[16:19]
	v_mfma_f32_16x16x32_bf16 v[8:11], v[168:171], v[234:237], v[8:11]
	v_mfma_f32_16x16x32_bf16 v[4:7], v[176:179], v[234:237], v[4:7]
	v_mfma_f32_16x16x32_bf16 v[56:59], v[172:175], v[188:191], v[56:59]
	v_mfma_f32_16x16x32_bf16 v[48:51], v[180:183], v[188:191], v[48:51]
	v_mfma_f32_16x16x32_bf16 v[40:43], v[172:175], v[210:213], v[40:43]
	v_mfma_f32_16x16x32_bf16 v[32:35], v[180:183], v[210:213], v[32:35]
	v_mfma_f32_16x16x32_bf16 v[24:27], v[172:175], v[230:233], v[24:27]
	v_mfma_f32_16x16x32_bf16 v[16:19], v[180:183], v[230:233], v[16:19]
	v_mfma_f32_16x16x32_bf16 v[8:11], v[172:175], v[238:241], v[8:11]
	v_mfma_f32_16x16x32_bf16 v[4:7], v[180:183], v[238:241], v[4:7]
	s_setprio 0
	s_barrier
	s_add_i32 s48, s48, 2
	s_add_u32 s46, s46, 0x100
	s_addc_u32 s47, s47, 0
	s_add_u32 s22, s22, 0x100
	s_addc_u32 s23, s23, 0
	s_cmp_gt_u32 s48, 13
	s_cbranch_scc0 .LBB0_1161
	s_and_b64 vcc, exec, s[12:13]
	s_cbranch_vccz .LBB0_1164
	s_barrier

; #define PG8_STAGE(bufoff, gbase, voff) do { _Pragma("unroll") for (int _i = 0; _i < 2; ++_i) \
;         __builtin_amdgcn_global_load_lds((const unsigned*)((const char*)(gbase) + (voff)[_i]), (PG8_LAS unsigned*)(lds + (bufoff) + ldsw + _i * 8192), 16, 0, 0); } while (0)
; #define PG8_WAIT_V(n) asm volatile("s_waitcnt vmcnt(" #n ")" ::: "memory")
; #define PG8_BAR __builtin_amdgcn_s_barrier()
; template <class Epi, class Sched, bool ALIGN_EPI = false, bool SP2 = false>
; __device__ __forceinline__ void gemm_phase(PG8_LAS unsigned char* lds, const Gemm g, const Sched& S, const Epi& E) {
;     ...
;     const int wid = __builtin_amdgcn_readfirstlane(tid >> 6), lane = tid & 63, wr = wid >> 2, wc = wid & 3, fr = lane & 15, fq = lane >> 4;
;     const int K = g.K, nt = K / BK;
;     unsigned voffA[2], voffB[2];
; #pragma unroll
;     for (int i = 0; i < 2; ++i) { int R, C; stage_rc(tid * 16 + i * 8192, R, C); const int Rb = Epi::PERM ? ((R & ~31) + perm32(R & 31)) : R;
;         voffA[i] = (unsigned)(R * g.lda + C) * 2u; voffB[i] = (unsigned)(Rb * g.ldb + C) * 2u; }
;     const size_t kstep = (size_t)(BK * 2);
;     const size_t hstepA = (size_t)HALF * g.lda * 2, hstepB = (size_t)HALF * g.ldb * 2;
;     const size_t tstepA = 2 * hstepA, tstepB = 2 * hstepB;
;     const unsigned ldsw = (unsigned)wid * 1024u;
;     const int aoff = lds_byte(wr * 64 + fr, fq * 8), boff = lds_byte(wc * 32 + fr, fq * 8);
;     ...
;     const char* cA = (const char*)g.A + (size_t)cur.pm * tstepA; const char* cB = (const char*)g.Bt + (size_t)cur.pn * tstepB;
;     S.a_ready(cur);
;     if constexpr (SP2) {
;         PG8_STAGE(PG8_SB(0, 0), cB, voffB); PG8_STAGE(PG8_SB(0, 1), cB + hstepB, voffB); PG8_STAGE(PG8_SA(0, 0), cA, voffA); PG8_STAGE(PG8_SA(0, 1), cA + hstepA, voffA);
;         if (wr == 1) PG8_BAR;
;         PG8_WAIT_V(2); PG8_BAR;
.LBB0_1681:
	v_ashrrev_i32_e32 v4, 31, v18
	v_lshrrev_b32_e32 v4, 26, v4
	v_add_u32_e32 v4, v18, v4
	v_ashrrev_i32_e32 v12, 6, v4
	v_bfe_i32 v4, v18, 27, 1
	v_lshlrev_b32_e32 v2, 4, v18
	v_lshrrev_b32_e32 v4, 22, v4
	v_add_u32_e32 v4, v2, v4
	v_and_b32_e32 v4, 0xfffffc00, v4
	v_sub_u32_e32 v4, v2, v4
	v_lshrrev_b32_e32 v5, 4, v4
	v_bitop3_b32 v4, v5, v4, 32 bitop3:0x6c
	v_ashrrev_i32_e32 v6, 31, v4
	v_lshrrev_b32_e32 v6, 26, v6
	s_add_u32 s27, s2, 0xf000000
	v_readlane_b32 s5, v252, 0
	v_add_u32_e32 v6, v4, v6
	s_addc_u32 s28, s3, 0
	s_lshl_b32 s5, s5, 21
	v_lshlrev_b32_e32 v5, 3, v12
	v_ashrrev_i32_e32 v13, 6, v6
	v_and_b32_e32 v6, 0xc0, v6
	s_add_u32 s5, s2, s5
	v_and_b32_e32 v5, -16, v5
	v_sub_u32_e32 v4, v4, v6
	s_addc_u32 s7, s3, 0
	v_add_u32_e32 v5, v13, v5
	v_ashrrev_i16_sdwa v4, v1, sext(v4) dst_sel:DWORD dst_unused:UNUSED_PAD src0_sel:DWORD src1_sel:BYTE_0
	s_add_u32 s29, s5, 0x9700000
	v_lshlrev_b32_e32 v7, 5, v12
	v_bfe_i32 v14, v4, 0, 16
	v_lshlrev_b32_e32 v4, 1, v5
	v_lshrrev_b32_e32 v6, 2, v5
	v_and_b32_e32 v8, 3, v13
	s_addc_u32 s30, s7, 0
	v_and_b32_e32 v7, 32, v7
	v_and_b32_e32 v4, 24, v4
	v_and_b32_e32 v6, 4, v6
	v_and_or_b32 v8, v5, s75, v8
	s_add_i32 s4, s6, s4
	v_or3_b32 v4, v8, v6, v4
	v_add_lshl_u32 v6, v7, v14, 1
	v_add_u32_e32 v2, 0x2000, v2
	s_ashr_i32 s5, s4, 31
	v_lshl_add_u32 v134, v4, 11, v6
	v_ashrrev_i32_e32 v4, 31, v2
	s_lshr_b32 s5, s5, 27
	v_lshrrev_b32_e32 v4, 22, v4
	s_add_i32 s5, s4, s5
	v_add_u32_e32 v4, v2, v4
	s_ashr_i32 s6, s5, 5
	s_and_b32 s5, s5, 0xffe0
	v_ashrrev_i32_e32 v15, 10, v4
	s_sub_i32 s4, s4, s5
	v_mul_i32_i24_e32 v4, 0x400, v15
	s_bfe_i32 s5, s4, 0x80000
	v_sub_u32_e32 v2, v2, v4
	s_bfe_u32 s5, s5, 0x3000c
	v_lshrrev_b32_e32 v4, 4, v2
	s_add_i32 s5, s4, s5
	v_bitop3_b32 v2, v4, v2, 32 bitop3:0x6c
	s_lshl_b32 s7, s6, 3
	s_bfe_i32 s6, s5, 0x80000
	s_and_b32 s5, s5, 0xf8
	v_lshl_add_u32 v132, v5, 11, v6
	v_ashrrev_i32_e32 v5, 31, v2
	s_sub_i32 s4, s4, s5
	v_lshrrev_b32_e32 v5, 26, v5
	s_sext_i32_i16 s6, s6
	s_sext_i32_i8 s4, s4
	v_add_u32_e32 v5, v2, v5
	s_lshr_b32 s6, s6, 3
	s_add_i32 s14, s7, s4
	s_ashr_i32 s9, s8, 6
	v_lshlrev_b32_e32 v4, 3, v15
	v_ashrrev_i32_e32 v16, 6, v5
	v_and_b32_e32 v5, 0xc0, v5
	s_ashr_i32 s15, s14, 31
	s_bfe_i64 s[12:13], s[6:7], 0x100000
	v_and_b32_e32 v4, -16, v4
	v_sub_u32_e32 v2, v2, v5
	s_ashr_i32 s10, s8, 8
	s_lshl_b32 s31, s9, 10
	s_lshl_b64 s[4:5], s[14:15], 19
	s_lshl_b64 s[12:13], s[12:13], 19
	v_add_u32_e32 v4, v16, v4
	v_ashrrev_i16_sdwa v2, v1, sext(v2) dst_sel:DWORD dst_unused:UNUSED_PAD src0_sel:DWORD src1_sel:BYTE_0
	s_add_u32 s20, s29, s12
	v_lshlrev_b32_e32 v6, 5, v15
	v_bfe_i32 v17, v2, 0, 16
	v_lshlrev_b32_e32 v2, 1, v4
	v_lshrrev_b32_e32 v5, 2, v4
	v_and_b32_e32 v7, 3, v16
	s_addc_u32 s21, s30, s13
	s_add_i32 s15, s31, 0
	v_and_b32_e32 v6, 32, v6
	v_and_b32_e32 v2, 24, v2
	v_and_b32_e32 v5, 4, v5
	v_and_or_b32 v7, v4, s75, v7
	s_add_i32 m0, s15, 0x10000
	v_or3_b32 v2, v7, v5, v2
	v_add_lshl_u32 v5, v6, v17, 1
	global_load_lds_dwordx4 v134, s[20:21]
	s_add_i32 m0, s15, 0x12000
	v_lshl_add_u32 v138, v2, 11, v5
	s_add_u32 s12, s20, 0x40000
	global_load_lds_dwordx4 v138, s[20:21]
	s_addc_u32 s13, s21, 0
	s_add_i32 m0, s15, 0x14000
	v_lshl_add_u32 v136, v4, 11, v5
	global_load_lds_dwordx4 v134, s[12:13]
	s_add_i32 m0, s15, 0x16000
	s_add_u32 s22, s27, s4
	s_addc_u32 s23, s28, s5
	s_add_i32 s33, s15, 0x2000
	global_load_lds_dwordx4 v138, s[12:13]
	s_mov_b32 m0, s15
	s_add_u32 s4, s22, 0x40000
	global_load_lds_dwordx4 v132, s[22:23]
	s_mov_b32 m0, s33
	s_addc_u32 s5, s23, 0
	s_add_i32 s34, s15, 0x4000
	global_load_lds_dwordx4 v136, s[22:23]
	s_mov_b32 m0, s34
	s_add_i32 s35, s15, 0x6000
	global_load_lds_dwordx4 v132, s[4:5]
	s_mov_b32 m0, s35
	v_mov_b32_e32 v135, v3
	global_load_lds_dwordx4 v136, s[4:5]
	v_mov_b32_e32 v139, v3
	v_mov_b32_e32 v133, v3
	v_mov_b32_e32 v137, v3
	s_cmp_eq_u32 s10, 1
	v_lshl_add_u64 v[10:11], s[20:21], 0, v[134:135]
	v_lshl_add_u64 v[8:9], s[20:21], 0, v[138:139]
	v_lshl_add_u64 v[4:5], s[22:23], 0, v[132:133]
	s_cselect_b64 s[4:5], -1, 0
	s_cmp_lg_u32 s10, 1
	v_lshl_add_u64 v[6:7], s[22:23], 0, v[136:137]
	v_lshl_add_u64 v[240:241], s[22:23], 0, v[132:133]
	v_lshl_add_u64 v[242:243], s[22:23], 0, v[136:137]
	s_cbranch_scc1 .LBB0_1683
	s_barrier

; #define PG8_STR(x) PG8_STR2(x)
; #define PG8_STAGE(bufoff, gbase, voff) do { _Pragma("unroll") for (int _i = 0; _i < 2; ++_i) \
;         __builtin_amdgcn_global_load_lds((const unsigned*)((const char*)(gbase) + (voff)[_i]), (PG8_LAS unsigned*)(lds + (bufoff) + ldsw + _i * 8192), 16, 0, 0); } while (0)
; #define PG8_LDA(dst, b, h) do { _Pragma("unroll") for (int m = 0; m < 4; ++m) _Pragma("unroll") for (int k = 0; k < 2; ++k) dst[m][k] = *(const PG8_LAS bf16x8*)(lds + PG8_SA(b, h) + aoff + m * 2048 + k * 1024); } while (0)
; #define PG8_LDB(dst, b, h) do { _Pragma("unroll") for (int n = 0; n < 2; ++n) _Pragma("unroll") for (int k = 0; k < 2; ++k) dst[n][k] = *(const PG8_LAS bf16x8*)(lds + PG8_SB(b, h) + boff + n * 2048 + k * 1024); } while (0)
; #define PG8_MMA(ai, bj, At, Bt) do { __builtin_amdgcn_s_setprio(1); _Pragma("unroll") for (int m = 0; m < 4; ++m) _Pragma("unroll") for (int n = 0; n < 2; ++n) _Pragma("unroll") for (int k = 0; k < 2; ++k) \
;         acc[ai][bj][m][n] = __builtin_amdgcn_mfma_f32_16x16x32_bf16(Bt[n][k], At[m][k], acc[ai][bj][m][n], 0, 0, 0); __builtin_amdgcn_s_setprio(0); } while (0)
; template <class Epi, class Sched, bool ALIGN_EPI = false, bool SP2 = false>
; __device__ __forceinline__ void gemm_phase(PG8_LAS unsigned char* lds, const Gemm g, const Sched& S, const Epi& E) {
;     ...
;         for (int t = 0; t < nt; t += 2) {
;     ...
;             asm volatile(".p2align 6\n\t.rept " PG8_STR(KLOOP_ALIGN) "\n\ts_nop 0\n\t.endr");
;     ...
;             const bool last = (t == nt - 2);
;             const char* a1 = cA + (size_t)(t + 1) * kstep;
;             const char* a2 = last ? nA : cA + (size_t)(t + 2) * kstep; const char* b2 = last ? nB : cB + (size_t)(t + 2) * kstep;
;             const char* a3 = a2 + kstep; const char* b3 = b2 + kstep;
;             if (last && has_next) S.a_ready(nxt);
;             if constexpr (SP2) {
;             PG8_LDB(B0, 0, 0); PG8_LDB(B1, 0, 1); PG8_SCHED; PG8_LDA(At, 0, 0); PG8_STAGE(PG8_SA(1, 1), a1 + hstepA, voffA);
;             PG8_WAIT_V(8); PG8_WAIT_L(0); PG8_BAR; PG8_MMA(0, 0, At, B0); PG8_MMA(0, 1, At, B1); PG8_BAR; PG8_SCHED;
;             PG8_LDA(At, 0, 1); PG8_STAGE(PG8_SB(0, 0), b2, voffB); PG8_STAGE(PG8_SB(0, 1), b2 + hstepB, voffB); PG8_STAGE(PG8_SA(0, 0), a2, voffA);
;             PG8_WAIT_V(8); PG8_WAIT_L(0); PG8_BAR; PG8_MMA(1, 0, At, B0); PG8_MMA(1, 1, At, B1); PG8_BAR; PG8_SCHED;
.LBB0_1693:
	s_add_u32 s22, s20, 0xfffc0080
	s_addc_u32 s23, s21, -1
	s_add_i32 s46, 0, 0x10000
	s_cmp_eq_u32 s45, 12
	s_cselect_b32 s25, s13, s23
	s_cselect_b32 s24, s41, s22
	v_add_u32_e32 v144, s46, v146
	s_cselect_b32 s23, s11, s44
	s_cselect_b32 s22, s42, s43
	s_add_i32 s48, 0, 0x14000
	ds_read_b128 v[150:153], v144
	ds_read_b128 v[154:157], v144 offset:1024
	ds_read_b128 v[158:161], v144 offset:2048
	ds_read_b128 v[162:165], v144 offset:3072
	v_add_u32_e32 v144, s48, v146
	ds_read_b128 v[166:169], v144
	ds_read_b128 v[170:173], v144 offset:1024
	ds_read_b128 v[174:177], v144 offset:2048
	ds_read_b128 v[178:181], v144 offset:3072
	v_lshl_add_u64 v[144:145], s[20:21], 0, v[142:143]
	s_add_i32 m0, s15, 0xc000
	ds_read_b128 v[182:185], v148
	ds_read_b128 v[186:189], v148 offset:1024
	ds_read_b128 v[190:193], v148 offset:2048
	ds_read_b128 v[194:197], v148 offset:3072
	ds_read_b128 v[210:213], v148 offset:4096
	ds_read_b128 v[226:229], v148 offset:5120
	ds_read_b128 v[230:233], v148 offset:6144
	ds_read_b128 v[234:237], v148 offset:7168
	v_lshl_add_u64 v[244:245], v[240:241], 0, s[64:65]
	s_mov_b32 m0, s36
	s_nop 0
	global_load_lds_dwordx4 v[244:245], off
	v_lshl_add_u64 v[244:245], v[242:243], 0, s[64:65]
	s_mov_b32 m0, s37
	s_nop 0
	global_load_lds_dwordx4 v[244:245], off
	s_add_i32 m0, s15, 0xc000
	s_nop 0
	global_load_lds_dwordx4 v[144:145], off
	v_lshl_add_u64 v[144:145], s[20:21], 0, v[140:141]
	s_add_i32 m0, s15, 0xe000
	s_nop 0
	global_load_lds_dwordx4 v[144:145], off
	s_waitcnt vmcnt(8)
	s_waitcnt lgkmcnt(0)
	s_barrier
	s_setprio 1
	s_waitcnt lgkmcnt(0)
	v_mfma_f32_16x16x32_bf16 v[128:131], v[150:153], v[182:185], v[128:131]
	v_mfma_f32_16x16x32_bf16 v[124:127], v[158:161], v[182:185], v[124:127]
	v_mfma_f32_16x16x32_bf16 v[120:123], v[150:153], v[190:193], v[120:123]
	v_mfma_f32_16x16x32_bf16 v[112:115], v[158:161], v[190:193], v[112:115]
	v_mfma_f32_16x16x32_bf16 v[104:107], v[150:153], v[210:213], v[104:107]
	v_mfma_f32_16x16x32_bf16 v[96:99], v[158:161], v[210:213], v[96:99]
	v_mfma_f32_16x16x32_bf16 v[88:91], v[150:153], v[230:233], v[88:91]
	v_mfma_f32_16x16x32_bf16 v[80:83], v[158:161], v[230:233], v[80:83]
	v_mfma_f32_16x16x32_bf16 v[128:131], v[154:157], v[186:189], v[128:131]
	v_mfma_f32_16x16x32_bf16 v[124:127], v[162:165], v[186:189], v[124:127]
	v_mfma_f32_16x16x32_bf16 v[120:123], v[154:157], v[194:197], v[120:123]
	v_mfma_f32_16x16x32_bf16 v[112:115], v[162:165], v[194:197], v[112:115]
	v_mfma_f32_16x16x32_bf16 v[104:107], v[154:157], v[226:229], v[104:107]
	v_mfma_f32_16x16x32_bf16 v[96:99], v[162:165], v[226:229], v[96:99]
	v_mfma_f32_16x16x32_bf16 v[88:91], v[154:157], v[234:237], v[88:91]
	v_mfma_f32_16x16x32_bf16 v[80:83], v[162:165], v[234:237], v[80:83]
	s_setprio 0
	s_setprio 1
	v_mfma_f32_16x16x32_bf16 v[116:119], v[166:169], v[182:185], v[116:119]
	v_mfma_f32_16x16x32_bf16 v[108:111], v[174:177], v[182:185], v[108:111]
	v_mfma_f32_16x16x32_bf16 v[100:103], v[166:169], v[190:193], v[100:103]
	v_mfma_f32_16x16x32_bf16 v[92:95], v[174:177], v[190:193], v[92:95]
	v_mfma_f32_16x16x32_bf16 v[84:87], v[166:169], v[210:213], v[84:87]
	v_mfma_f32_16x16x32_bf16 v[76:79], v[174:177], v[210:213], v[76:79]
	v_mfma_f32_16x16x32_bf16 v[72:75], v[166:169], v[230:233], v[72:75]
	v_mfma_f32_16x16x32_bf16 v[68:71], v[174:177], v[230:233], v[68:71]
	v_mfma_f32_16x16x32_bf16 v[116:119], v[170:173], v[186:189], v[116:119]
	v_mfma_f32_16x16x32_bf16 v[108:111], v[178:181], v[186:189], v[108:111]
	v_mfma_f32_16x16x32_bf16 v[100:103], v[170:173], v[194:197], v[100:103]
	v_mfma_f32_16x16x32_bf16 v[92:95], v[178:181], v[194:197], v[92:95]
	v_mfma_f32_16x16x32_bf16 v[84:87], v[170:173], v[226:229], v[84:87]
	v_mfma_f32_16x16x32_bf16 v[76:79], v[178:181], v[226:229], v[76:79]
	v_mfma_f32_16x16x32_bf16 v[72:75], v[170:173], v[234:237], v[72:75]
	v_mfma_f32_16x16x32_bf16 v[68:71], v[178:181], v[234:237], v[68:71]
	s_setprio 0
	s_barrier
	s_add_i32 s46, s46, s31
	v_lshl_add_u64 v[144:145], s[22:23], 0, v[134:135]
	s_mov_b32 m0, s46
	ds_read_b128 v[182:185], v148 offset:16384
	ds_read_b128 v[186:189], v148 offset:17408
	ds_read_b128 v[190:193], v148 offset:18432
	ds_read_b128 v[194:197], v148 offset:19456
	ds_read_b128 v[210:213], v148 offset:20480
	ds_read_b128 v[226:229], v148 offset:21504
	ds_read_b128 v[230:233], v148 offset:22528
	ds_read_b128 v[234:237], v148 offset:23552
	global_load_lds_dwordx4 v[144:145], off
	s_add_i32 m0, s46, 0x2000
	s_add_u32 s46, s22, 0x40000
	v_lshl_add_u64 v[238:239], s[22:23], 0, v[138:139]
	s_addc_u32 s47, s23, 0
	s_add_i32 s48, s48, s31
	global_load_lds_dwordx4 v[238:239], off
	v_lshl_add_u64 v[240:241], s[46:47], 0, v[134:135]
	s_mov_b32 m0, s48
	v_lshl_add_u64 v[242:243], s[24:25], 0, v[136:137]
	global_load_lds_dwordx4 v[240:241], off
	v_lshl_add_u64 v[240:241], s[46:47], 0, v[138:139]
	s_add_i32 m0, s48, 0x2000
	s_nop 0
	global_load_lds_dwordx4 v[240:241], off
	v_lshl_add_u64 v[240:241], s[24:25], 0, v[132:133]
	s_waitcnt vmcnt(6)
	s_waitcnt lgkmcnt(0)
	s_barrier
; #define PG8_STAGE(bufoff, gbase, voff) do { _Pragma("unroll") for (int _i = 0; _i < 2; ++_i) \
;         __builtin_amdgcn_global_load_lds((const unsigned*)((const char*)(gbase) + (voff)[_i]), (PG8_LAS unsigned*)(lds + (bufoff) + ldsw + _i * 8192), 16, 0, 0); } while (0)
; #define PG8_LDA(dst, b, h) do { _Pragma("unroll") for (int m = 0; m < 4; ++m) _Pragma("unroll") for (int k = 0; k < 2; ++k) dst[m][k] = *(const PG8_LAS bf16x8*)(lds + PG8_SA(b, h) + aoff + m * 2048 + k * 1024); } while (0)
; #define PG8_LDB(dst, b, h) do { _Pragma("unroll") for (int n = 0; n < 2; ++n) _Pragma("unroll") for (int k = 0; k < 2; ++k) dst[n][k] = *(const PG8_LAS bf16x8*)(lds + PG8_SB(b, h) + boff + n * 2048 + k * 1024); } while (0)
; #define PG8_MMA(ai, bj, At, Bt) do { __builtin_amdgcn_s_setprio(1); _Pragma("unroll") for (int m = 0; m < 4; ++m) _Pragma("unroll") for (int n = 0; n < 2; ++n) _Pragma("unroll") for (int k = 0; k < 2; ++k) \
;         acc[ai][bj][m][n] = __builtin_amdgcn_mfma_f32_16x16x32_bf16(Bt[n][k], At[m][k], acc[ai][bj][m][n], 0, 0, 0); __builtin_amdgcn_s_setprio(0); } while (0)
; #define PG8_WAIT_V(n) asm volatile("s_waitcnt vmcnt(" #n ")" ::: "memory")
; #define PG8_WAIT_L(n) asm volatile("s_waitcnt lgkmcnt(" #n ")" ::: "memory")
; #define PG8_BAR __builtin_amdgcn_s_barrier()
; #define PG8_SCHED __builtin_amdgcn_sched_barrier(0)
; template <class Epi, class Sched, bool ALIGN_EPI = false, bool SP2 = false>
; __device__ __forceinline__ void gemm_phase(PG8_LAS unsigned char* lds, const Gemm g, const Sched& S, const Epi& E) {
;     ...
;             PG8_LDA(At, 0, 1); PG8_STAGE(PG8_SB(0, 0), b2, voffB); PG8_STAGE(PG8_SB(0, 1), b2 + hstepB, voffB); PG8_STAGE(PG8_SA(0, 0), a2, voffA);
;             PG8_WAIT_V(8); PG8_WAIT_L(0); PG8_BAR; PG8_MMA(1, 0, At, B0); PG8_MMA(1, 1, At, B1); PG8_BAR; PG8_SCHED;
;             PG8_LDB(B0, 1, 0); PG8_LDB(B1, 1, 1); PG8_SCHED; PG8_LDA(At, 1, 0); PG8_STAGE(PG8_SA(0, 1), a2 + hstepA, voffA);
;             PG8_WAIT_V(8); PG8_WAIT_L(0); PG8_BAR; PG8_MMA(0, 0, At, B0); PG8_MMA(0, 1, At, B1); PG8_BAR; PG8_SCHED;
	s_setprio 1
	s_waitcnt lgkmcnt(0)
	v_mfma_f32_16x16x32_bf16 v[64:67], v[150:153], v[182:185], v[64:67]
	v_mfma_f32_16x16x32_bf16 v[60:63], v[158:161], v[182:185], v[60:63]
	v_mfma_f32_16x16x32_bf16 v[56:59], v[150:153], v[190:193], v[56:59]
	v_mfma_f32_16x16x32_bf16 v[48:51], v[158:161], v[190:193], v[48:51]
	v_mfma_f32_16x16x32_bf16 v[40:43], v[150:153], v[210:213], v[40:43]
	v_mfma_f32_16x16x32_bf16 v[32:35], v[158:161], v[210:213], v[32:35]
	v_mfma_f32_16x16x32_bf16 v[24:27], v[150:153], v[230:233], v[24:27]
	v_mfma_f32_16x16x32_bf16 v[16:19], v[158:161], v[230:233], v[16:19]
	v_mfma_f32_16x16x32_bf16 v[64:67], v[154:157], v[186:189], v[64:67]
	v_mfma_f32_16x16x32_bf16 v[60:63], v[162:165], v[186:189], v[60:63]
	v_mfma_f32_16x16x32_bf16 v[56:59], v[154:157], v[194:197], v[56:59]
	v_mfma_f32_16x16x32_bf16 v[48:51], v[162:165], v[194:197], v[48:51]
	v_mfma_f32_16x16x32_bf16 v[40:43], v[154:157], v[226:229], v[40:43]
	v_mfma_f32_16x16x32_bf16 v[32:35], v[162:165], v[226:229], v[32:35]
	v_mfma_f32_16x16x32_bf16 v[24:27], v[154:157], v[234:237], v[24:27]
	v_mfma_f32_16x16x32_bf16 v[16:19], v[162:165], v[234:237], v[16:19]
	s_setprio 0
	s_setprio 1
	v_mfma_f32_16x16x32_bf16 v[52:55], v[166:169], v[182:185], v[52:55]
	v_mfma_f32_16x16x32_bf16 v[44:47], v[174:177], v[182:185], v[44:47]
	v_mfma_f32_16x16x32_bf16 v[36:39], v[166:169], v[190:193], v[36:39]
	v_mfma_f32_16x16x32_bf16 v[28:31], v[174:177], v[190:193], v[28:31]
	v_mfma_f32_16x16x32_bf16 v[20:23], v[166:169], v[210:213], v[20:23]
	v_mfma_f32_16x16x32_bf16 v[12:15], v[174:177], v[210:213], v[12:15]
	v_mfma_f32_16x16x32_bf16 v[8:11], v[166:169], v[230:233], v[8:11]
	v_mfma_f32_16x16x32_bf16 v[4:7], v[174:177], v[230:233], v[4:7]
	v_mfma_f32_16x16x32_bf16 v[52:55], v[170:173], v[186:189], v[52:55]
	v_mfma_f32_16x16x32_bf16 v[44:47], v[178:181], v[186:189], v[44:47]
	v_mfma_f32_16x16x32_bf16 v[36:39], v[170:173], v[194:197], v[36:39]
	v_mfma_f32_16x16x32_bf16 v[28:31], v[178:181], v[194:197], v[28:31]
	v_mfma_f32_16x16x32_bf16 v[20:23], v[170:173], v[226:229], v[20:23]
	v_mfma_f32_16x16x32_bf16 v[12:15], v[178:181], v[226:229], v[12:15]
	v_mfma_f32_16x16x32_bf16 v[8:11], v[170:173], v[234:237], v[8:11]
	v_mfma_f32_16x16x32_bf16 v[4:7], v[178:181], v[234:237], v[4:7]
	s_setprio 0
	s_barrier
	s_add_i32 s46, 0, 0x18000
	v_add_u32_e32 v149, s46, v146
	s_add_i32 s47, 0, 0x1c000
	ds_read_b128 v[150:153], v149
	ds_read_b128 v[154:157], v149 offset:1024
	ds_read_b128 v[158:161], v149 offset:2048
	ds_read_b128 v[162:165], v149 offset:3072
	v_add_u32_e32 v149, s47, v146
	ds_read_b128 v[166:169], v149
	ds_read_b128 v[170:173], v149 offset:1024
	ds_read_b128 v[174:177], v149 offset:2048
	ds_read_b128 v[178:181], v149 offset:3072
	s_add_u32 s24, s24, 0x40000
	s_addc_u32 s25, s25, 0
	s_mov_b32 m0, s34
	v_lshl_add_u64 v[244:245], s[24:25], 0, v[132:133]
	ds_read_b128 v[182:185], v148 offset:32768
	ds_read_b128 v[186:189], v148 offset:33792
	ds_read_b128 v[190:193], v148 offset:34816
	ds_read_b128 v[194:197], v148 offset:35840
	ds_read_b128 v[210:213], v148 offset:36864
	ds_read_b128 v[226:229], v148 offset:37888
	ds_read_b128 v[230:233], v148 offset:38912
	ds_read_b128 v[234:237], v148 offset:39936
	s_mov_b32 m0, s15
	s_nop 0
	global_load_lds_dwordx4 v[240:241], off
	s_mov_b32 m0, s33
	s_nop 0
	global_load_lds_dwordx4 v[242:243], off
	s_mov_b32 m0, s34
	s_nop 0
	global_load_lds_dwordx4 v[244:245], off
	v_lshl_add_u64 v[244:245], s[24:25], 0, v[136:137]
	s_mov_b32 m0, s35
	s_nop 0
	global_load_lds_dwordx4 v[244:245], off
	s_waitcnt vmcnt(8)
	s_waitcnt lgkmcnt(0)
	s_barrier
; #define PG8_STAGE(bufoff, gbase, voff) do { _Pragma("unroll") for (int _i = 0; _i < 2; ++_i) \
;         __builtin_amdgcn_global_load_lds((const unsigned*)((const char*)(gbase) + (voff)[_i]), (PG8_LAS unsigned*)(lds + (bufoff) + ldsw + _i * 8192), 16, 0, 0); } while (0)
; #define PG8_LDA(dst, b, h) do { _Pragma("unroll") for (int m = 0; m < 4; ++m) _Pragma("unroll") for (int k = 0; k < 2; ++k) dst[m][k] = *(const PG8_LAS bf16x8*)(lds + PG8_SA(b, h) + aoff + m * 2048 + k * 1024); } while (0)
; #define PG8_MMA(ai, bj, At, Bt) do { __builtin_amdgcn_s_setprio(1); _Pragma("unroll") for (int m = 0; m < 4; ++m) _Pragma("unroll") for (int n = 0; n < 2; ++n) _Pragma("unroll") for (int k = 0; k < 2; ++k) \
;         acc[ai][bj][m][n] = __builtin_amdgcn_mfma_f32_16x16x32_bf16(Bt[n][k], At[m][k], acc[ai][bj][m][n], 0, 0, 0); __builtin_amdgcn_s_setprio(0); } while (0)
; #define PG8_WAIT_V(n) asm volatile("s_waitcnt vmcnt(" #n ")" ::: "memory")
; #define PG8_WAIT_L(n) asm volatile("s_waitcnt lgkmcnt(" #n ")" ::: "memory")
; #define PG8_BAR __builtin_amdgcn_s_barrier()
; #define PG8_SCHED __builtin_amdgcn_sched_barrier(0)
; template <class Epi, class Sched, bool ALIGN_EPI = false, bool SP2 = false>
; __device__ __forceinline__ void gemm_phase(PG8_LAS unsigned char* lds, const Gemm g, const Sched& S, const Epi& E) {
;     ...
;             PG8_WAIT_V(8); PG8_WAIT_L(0); PG8_BAR; PG8_MMA(0, 0, At, B0); PG8_MMA(0, 1, At, B1); PG8_BAR; PG8_SCHED;
;             PG8_LDA(At, 1, 1); PG8_STAGE(PG8_SB(1, 0), b3, voffB); PG8_STAGE(PG8_SB(1, 1), b3 + hstepB, voffB); PG8_STAGE(PG8_SA(1, 0), a3, voffA);
;             PG8_WAIT_V(8); PG8_WAIT_L(0); PG8_BAR; PG8_MMA(1, 0, At, B0); PG8_MMA(1, 1, At, B1); PG8_BAR; PG8_SCHED;
;     ...
;         if constexpr (ALIGN_EPI) { if (wr == 0) PG8_BAR; }
	s_setprio 1
	s_waitcnt lgkmcnt(0)
	v_mfma_f32_16x16x32_bf16 v[128:131], v[150:153], v[182:185], v[128:131]
	v_mfma_f32_16x16x32_bf16 v[124:127], v[158:161], v[182:185], v[124:127]
	v_mfma_f32_16x16x32_bf16 v[120:123], v[150:153], v[190:193], v[120:123]
	v_mfma_f32_16x16x32_bf16 v[112:115], v[158:161], v[190:193], v[112:115]
	v_mfma_f32_16x16x32_bf16 v[104:107], v[150:153], v[210:213], v[104:107]
	v_mfma_f32_16x16x32_bf16 v[96:99], v[158:161], v[210:213], v[96:99]
	v_mfma_f32_16x16x32_bf16 v[88:91], v[150:153], v[230:233], v[88:91]
	v_mfma_f32_16x16x32_bf16 v[80:83], v[158:161], v[230:233], v[80:83]
	v_mfma_f32_16x16x32_bf16 v[128:131], v[154:157], v[186:189], v[128:131]
	v_mfma_f32_16x16x32_bf16 v[124:127], v[162:165], v[186:189], v[124:127]
	v_mfma_f32_16x16x32_bf16 v[120:123], v[154:157], v[194:197], v[120:123]
	v_mfma_f32_16x16x32_bf16 v[112:115], v[162:165], v[194:197], v[112:115]
	v_mfma_f32_16x16x32_bf16 v[104:107], v[154:157], v[226:229], v[104:107]
	v_mfma_f32_16x16x32_bf16 v[96:99], v[162:165], v[226:229], v[96:99]
	v_mfma_f32_16x16x32_bf16 v[88:91], v[154:157], v[234:237], v[88:91]
	v_mfma_f32_16x16x32_bf16 v[80:83], v[162:165], v[234:237], v[80:83]
	s_setprio 0
	s_setprio 1
	v_mfma_f32_16x16x32_bf16 v[116:119], v[166:169], v[182:185], v[116:119]
	v_mfma_f32_16x16x32_bf16 v[108:111], v[174:177], v[182:185], v[108:111]
	v_mfma_f32_16x16x32_bf16 v[100:103], v[166:169], v[190:193], v[100:103]
	v_mfma_f32_16x16x32_bf16 v[92:95], v[174:177], v[190:193], v[92:95]
	v_mfma_f32_16x16x32_bf16 v[84:87], v[166:169], v[210:213], v[84:87]
	v_mfma_f32_16x16x32_bf16 v[76:79], v[174:177], v[210:213], v[76:79]
	v_mfma_f32_16x16x32_bf16 v[72:75], v[166:169], v[230:233], v[72:75]
	v_mfma_f32_16x16x32_bf16 v[68:71], v[174:177], v[230:233], v[68:71]
	v_mfma_f32_16x16x32_bf16 v[116:119], v[170:173], v[186:189], v[116:119]
	v_mfma_f32_16x16x32_bf16 v[108:111], v[178:181], v[186:189], v[108:111]
	v_mfma_f32_16x16x32_bf16 v[100:103], v[170:173], v[194:197], v[100:103]
	v_mfma_f32_16x16x32_bf16 v[92:95], v[178:181], v[194:197], v[92:95]
	v_mfma_f32_16x16x32_bf16 v[84:87], v[170:173], v[226:229], v[84:87]
	v_mfma_f32_16x16x32_bf16 v[76:79], v[178:181], v[226:229], v[76:79]
	v_mfma_f32_16x16x32_bf16 v[72:75], v[170:173], v[234:237], v[72:75]
	v_mfma_f32_16x16x32_bf16 v[68:71], v[178:181], v[234:237], v[68:71]
	s_setprio 0
	s_barrier
	s_add_i32 s24, s46, s31
	v_lshl_add_u64 v[144:145], v[144:145], 0, s[64:65]
	s_mov_b32 m0, s24
	ds_read_b128 v[182:185], v148 offset:49152
	ds_read_b128 v[186:189], v148 offset:50176
	ds_read_b128 v[190:193], v148 offset:51200
	ds_read_b128 v[194:197], v148 offset:52224
	ds_read_b128 v[210:213], v148 offset:53248
	ds_read_b128 v[226:229], v148 offset:54272
	ds_read_b128 v[230:233], v148 offset:55296
	ds_read_b128 v[234:237], v148 offset:56320
	global_load_lds_dwordx4 v[144:145], off
	s_add_i32 m0, s24, 0x2000
	s_add_u32 s22, s22, 0x40080
	v_lshl_add_u64 v[144:145], v[238:239], 0, s[64:65]
	s_addc_u32 s23, s23, 0
	s_add_i32 s24, s47, s31
	global_load_lds_dwordx4 v[144:145], off
	v_lshl_add_u64 v[144:145], s[22:23], 0, v[134:135]
	s_mov_b32 m0, s24
	s_nop 0
	global_load_lds_dwordx4 v[144:145], off
	v_lshl_add_u64 v[144:145], s[22:23], 0, v[138:139]
	s_add_i32 m0, s24, 0x2000
	s_nop 0
	global_load_lds_dwordx4 v[144:145], off
	s_waitcnt vmcnt(6)
	s_waitcnt lgkmcnt(0)
	s_barrier
	s_setprio 1
	s_waitcnt lgkmcnt(0)
	v_mfma_f32_16x16x32_bf16 v[64:67], v[150:153], v[182:185], v[64:67]
	v_mfma_f32_16x16x32_bf16 v[60:63], v[158:161], v[182:185], v[60:63]
	v_mfma_f32_16x16x32_bf16 v[56:59], v[150:153], v[190:193], v[56:59]
	v_mfma_f32_16x16x32_bf16 v[48:51], v[158:161], v[190:193], v[48:51]
	v_mfma_f32_16x16x32_bf16 v[40:43], v[150:153], v[210:213], v[40:43]
	v_mfma_f32_16x16x32_bf16 v[32:35], v[158:161], v[210:213], v[32:35]
	v_mfma_f32_16x16x32_bf16 v[24:27], v[150:153], v[230:233], v[24:27]
	v_mfma_f32_16x16x32_bf16 v[16:19], v[158:161], v[230:233], v[16:19]
	v_mfma_f32_16x16x32_bf16 v[64:67], v[154:157], v[186:189], v[64:67]
	v_mfma_f32_16x16x32_bf16 v[60:63], v[162:165], v[186:189], v[60:63]
	v_mfma_f32_16x16x32_bf16 v[56:59], v[154:157], v[194:197], v[56:59]
	v_mfma_f32_16x16x32_bf16 v[48:51], v[162:165], v[194:197], v[48:51]
	v_mfma_f32_16x16x32_bf16 v[40:43], v[154:157], v[226:229], v[40:43]
	v_mfma_f32_16x16x32_bf16 v[32:35], v[162:165], v[226:229], v[32:35]
	v_mfma_f32_16x16x32_bf16 v[24:27], v[154:157], v[234:237], v[24:27]
	v_mfma_f32_16x16x32_bf16 v[16:19], v[162:165], v[234:237], v[16:19]
	s_setprio 0
	s_setprio 1
	v_mfma_f32_16x16x32_bf16 v[52:55], v[166:169], v[182:185], v[52:55]
	v_mfma_f32_16x16x32_bf16 v[44:47], v[174:177], v[182:185], v[44:47]
	v_mfma_f32_16x16x32_bf16 v[36:39], v[166:169], v[190:193], v[36:39]
	v_mfma_f32_16x16x32_bf16 v[28:31], v[174:177], v[190:193], v[28:31]
	v_mfma_f32_16x16x32_bf16 v[20:23], v[166:169], v[210:213], v[20:23]
	v_mfma_f32_16x16x32_bf16 v[12:15], v[174:177], v[210:213], v[12:15]
	v_mfma_f32_16x16x32_bf16 v[8:11], v[166:169], v[230:233], v[8:11]
	v_mfma_f32_16x16x32_bf16 v[4:7], v[174:177], v[230:233], v[4:7]
	v_mfma_f32_16x16x32_bf16 v[52:55], v[170:173], v[186:189], v[52:55]
	v_mfma_f32_16x16x32_bf16 v[44:47], v[178:181], v[186:189], v[44:47]
	v_mfma_f32_16x16x32_bf16 v[36:39], v[170:173], v[194:197], v[36:39]
	v_mfma_f32_16x16x32_bf16 v[28:31], v[178:181], v[194:197], v[28:31]
	v_mfma_f32_16x16x32_bf16 v[20:23], v[170:173], v[226:229], v[20:23]
	v_mfma_f32_16x16x32_bf16 v[12:15], v[178:181], v[226:229], v[12:15]
	v_mfma_f32_16x16x32_bf16 v[8:11], v[170:173], v[234:237], v[8:11]
	v_mfma_f32_16x16x32_bf16 v[4:7], v[178:181], v[234:237], v[4:7]
	s_setprio 0
	s_barrier
	s_add_i32 s45, s45, 2
	s_add_u32 s43, s43, 0x100
	s_addc_u32 s44, s44, 0
	s_add_u32 s20, s20, 0x100
	s_addc_u32 s21, s21, 0
	s_cmp_gt_u32 s45, 13
	s_cbranch_scc0 .LBB0_1693
	s_and_b64 vcc, exec, s[8:9]
	s_cbranch_vccz .LBB0_1696
	s_barrier
